# full 8-row batches: per-pair early-exit tests removed from the U dot and V axpy (every batch is full now)
# speedup vs baseline: 1.0088x; 1.0004x over previous
.Lp6a0_956:
	s_bfe_u32 s36, s26, 0x4000a
	v_cvt_pk_f32_fp8_e32 v[184:185], v68
	v_cvt_pk_f32_fp8_e32 v[192:193], v64
	v_cvt_pk_f32_fp8_sdwa v[186:187], v68 src0_sel:WORD_1
	v_cvt_pk_f32_fp8_sdwa v[194:195], v64 src0_sel:WORD_1
	v_pk_mul_f32 v[188:189], v[184:185], v[144:145]
	v_pk_mul_f32 v[222:223], v[192:193], v[144:145]
	v_pk_mul_f32 v[190:191], v[186:187], v[146:147]
	v_pk_mul_f32 v[176:177], v[194:195], v[146:147]
	v_cvt_pk_f32_fp8_e32 v[184:185], v69
	v_cvt_pk_f32_fp8_e32 v[192:193], v65
	v_cvt_pk_f32_fp8_sdwa v[186:187], v69 src0_sel:WORD_1
	v_cvt_pk_f32_fp8_sdwa v[194:195], v65 src0_sel:WORD_1
	v_pk_fma_f32 v[188:189], v[184:185], v[148:149], v[188:189]
	v_pk_fma_f32 v[222:223], v[192:193], v[148:149], v[222:223]
	v_pk_fma_f32 v[190:191], v[186:187], v[150:151], v[190:191]
	v_pk_fma_f32 v[176:177], v[194:195], v[150:151], v[176:177]
	v_cvt_pk_f32_fp8_e32 v[184:185], v70
	v_cvt_pk_f32_fp8_e32 v[192:193], v66
	v_cvt_pk_f32_fp8_sdwa v[186:187], v70 src0_sel:WORD_1
	v_cvt_pk_f32_fp8_sdwa v[194:195], v66 src0_sel:WORD_1
	v_pk_fma_f32 v[188:189], v[184:185], v[152:153], v[188:189]
	v_pk_fma_f32 v[222:223], v[192:193], v[152:153], v[222:223]
	v_pk_fma_f32 v[190:191], v[186:187], v[154:155], v[190:191]
	v_pk_fma_f32 v[176:177], v[194:195], v[154:155], v[176:177]
	v_cvt_pk_f32_fp8_e32 v[184:185], v71
	v_cvt_pk_f32_fp8_e32 v[192:193], v67
	v_cvt_pk_f32_fp8_sdwa v[186:187], v71 src0_sel:WORD_1
	v_cvt_pk_f32_fp8_sdwa v[194:195], v67 src0_sel:WORD_1
	v_pk_fma_f32 v[188:189], v[184:185], v[156:157], v[188:189]
	v_pk_fma_f32 v[222:223], v[192:193], v[156:157], v[222:223]
	v_pk_fma_f32 v[190:191], v[186:187], v[158:159], v[190:191]
	v_pk_fma_f32 v[176:177], v[194:195], v[158:159], v[176:177]
	v_pk_add_f32 v[188:189], v[188:189], v[190:191]
	v_pk_add_f32 v[222:223], v[222:223], v[176:177]
	v_add_f32_e32 v160, v188, v189
	v_add_f32_e32 v162, v222, v223
	v_cvt_pk_f32_fp8_e32 v[184:185], v60
	v_cvt_pk_f32_fp8_e32 v[192:193], v56
	v_cvt_pk_f32_fp8_sdwa v[186:187], v60 src0_sel:WORD_1
	v_cvt_pk_f32_fp8_sdwa v[194:195], v56 src0_sel:WORD_1
	v_pk_mul_f32 v[188:189], v[184:185], v[144:145]
	v_pk_mul_f32 v[222:223], v[192:193], v[144:145]
	v_pk_mul_f32 v[190:191], v[186:187], v[146:147]
	v_pk_mul_f32 v[176:177], v[194:195], v[146:147]
	v_cvt_pk_f32_fp8_e32 v[184:185], v61
	v_cvt_pk_f32_fp8_e32 v[192:193], v57
	v_cvt_pk_f32_fp8_sdwa v[186:187], v61 src0_sel:WORD_1
	v_cvt_pk_f32_fp8_sdwa v[194:195], v57 src0_sel:WORD_1
	v_pk_fma_f32 v[188:189], v[184:185], v[148:149], v[188:189]
	v_pk_fma_f32 v[222:223], v[192:193], v[148:149], v[222:223]
	v_pk_fma_f32 v[190:191], v[186:187], v[150:151], v[190:191]
	v_pk_fma_f32 v[176:177], v[194:195], v[150:151], v[176:177]
	v_cvt_pk_f32_fp8_e32 v[184:185], v62
	v_cvt_pk_f32_fp8_e32 v[192:193], v58
	v_cvt_pk_f32_fp8_sdwa v[186:187], v62 src0_sel:WORD_1
	v_cvt_pk_f32_fp8_sdwa v[194:195], v58 src0_sel:WORD_1
	v_pk_fma_f32 v[188:189], v[184:185], v[152:153], v[188:189]
	v_pk_fma_f32 v[222:223], v[192:193], v[152:153], v[222:223]
	v_pk_fma_f32 v[190:191], v[186:187], v[154:155], v[190:191]
	v_pk_fma_f32 v[176:177], v[194:195], v[154:155], v[176:177]
	v_cvt_pk_f32_fp8_e32 v[184:185], v63
	v_cvt_pk_f32_fp8_e32 v[192:193], v59
	v_cvt_pk_f32_fp8_sdwa v[186:187], v63 src0_sel:WORD_1
	v_cvt_pk_f32_fp8_sdwa v[194:195], v59 src0_sel:WORD_1
	v_pk_fma_f32 v[188:189], v[184:185], v[156:157], v[188:189]
	v_pk_fma_f32 v[222:223], v[192:193], v[156:157], v[222:223]
	v_pk_fma_f32 v[190:191], v[186:187], v[158:159], v[190:191]
	v_pk_fma_f32 v[176:177], v[194:195], v[158:159], v[176:177]
	v_pk_add_f32 v[188:189], v[188:189], v[190:191]
	v_pk_add_f32 v[222:223], v[222:223], v[176:177]
	v_add_f32_e32 v164, v188, v189
	v_add_f32_e32 v166, v222, v223
	v_cvt_pk_f32_fp8_e32 v[184:185], v48
	v_cvt_pk_f32_fp8_e32 v[192:193], v32
	v_cvt_pk_f32_fp8_sdwa v[186:187], v48 src0_sel:WORD_1
	v_cvt_pk_f32_fp8_sdwa v[194:195], v32 src0_sel:WORD_1
	v_pk_mul_f32 v[188:189], v[184:185], v[144:145]
	v_pk_mul_f32 v[222:223], v[192:193], v[144:145]
	v_pk_mul_f32 v[190:191], v[186:187], v[146:147]
	v_pk_mul_f32 v[176:177], v[194:195], v[146:147]
	v_cvt_pk_f32_fp8_e32 v[184:185], v49
	v_cvt_pk_f32_fp8_e32 v[192:193], v33
	v_cvt_pk_f32_fp8_sdwa v[186:187], v49 src0_sel:WORD_1
	v_cvt_pk_f32_fp8_sdwa v[194:195], v33 src0_sel:WORD_1
	v_pk_fma_f32 v[188:189], v[184:185], v[148:149], v[188:189]
	v_pk_fma_f32 v[222:223], v[192:193], v[148:149], v[222:223]
	v_pk_fma_f32 v[190:191], v[186:187], v[150:151], v[190:191]
	v_pk_fma_f32 v[176:177], v[194:195], v[150:151], v[176:177]
	v_cvt_pk_f32_fp8_e32 v[184:185], v50
	v_cvt_pk_f32_fp8_e32 v[192:193], v34
	v_cvt_pk_f32_fp8_sdwa v[186:187], v50 src0_sel:WORD_1
	v_cvt_pk_f32_fp8_sdwa v[194:195], v34 src0_sel:WORD_1
	v_pk_fma_f32 v[188:189], v[184:185], v[152:153], v[188:189]
	v_pk_fma_f32 v[222:223], v[192:193], v[152:153], v[222:223]
	v_pk_fma_f32 v[190:191], v[186:187], v[154:155], v[190:191]
	v_pk_fma_f32 v[176:177], v[194:195], v[154:155], v[176:177]
	v_cvt_pk_f32_fp8_e32 v[184:185], v51
	v_cvt_pk_f32_fp8_e32 v[192:193], v35
	v_cvt_pk_f32_fp8_sdwa v[186:187], v51 src0_sel:WORD_1
	v_cvt_pk_f32_fp8_sdwa v[194:195], v35 src0_sel:WORD_1
	v_pk_fma_f32 v[188:189], v[184:185], v[156:157], v[188:189]
	v_pk_fma_f32 v[222:223], v[192:193], v[156:157], v[222:223]
	v_pk_fma_f32 v[190:191], v[186:187], v[158:159], v[190:191]
	v_pk_fma_f32 v[176:177], v[194:195], v[158:159], v[176:177]
	v_pk_add_f32 v[188:189], v[188:189], v[190:191]
	v_pk_add_f32 v[222:223], v[222:223], v[176:177]
	v_add_f32_e32 v168, v188, v189
	v_add_f32_e32 v170, v222, v223
	v_cvt_pk_f32_fp8_e32 v[184:185], v16
	v_cvt_pk_f32_fp8_e32 v[192:193], v12
	v_cvt_pk_f32_fp8_sdwa v[186:187], v16 src0_sel:WORD_1
	v_cvt_pk_f32_fp8_sdwa v[194:195], v12 src0_sel:WORD_1
	v_pk_mul_f32 v[188:189], v[184:185], v[144:145]
	v_pk_mul_f32 v[222:223], v[192:193], v[144:145]
	v_pk_mul_f32 v[190:191], v[186:187], v[146:147]
	v_pk_mul_f32 v[176:177], v[194:195], v[146:147]
	v_cvt_pk_f32_fp8_e32 v[184:185], v17
	v_cvt_pk_f32_fp8_e32 v[192:193], v13
	v_cvt_pk_f32_fp8_sdwa v[186:187], v17 src0_sel:WORD_1
	v_cvt_pk_f32_fp8_sdwa v[194:195], v13 src0_sel:WORD_1
	v_pk_fma_f32 v[188:189], v[184:185], v[148:149], v[188:189]
	v_pk_fma_f32 v[222:223], v[192:193], v[148:149], v[222:223]
	v_pk_fma_f32 v[190:191], v[186:187], v[150:151], v[190:191]
	v_pk_fma_f32 v[176:177], v[194:195], v[150:151], v[176:177]
	v_cvt_pk_f32_fp8_e32 v[184:185], v18
	v_cvt_pk_f32_fp8_e32 v[192:193], v14
	v_cvt_pk_f32_fp8_sdwa v[186:187], v18 src0_sel:WORD_1
	v_cvt_pk_f32_fp8_sdwa v[194:195], v14 src0_sel:WORD_1
	v_pk_fma_f32 v[188:189], v[184:185], v[152:153], v[188:189]
	v_pk_fma_f32 v[222:223], v[192:193], v[152:153], v[222:223]
	v_pk_fma_f32 v[190:191], v[186:187], v[154:155], v[190:191]
	v_pk_fma_f32 v[176:177], v[194:195], v[154:155], v[176:177]
	v_cvt_pk_f32_fp8_e32 v[184:185], v19
	v_cvt_pk_f32_fp8_e32 v[192:193], v15
	v_cvt_pk_f32_fp8_sdwa v[186:187], v19 src0_sel:WORD_1
	v_cvt_pk_f32_fp8_sdwa v[194:195], v15 src0_sel:WORD_1
	v_pk_fma_f32 v[188:189], v[184:185], v[156:157], v[188:189]
	v_pk_fma_f32 v[222:223], v[192:193], v[156:157], v[222:223]
	v_pk_fma_f32 v[190:191], v[186:187], v[158:159], v[190:191]
	v_pk_fma_f32 v[176:177], v[194:195], v[158:159], v[176:177]
	v_pk_add_f32 v[188:189], v[188:189], v[190:191]
	v_pk_add_f32 v[222:223], v[222:223], v[176:177]
	v_add_f32_e32 v172, v188, v189
	v_add_f32_e32 v174, v222, v223

.Lp6a1_956:
	s_bfe_u32 s36, s26, 0x4000a
	v_cvt_pk_f32_fp8_e32 v[184:185], v72
	v_cvt_pk_f32_fp8_e32 v[192:193], v52
	v_cvt_pk_f32_fp8_sdwa v[186:187], v72 src0_sel:WORD_1
	v_cvt_pk_f32_fp8_sdwa v[194:195], v52 src0_sel:WORD_1
	v_pk_mul_f32 v[188:189], v[184:185], v[144:145]
	v_pk_mul_f32 v[222:223], v[192:193], v[144:145]
	v_pk_mul_f32 v[190:191], v[186:187], v[146:147]
	v_pk_mul_f32 v[176:177], v[194:195], v[146:147]
	v_cvt_pk_f32_fp8_e32 v[184:185], v73
	v_cvt_pk_f32_fp8_e32 v[192:193], v53
	v_cvt_pk_f32_fp8_sdwa v[186:187], v73 src0_sel:WORD_1
	v_cvt_pk_f32_fp8_sdwa v[194:195], v53 src0_sel:WORD_1
	v_pk_fma_f32 v[188:189], v[184:185], v[148:149], v[188:189]
	v_pk_fma_f32 v[222:223], v[192:193], v[148:149], v[222:223]
	v_pk_fma_f32 v[190:191], v[186:187], v[150:151], v[190:191]
	v_pk_fma_f32 v[176:177], v[194:195], v[150:151], v[176:177]
	v_cvt_pk_f32_fp8_e32 v[184:185], v74
	v_cvt_pk_f32_fp8_e32 v[192:193], v54
	v_cvt_pk_f32_fp8_sdwa v[186:187], v74 src0_sel:WORD_1
	v_cvt_pk_f32_fp8_sdwa v[194:195], v54 src0_sel:WORD_1
	v_pk_fma_f32 v[188:189], v[184:185], v[152:153], v[188:189]
	v_pk_fma_f32 v[222:223], v[192:193], v[152:153], v[222:223]
	v_pk_fma_f32 v[190:191], v[186:187], v[154:155], v[190:191]
	v_pk_fma_f32 v[176:177], v[194:195], v[154:155], v[176:177]
	v_cvt_pk_f32_fp8_e32 v[184:185], v75
	v_cvt_pk_f32_fp8_e32 v[192:193], v55
	v_cvt_pk_f32_fp8_sdwa v[186:187], v75 src0_sel:WORD_1
	v_cvt_pk_f32_fp8_sdwa v[194:195], v55 src0_sel:WORD_1
	v_pk_fma_f32 v[188:189], v[184:185], v[156:157], v[188:189]
	v_pk_fma_f32 v[222:223], v[192:193], v[156:157], v[222:223]
	v_pk_fma_f32 v[190:191], v[186:187], v[158:159], v[190:191]
	v_pk_fma_f32 v[176:177], v[194:195], v[158:159], v[176:177]
	v_pk_add_f32 v[188:189], v[188:189], v[190:191]
	v_pk_add_f32 v[222:223], v[222:223], v[176:177]
	v_add_f32_e32 v160, v188, v189
	v_add_f32_e32 v162, v222, v223
	v_cvt_pk_f32_fp8_e32 v[184:185], v44
	v_cvt_pk_f32_fp8_e32 v[192:193], v40
	v_cvt_pk_f32_fp8_sdwa v[186:187], v44 src0_sel:WORD_1
	v_cvt_pk_f32_fp8_sdwa v[194:195], v40 src0_sel:WORD_1
	v_pk_mul_f32 v[188:189], v[184:185], v[144:145]
	v_pk_mul_f32 v[222:223], v[192:193], v[144:145]
	v_pk_mul_f32 v[190:191], v[186:187], v[146:147]
	v_pk_mul_f32 v[176:177], v[194:195], v[146:147]
	v_cvt_pk_f32_fp8_e32 v[184:185], v45
	v_cvt_pk_f32_fp8_e32 v[192:193], v41
	v_cvt_pk_f32_fp8_sdwa v[186:187], v45 src0_sel:WORD_1
	v_cvt_pk_f32_fp8_sdwa v[194:195], v41 src0_sel:WORD_1
	v_pk_fma_f32 v[188:189], v[184:185], v[148:149], v[188:189]
	v_pk_fma_f32 v[222:223], v[192:193], v[148:149], v[222:223]
	v_pk_fma_f32 v[190:191], v[186:187], v[150:151], v[190:191]
	v_pk_fma_f32 v[176:177], v[194:195], v[150:151], v[176:177]
	v_cvt_pk_f32_fp8_e32 v[184:185], v46
	v_cvt_pk_f32_fp8_e32 v[192:193], v42
	v_cvt_pk_f32_fp8_sdwa v[186:187], v46 src0_sel:WORD_1
	v_cvt_pk_f32_fp8_sdwa v[194:195], v42 src0_sel:WORD_1
	v_pk_fma_f32 v[188:189], v[184:185], v[152:153], v[188:189]
	v_pk_fma_f32 v[222:223], v[192:193], v[152:153], v[222:223]
	v_pk_fma_f32 v[190:191], v[186:187], v[154:155], v[190:191]
	v_pk_fma_f32 v[176:177], v[194:195], v[154:155], v[176:177]
	v_cvt_pk_f32_fp8_e32 v[184:185], v47
	v_cvt_pk_f32_fp8_e32 v[192:193], v43
	v_cvt_pk_f32_fp8_sdwa v[186:187], v47 src0_sel:WORD_1
	v_cvt_pk_f32_fp8_sdwa v[194:195], v43 src0_sel:WORD_1
	v_pk_fma_f32 v[188:189], v[184:185], v[156:157], v[188:189]
	v_pk_fma_f32 v[222:223], v[192:193], v[156:157], v[222:223]
	v_pk_fma_f32 v[190:191], v[186:187], v[158:159], v[190:191]
	v_pk_fma_f32 v[176:177], v[194:195], v[158:159], v[176:177]
	v_pk_add_f32 v[188:189], v[188:189], v[190:191]
	v_pk_add_f32 v[222:223], v[222:223], v[176:177]
	v_add_f32_e32 v164, v188, v189
	v_add_f32_e32 v166, v222, v223
	v_cvt_pk_f32_fp8_e32 v[184:185], v36
	v_cvt_pk_f32_fp8_e32 v[192:193], v28
	v_cvt_pk_f32_fp8_sdwa v[186:187], v36 src0_sel:WORD_1
	v_cvt_pk_f32_fp8_sdwa v[194:195], v28 src0_sel:WORD_1
	v_pk_mul_f32 v[188:189], v[184:185], v[144:145]
	v_pk_mul_f32 v[222:223], v[192:193], v[144:145]
	v_pk_mul_f32 v[190:191], v[186:187], v[146:147]
	v_pk_mul_f32 v[176:177], v[194:195], v[146:147]
	v_cvt_pk_f32_fp8_e32 v[184:185], v37
	v_cvt_pk_f32_fp8_e32 v[192:193], v29
	v_cvt_pk_f32_fp8_sdwa v[186:187], v37 src0_sel:WORD_1
	v_cvt_pk_f32_fp8_sdwa v[194:195], v29 src0_sel:WORD_1
	v_pk_fma_f32 v[188:189], v[184:185], v[148:149], v[188:189]
	v_pk_fma_f32 v[222:223], v[192:193], v[148:149], v[222:223]
	v_pk_fma_f32 v[190:191], v[186:187], v[150:151], v[190:191]
	v_pk_fma_f32 v[176:177], v[194:195], v[150:151], v[176:177]
	v_cvt_pk_f32_fp8_e32 v[184:185], v38
	v_cvt_pk_f32_fp8_e32 v[192:193], v30
	v_cvt_pk_f32_fp8_sdwa v[186:187], v38 src0_sel:WORD_1
	v_cvt_pk_f32_fp8_sdwa v[194:195], v30 src0_sel:WORD_1
	v_pk_fma_f32 v[188:189], v[184:185], v[152:153], v[188:189]
	v_pk_fma_f32 v[222:223], v[192:193], v[152:153], v[222:223]
	v_pk_fma_f32 v[190:191], v[186:187], v[154:155], v[190:191]
	v_pk_fma_f32 v[176:177], v[194:195], v[154:155], v[176:177]
	v_cvt_pk_f32_fp8_e32 v[184:185], v39
	v_cvt_pk_f32_fp8_e32 v[192:193], v31
	v_cvt_pk_f32_fp8_sdwa v[186:187], v39 src0_sel:WORD_1
	v_cvt_pk_f32_fp8_sdwa v[194:195], v31 src0_sel:WORD_1
	v_pk_fma_f32 v[188:189], v[184:185], v[156:157], v[188:189]
	v_pk_fma_f32 v[222:223], v[192:193], v[156:157], v[222:223]
	v_pk_fma_f32 v[190:191], v[186:187], v[158:159], v[190:191]
	v_pk_fma_f32 v[176:177], v[194:195], v[158:159], v[176:177]
	v_pk_add_f32 v[188:189], v[188:189], v[190:191]
	v_pk_add_f32 v[222:223], v[222:223], v[176:177]
	v_add_f32_e32 v168, v188, v189
	v_add_f32_e32 v170, v222, v223
	v_cvt_pk_f32_fp8_e32 v[184:185], v24
	v_cvt_pk_f32_fp8_e32 v[192:193], v20
	v_cvt_pk_f32_fp8_sdwa v[186:187], v24 src0_sel:WORD_1
	v_cvt_pk_f32_fp8_sdwa v[194:195], v20 src0_sel:WORD_1
	v_pk_mul_f32 v[188:189], v[184:185], v[144:145]
	v_pk_mul_f32 v[222:223], v[192:193], v[144:145]
	v_pk_mul_f32 v[190:191], v[186:187], v[146:147]
	v_pk_mul_f32 v[176:177], v[194:195], v[146:147]
	v_cvt_pk_f32_fp8_e32 v[184:185], v25
	v_cvt_pk_f32_fp8_e32 v[192:193], v21
	v_cvt_pk_f32_fp8_sdwa v[186:187], v25 src0_sel:WORD_1
	v_cvt_pk_f32_fp8_sdwa v[194:195], v21 src0_sel:WORD_1
	v_pk_fma_f32 v[188:189], v[184:185], v[148:149], v[188:189]
	v_pk_fma_f32 v[222:223], v[192:193], v[148:149], v[222:223]
	v_pk_fma_f32 v[190:191], v[186:187], v[150:151], v[190:191]
	v_pk_fma_f32 v[176:177], v[194:195], v[150:151], v[176:177]
	v_cvt_pk_f32_fp8_e32 v[184:185], v26
	v_cvt_pk_f32_fp8_e32 v[192:193], v22
	v_cvt_pk_f32_fp8_sdwa v[186:187], v26 src0_sel:WORD_1
	v_cvt_pk_f32_fp8_sdwa v[194:195], v22 src0_sel:WORD_1
	v_pk_fma_f32 v[188:189], v[184:185], v[152:153], v[188:189]
	v_pk_fma_f32 v[222:223], v[192:193], v[152:153], v[222:223]
	v_pk_fma_f32 v[190:191], v[186:187], v[154:155], v[190:191]
	v_pk_fma_f32 v[176:177], v[194:195], v[154:155], v[176:177]
	v_cvt_pk_f32_fp8_e32 v[184:185], v27
	v_cvt_pk_f32_fp8_e32 v[192:193], v23
	v_cvt_pk_f32_fp8_sdwa v[186:187], v27 src0_sel:WORD_1
	v_cvt_pk_f32_fp8_sdwa v[194:195], v23 src0_sel:WORD_1
	v_pk_fma_f32 v[188:189], v[184:185], v[156:157], v[188:189]
	v_pk_fma_f32 v[222:223], v[192:193], v[156:157], v[222:223]
	v_pk_fma_f32 v[190:191], v[186:187], v[158:159], v[190:191]
	v_pk_fma_f32 v[176:177], v[194:195], v[158:159], v[176:177]
	v_pk_add_f32 v[188:189], v[188:189], v[190:191]
	v_pk_add_f32 v[222:223], v[222:223], v[176:177]
	v_add_f32_e32 v172, v188, v189
	v_add_f32_e32 v174, v222, v223

.Lp6a2_956:
	s_bfe_u32 s36, s26, 0x4000a
	v_cvt_pk_f32_fp8_e32 v[184:185], v224
	v_cvt_pk_f32_fp8_e32 v[192:193], v228
	v_cvt_pk_f32_fp8_sdwa v[186:187], v224 src0_sel:WORD_1
	v_cvt_pk_f32_fp8_sdwa v[194:195], v228 src0_sel:WORD_1
	v_pk_mul_f32 v[188:189], v[184:185], v[144:145]
	v_pk_mul_f32 v[222:223], v[192:193], v[144:145]
	v_pk_mul_f32 v[190:191], v[186:187], v[146:147]
	v_pk_mul_f32 v[176:177], v[194:195], v[146:147]
	v_cvt_pk_f32_fp8_e32 v[184:185], v225
	v_cvt_pk_f32_fp8_e32 v[192:193], v229
	v_cvt_pk_f32_fp8_sdwa v[186:187], v225 src0_sel:WORD_1
	v_cvt_pk_f32_fp8_sdwa v[194:195], v229 src0_sel:WORD_1
	v_pk_fma_f32 v[188:189], v[184:185], v[148:149], v[188:189]
	v_pk_fma_f32 v[222:223], v[192:193], v[148:149], v[222:223]
	v_pk_fma_f32 v[190:191], v[186:187], v[150:151], v[190:191]
	v_pk_fma_f32 v[176:177], v[194:195], v[150:151], v[176:177]
	v_cvt_pk_f32_fp8_e32 v[184:185], v226
	v_cvt_pk_f32_fp8_e32 v[192:193], v230
	v_cvt_pk_f32_fp8_sdwa v[186:187], v226 src0_sel:WORD_1
	v_cvt_pk_f32_fp8_sdwa v[194:195], v230 src0_sel:WORD_1
	v_pk_fma_f32 v[188:189], v[184:185], v[152:153], v[188:189]
	v_pk_fma_f32 v[222:223], v[192:193], v[152:153], v[222:223]
	v_pk_fma_f32 v[190:191], v[186:187], v[154:155], v[190:191]
	v_pk_fma_f32 v[176:177], v[194:195], v[154:155], v[176:177]
	v_cvt_pk_f32_fp8_e32 v[184:185], v227
	v_cvt_pk_f32_fp8_e32 v[192:193], v231
	v_cvt_pk_f32_fp8_sdwa v[186:187], v227 src0_sel:WORD_1
	v_cvt_pk_f32_fp8_sdwa v[194:195], v231 src0_sel:WORD_1
	v_pk_fma_f32 v[188:189], v[184:185], v[156:157], v[188:189]
	v_pk_fma_f32 v[222:223], v[192:193], v[156:157], v[222:223]
	v_pk_fma_f32 v[190:191], v[186:187], v[158:159], v[190:191]
	v_pk_fma_f32 v[176:177], v[194:195], v[158:159], v[176:177]
	v_pk_add_f32 v[188:189], v[188:189], v[190:191]
	v_pk_add_f32 v[222:223], v[222:223], v[176:177]
	v_add_f32_e32 v160, v188, v189
	v_add_f32_e32 v162, v222, v223
	v_cvt_pk_f32_fp8_e32 v[184:185], v232
	v_cvt_pk_f32_fp8_e32 v[192:193], v236
	v_cvt_pk_f32_fp8_sdwa v[186:187], v232 src0_sel:WORD_1
	v_cvt_pk_f32_fp8_sdwa v[194:195], v236 src0_sel:WORD_1
	v_pk_mul_f32 v[188:189], v[184:185], v[144:145]
	v_pk_mul_f32 v[222:223], v[192:193], v[144:145]
	v_pk_mul_f32 v[190:191], v[186:187], v[146:147]
	v_pk_mul_f32 v[176:177], v[194:195], v[146:147]
	v_cvt_pk_f32_fp8_e32 v[184:185], v233
	v_cvt_pk_f32_fp8_e32 v[192:193], v237
	v_cvt_pk_f32_fp8_sdwa v[186:187], v233 src0_sel:WORD_1
	v_cvt_pk_f32_fp8_sdwa v[194:195], v237 src0_sel:WORD_1
	v_pk_fma_f32 v[188:189], v[184:185], v[148:149], v[188:189]
	v_pk_fma_f32 v[222:223], v[192:193], v[148:149], v[222:223]
	v_pk_fma_f32 v[190:191], v[186:187], v[150:151], v[190:191]
	v_pk_fma_f32 v[176:177], v[194:195], v[150:151], v[176:177]
	v_cvt_pk_f32_fp8_e32 v[184:185], v234
	v_cvt_pk_f32_fp8_e32 v[192:193], v238
	v_cvt_pk_f32_fp8_sdwa v[186:187], v234 src0_sel:WORD_1
	v_cvt_pk_f32_fp8_sdwa v[194:195], v238 src0_sel:WORD_1
	v_pk_fma_f32 v[188:189], v[184:185], v[152:153], v[188:189]
	v_pk_fma_f32 v[222:223], v[192:193], v[152:153], v[222:223]
	v_pk_fma_f32 v[190:191], v[186:187], v[154:155], v[190:191]
	v_pk_fma_f32 v[176:177], v[194:195], v[154:155], v[176:177]
	v_cvt_pk_f32_fp8_e32 v[184:185], v235
	v_cvt_pk_f32_fp8_e32 v[192:193], v239
	v_cvt_pk_f32_fp8_sdwa v[186:187], v235 src0_sel:WORD_1
	v_cvt_pk_f32_fp8_sdwa v[194:195], v239 src0_sel:WORD_1
	v_pk_fma_f32 v[188:189], v[184:185], v[156:157], v[188:189]
	v_pk_fma_f32 v[222:223], v[192:193], v[156:157], v[222:223]
	v_pk_fma_f32 v[190:191], v[186:187], v[158:159], v[190:191]
	v_pk_fma_f32 v[176:177], v[194:195], v[158:159], v[176:177]
	v_pk_add_f32 v[188:189], v[188:189], v[190:191]
	v_pk_add_f32 v[222:223], v[222:223], v[176:177]
	v_add_f32_e32 v164, v188, v189
	v_add_f32_e32 v166, v222, v223
	v_cvt_pk_f32_fp8_e32 v[184:185], v240
	v_cvt_pk_f32_fp8_e32 v[192:193], v244
	v_cvt_pk_f32_fp8_sdwa v[186:187], v240 src0_sel:WORD_1
	v_cvt_pk_f32_fp8_sdwa v[194:195], v244 src0_sel:WORD_1
	v_pk_mul_f32 v[188:189], v[184:185], v[144:145]
	v_pk_mul_f32 v[222:223], v[192:193], v[144:145]
	v_pk_mul_f32 v[190:191], v[186:187], v[146:147]
	v_pk_mul_f32 v[176:177], v[194:195], v[146:147]
	v_cvt_pk_f32_fp8_e32 v[184:185], v241
	v_cvt_pk_f32_fp8_e32 v[192:193], v245
	v_cvt_pk_f32_fp8_sdwa v[186:187], v241 src0_sel:WORD_1
	v_cvt_pk_f32_fp8_sdwa v[194:195], v245 src0_sel:WORD_1
	v_pk_fma_f32 v[188:189], v[184:185], v[148:149], v[188:189]
	v_pk_fma_f32 v[222:223], v[192:193], v[148:149], v[222:223]
	v_pk_fma_f32 v[190:191], v[186:187], v[150:151], v[190:191]
	v_pk_fma_f32 v[176:177], v[194:195], v[150:151], v[176:177]
	v_cvt_pk_f32_fp8_e32 v[184:185], v242
	v_cvt_pk_f32_fp8_e32 v[192:193], v246
	v_cvt_pk_f32_fp8_sdwa v[186:187], v242 src0_sel:WORD_1
	v_cvt_pk_f32_fp8_sdwa v[194:195], v246 src0_sel:WORD_1
	v_pk_fma_f32 v[188:189], v[184:185], v[152:153], v[188:189]
	v_pk_fma_f32 v[222:223], v[192:193], v[152:153], v[222:223]
	v_pk_fma_f32 v[190:191], v[186:187], v[154:155], v[190:191]
	v_pk_fma_f32 v[176:177], v[194:195], v[154:155], v[176:177]
	v_cvt_pk_f32_fp8_e32 v[184:185], v243
	v_cvt_pk_f32_fp8_e32 v[192:193], v247
	v_cvt_pk_f32_fp8_sdwa v[186:187], v243 src0_sel:WORD_1
	v_cvt_pk_f32_fp8_sdwa v[194:195], v247 src0_sel:WORD_1
	v_pk_fma_f32 v[188:189], v[184:185], v[156:157], v[188:189]
	v_pk_fma_f32 v[222:223], v[192:193], v[156:157], v[222:223]
	v_pk_fma_f32 v[190:191], v[186:187], v[158:159], v[190:191]
	v_pk_fma_f32 v[176:177], v[194:195], v[158:159], v[176:177]
	v_pk_add_f32 v[188:189], v[188:189], v[190:191]
	v_pk_add_f32 v[222:223], v[222:223], v[176:177]
	v_add_f32_e32 v168, v188, v189
	v_add_f32_e32 v170, v222, v223
	v_cvt_pk_f32_fp8_e32 v[184:185], v248
	v_cvt_pk_f32_fp8_e32 v[192:193], v216
	v_cvt_pk_f32_fp8_sdwa v[186:187], v248 src0_sel:WORD_1
	v_cvt_pk_f32_fp8_sdwa v[194:195], v216 src0_sel:WORD_1
	v_pk_mul_f32 v[188:189], v[184:185], v[144:145]
	v_pk_mul_f32 v[222:223], v[192:193], v[144:145]
	v_pk_mul_f32 v[190:191], v[186:187], v[146:147]
	v_pk_mul_f32 v[176:177], v[194:195], v[146:147]
	v_cvt_pk_f32_fp8_e32 v[184:185], v249
	v_cvt_pk_f32_fp8_e32 v[192:193], v217
	v_cvt_pk_f32_fp8_sdwa v[186:187], v249 src0_sel:WORD_1
	v_cvt_pk_f32_fp8_sdwa v[194:195], v217 src0_sel:WORD_1
	v_pk_fma_f32 v[188:189], v[184:185], v[148:149], v[188:189]
	v_pk_fma_f32 v[222:223], v[192:193], v[148:149], v[222:223]
	v_pk_fma_f32 v[190:191], v[186:187], v[150:151], v[190:191]
	v_pk_fma_f32 v[176:177], v[194:195], v[150:151], v[176:177]
	v_cvt_pk_f32_fp8_e32 v[184:185], v250
	v_cvt_pk_f32_fp8_e32 v[192:193], v218
	v_cvt_pk_f32_fp8_sdwa v[186:187], v250 src0_sel:WORD_1
	v_cvt_pk_f32_fp8_sdwa v[194:195], v218 src0_sel:WORD_1
	v_pk_fma_f32 v[188:189], v[184:185], v[152:153], v[188:189]
	v_pk_fma_f32 v[222:223], v[192:193], v[152:153], v[222:223]
	v_pk_fma_f32 v[190:191], v[186:187], v[154:155], v[190:191]
	v_pk_fma_f32 v[176:177], v[194:195], v[154:155], v[176:177]
	v_cvt_pk_f32_fp8_e32 v[184:185], v251
	v_cvt_pk_f32_fp8_e32 v[192:193], v219
	v_cvt_pk_f32_fp8_sdwa v[186:187], v251 src0_sel:WORD_1
	v_cvt_pk_f32_fp8_sdwa v[194:195], v219 src0_sel:WORD_1
	v_pk_fma_f32 v[188:189], v[184:185], v[156:157], v[188:189]
	v_pk_fma_f32 v[222:223], v[192:193], v[156:157], v[222:223]
	v_pk_fma_f32 v[190:191], v[186:187], v[158:159], v[190:191]
	v_pk_fma_f32 v[176:177], v[194:195], v[158:159], v[176:177]
	v_pk_add_f32 v[188:189], v[188:189], v[190:191]
	v_pk_add_f32 v[222:223], v[222:223], v[176:177]
	v_add_f32_e32 v172, v188, v189
	v_add_f32_e32 v174, v222, v223

.Lp6c0_t0:
	v_readlane_b32 s14, v1, 0
	v_cvt_pk_f32_fp8_e32 v[184:185], v68
	v_cvt_pk_f32_fp8_sdwa v[186:187], v68 src0_sel:WORD_1
	v_pk_fma_f32 v[126:127], v[184:185], s[14:15], v[126:127] op_sel_hi:[1,0,1]
	v_pk_fma_f32 v[128:129], v[186:187], s[14:15], v[128:129] op_sel_hi:[1,0,1]
	v_cvt_pk_f32_fp8_e32 v[188:189], v69
	v_cvt_pk_f32_fp8_sdwa v[190:191], v69 src0_sel:WORD_1
	v_pk_fma_f32 v[130:131], v[188:189], s[14:15], v[130:131] op_sel_hi:[1,0,1]
	v_pk_fma_f32 v[132:133], v[190:191], s[14:15], v[132:133] op_sel_hi:[1,0,1]
	v_cvt_pk_f32_fp8_e32 v[184:185], v70
	v_cvt_pk_f32_fp8_sdwa v[186:187], v70 src0_sel:WORD_1
	v_pk_fma_f32 v[134:135], v[184:185], s[14:15], v[134:135] op_sel_hi:[1,0,1]
	v_pk_fma_f32 v[136:137], v[186:187], s[14:15], v[136:137] op_sel_hi:[1,0,1]
	v_cvt_pk_f32_fp8_e32 v[188:189], v71
	v_cvt_pk_f32_fp8_sdwa v[190:191], v71 src0_sel:WORD_1
	v_pk_fma_f32 v[138:139], v[188:189], s[14:15], v[138:139] op_sel_hi:[1,0,1]
	v_pk_fma_f32 v[140:141], v[190:191], s[14:15], v[140:141] op_sel_hi:[1,0,1]
	v_readlane_b32 s14, v1, 8
	v_cvt_pk_f32_fp8_e32 v[184:185], v64
	v_cvt_pk_f32_fp8_sdwa v[186:187], v64 src0_sel:WORD_1
	v_pk_fma_f32 v[126:127], v[184:185], s[14:15], v[126:127] op_sel_hi:[1,0,1]
	v_pk_fma_f32 v[128:129], v[186:187], s[14:15], v[128:129] op_sel_hi:[1,0,1]
	v_cvt_pk_f32_fp8_e32 v[188:189], v65
	v_cvt_pk_f32_fp8_sdwa v[190:191], v65 src0_sel:WORD_1
	v_pk_fma_f32 v[130:131], v[188:189], s[14:15], v[130:131] op_sel_hi:[1,0,1]
	v_pk_fma_f32 v[132:133], v[190:191], s[14:15], v[132:133] op_sel_hi:[1,0,1]
	v_cvt_pk_f32_fp8_e32 v[184:185], v66
	v_cvt_pk_f32_fp8_sdwa v[186:187], v66 src0_sel:WORD_1
	v_pk_fma_f32 v[134:135], v[184:185], s[14:15], v[134:135] op_sel_hi:[1,0,1]
	v_pk_fma_f32 v[136:137], v[186:187], s[14:15], v[136:137] op_sel_hi:[1,0,1]
	v_cvt_pk_f32_fp8_e32 v[188:189], v67
	v_cvt_pk_f32_fp8_sdwa v[190:191], v67 src0_sel:WORD_1
	v_pk_fma_f32 v[138:139], v[188:189], s[14:15], v[138:139] op_sel_hi:[1,0,1]
	v_pk_fma_f32 v[140:141], v[190:191], s[14:15], v[140:141] op_sel_hi:[1,0,1]
	v_readlane_b32 s14, v1, 16
	v_cvt_pk_f32_fp8_e32 v[184:185], v60
	v_cvt_pk_f32_fp8_sdwa v[186:187], v60 src0_sel:WORD_1
	v_pk_fma_f32 v[126:127], v[184:185], s[14:15], v[126:127] op_sel_hi:[1,0,1]
	v_pk_fma_f32 v[128:129], v[186:187], s[14:15], v[128:129] op_sel_hi:[1,0,1]
	v_cvt_pk_f32_fp8_e32 v[188:189], v61
	v_cvt_pk_f32_fp8_sdwa v[190:191], v61 src0_sel:WORD_1
	v_pk_fma_f32 v[130:131], v[188:189], s[14:15], v[130:131] op_sel_hi:[1,0,1]
	v_pk_fma_f32 v[132:133], v[190:191], s[14:15], v[132:133] op_sel_hi:[1,0,1]
	v_cvt_pk_f32_fp8_e32 v[184:185], v62
	v_cvt_pk_f32_fp8_sdwa v[186:187], v62 src0_sel:WORD_1
	v_pk_fma_f32 v[134:135], v[184:185], s[14:15], v[134:135] op_sel_hi:[1,0,1]
	v_pk_fma_f32 v[136:137], v[186:187], s[14:15], v[136:137] op_sel_hi:[1,0,1]
	v_cvt_pk_f32_fp8_e32 v[188:189], v63
	v_cvt_pk_f32_fp8_sdwa v[190:191], v63 src0_sel:WORD_1
	v_pk_fma_f32 v[138:139], v[188:189], s[14:15], v[138:139] op_sel_hi:[1,0,1]
	v_pk_fma_f32 v[140:141], v[190:191], s[14:15], v[140:141] op_sel_hi:[1,0,1]
	v_readlane_b32 s14, v1, 24
	v_cvt_pk_f32_fp8_e32 v[184:185], v56
	v_cvt_pk_f32_fp8_sdwa v[186:187], v56 src0_sel:WORD_1
	v_pk_fma_f32 v[126:127], v[184:185], s[14:15], v[126:127] op_sel_hi:[1,0,1]
	v_pk_fma_f32 v[128:129], v[186:187], s[14:15], v[128:129] op_sel_hi:[1,0,1]
	v_cvt_pk_f32_fp8_e32 v[188:189], v57
	v_cvt_pk_f32_fp8_sdwa v[190:191], v57 src0_sel:WORD_1
	v_pk_fma_f32 v[130:131], v[188:189], s[14:15], v[130:131] op_sel_hi:[1,0,1]
	v_pk_fma_f32 v[132:133], v[190:191], s[14:15], v[132:133] op_sel_hi:[1,0,1]
	v_cvt_pk_f32_fp8_e32 v[184:185], v58
	v_cvt_pk_f32_fp8_sdwa v[186:187], v58 src0_sel:WORD_1
	v_pk_fma_f32 v[134:135], v[184:185], s[14:15], v[134:135] op_sel_hi:[1,0,1]
	v_pk_fma_f32 v[136:137], v[186:187], s[14:15], v[136:137] op_sel_hi:[1,0,1]
	v_cvt_pk_f32_fp8_e32 v[188:189], v59
	v_cvt_pk_f32_fp8_sdwa v[190:191], v59 src0_sel:WORD_1
	v_pk_fma_f32 v[138:139], v[188:189], s[14:15], v[138:139] op_sel_hi:[1,0,1]
	v_pk_fma_f32 v[140:141], v[190:191], s[14:15], v[140:141] op_sel_hi:[1,0,1]
	v_readlane_b32 s14, v1, 32
	v_cvt_pk_f32_fp8_e32 v[184:185], v48
	v_cvt_pk_f32_fp8_sdwa v[186:187], v48 src0_sel:WORD_1
	v_pk_fma_f32 v[126:127], v[184:185], s[14:15], v[126:127] op_sel_hi:[1,0,1]
	v_pk_fma_f32 v[128:129], v[186:187], s[14:15], v[128:129] op_sel_hi:[1,0,1]
	v_cvt_pk_f32_fp8_e32 v[188:189], v49
	v_cvt_pk_f32_fp8_sdwa v[190:191], v49 src0_sel:WORD_1
	v_pk_fma_f32 v[130:131], v[188:189], s[14:15], v[130:131] op_sel_hi:[1,0,1]
	v_pk_fma_f32 v[132:133], v[190:191], s[14:15], v[132:133] op_sel_hi:[1,0,1]
	v_cvt_pk_f32_fp8_e32 v[184:185], v50
	v_cvt_pk_f32_fp8_sdwa v[186:187], v50 src0_sel:WORD_1
	v_pk_fma_f32 v[134:135], v[184:185], s[14:15], v[134:135] op_sel_hi:[1,0,1]
	v_pk_fma_f32 v[136:137], v[186:187], s[14:15], v[136:137] op_sel_hi:[1,0,1]
	v_cvt_pk_f32_fp8_e32 v[188:189], v51
	v_cvt_pk_f32_fp8_sdwa v[190:191], v51 src0_sel:WORD_1
	v_pk_fma_f32 v[138:139], v[188:189], s[14:15], v[138:139] op_sel_hi:[1,0,1]
	v_pk_fma_f32 v[140:141], v[190:191], s[14:15], v[140:141] op_sel_hi:[1,0,1]
	v_readlane_b32 s14, v1, 40
	v_cvt_pk_f32_fp8_e32 v[184:185], v32
	v_cvt_pk_f32_fp8_sdwa v[186:187], v32 src0_sel:WORD_1
	v_pk_fma_f32 v[126:127], v[184:185], s[14:15], v[126:127] op_sel_hi:[1,0,1]
	v_pk_fma_f32 v[128:129], v[186:187], s[14:15], v[128:129] op_sel_hi:[1,0,1]
	v_cvt_pk_f32_fp8_e32 v[188:189], v33
	v_cvt_pk_f32_fp8_sdwa v[190:191], v33 src0_sel:WORD_1
	v_pk_fma_f32 v[130:131], v[188:189], s[14:15], v[130:131] op_sel_hi:[1,0,1]
	v_pk_fma_f32 v[132:133], v[190:191], s[14:15], v[132:133] op_sel_hi:[1,0,1]
	v_cvt_pk_f32_fp8_e32 v[184:185], v34
	v_cvt_pk_f32_fp8_sdwa v[186:187], v34 src0_sel:WORD_1
	v_pk_fma_f32 v[134:135], v[184:185], s[14:15], v[134:135] op_sel_hi:[1,0,1]
	v_pk_fma_f32 v[136:137], v[186:187], s[14:15], v[136:137] op_sel_hi:[1,0,1]
	v_cvt_pk_f32_fp8_e32 v[188:189], v35
	v_cvt_pk_f32_fp8_sdwa v[190:191], v35 src0_sel:WORD_1
	v_pk_fma_f32 v[138:139], v[188:189], s[14:15], v[138:139] op_sel_hi:[1,0,1]
	v_pk_fma_f32 v[140:141], v[190:191], s[14:15], v[140:141] op_sel_hi:[1,0,1]
	v_readlane_b32 s14, v1, 48
	v_cvt_pk_f32_fp8_e32 v[184:185], v16
	v_cvt_pk_f32_fp8_sdwa v[186:187], v16 src0_sel:WORD_1
	v_pk_fma_f32 v[126:127], v[184:185], s[14:15], v[126:127] op_sel_hi:[1,0,1]
	v_pk_fma_f32 v[128:129], v[186:187], s[14:15], v[128:129] op_sel_hi:[1,0,1]
	v_cvt_pk_f32_fp8_e32 v[188:189], v17
	v_cvt_pk_f32_fp8_sdwa v[190:191], v17 src0_sel:WORD_1
	v_pk_fma_f32 v[130:131], v[188:189], s[14:15], v[130:131] op_sel_hi:[1,0,1]
	v_pk_fma_f32 v[132:133], v[190:191], s[14:15], v[132:133] op_sel_hi:[1,0,1]
	v_cvt_pk_f32_fp8_e32 v[184:185], v18
	v_cvt_pk_f32_fp8_sdwa v[186:187], v18 src0_sel:WORD_1
	v_pk_fma_f32 v[134:135], v[184:185], s[14:15], v[134:135] op_sel_hi:[1,0,1]
	v_pk_fma_f32 v[136:137], v[186:187], s[14:15], v[136:137] op_sel_hi:[1,0,1]
	v_cvt_pk_f32_fp8_e32 v[188:189], v19
	v_cvt_pk_f32_fp8_sdwa v[190:191], v19 src0_sel:WORD_1
	v_pk_fma_f32 v[138:139], v[188:189], s[14:15], v[138:139] op_sel_hi:[1,0,1]
	v_pk_fma_f32 v[140:141], v[190:191], s[14:15], v[140:141] op_sel_hi:[1,0,1]
	v_readlane_b32 s14, v1, 56
	v_cvt_pk_f32_fp8_e32 v[184:185], v12
	v_cvt_pk_f32_fp8_sdwa v[186:187], v12 src0_sel:WORD_1
	v_pk_fma_f32 v[126:127], v[184:185], s[14:15], v[126:127] op_sel_hi:[1,0,1]
	v_pk_fma_f32 v[128:129], v[186:187], s[14:15], v[128:129] op_sel_hi:[1,0,1]
	v_cvt_pk_f32_fp8_e32 v[188:189], v13
	v_cvt_pk_f32_fp8_sdwa v[190:191], v13 src0_sel:WORD_1
	v_pk_fma_f32 v[130:131], v[188:189], s[14:15], v[130:131] op_sel_hi:[1,0,1]
	v_pk_fma_f32 v[132:133], v[190:191], s[14:15], v[132:133] op_sel_hi:[1,0,1]
	v_cvt_pk_f32_fp8_e32 v[184:185], v14
	v_cvt_pk_f32_fp8_sdwa v[186:187], v14 src0_sel:WORD_1
	v_pk_fma_f32 v[134:135], v[184:185], s[14:15], v[134:135] op_sel_hi:[1,0,1]
	v_pk_fma_f32 v[136:137], v[186:187], s[14:15], v[136:137] op_sel_hi:[1,0,1]
	v_cvt_pk_f32_fp8_e32 v[188:189], v15
	v_cvt_pk_f32_fp8_sdwa v[190:191], v15 src0_sel:WORD_1
	v_pk_fma_f32 v[138:139], v[188:189], s[14:15], v[138:139] op_sel_hi:[1,0,1]
	v_pk_fma_f32 v[140:141], v[190:191], s[14:15], v[140:141] op_sel_hi:[1,0,1]
	s_branch .Lp6c0_axdone
.Lp6c0_t1:
	v_readlane_b32 s14, v1, 0
	v_cvt_pk_f32_fp8_e32 v[184:185], v68
	v_cvt_pk_f32_fp8_sdwa v[186:187], v68 src0_sel:WORD_1
	v_pk_fma_f32 v[110:111], v[184:185], s[14:15], v[110:111] op_sel_hi:[1,0,1]
	v_pk_fma_f32 v[112:113], v[186:187], s[14:15], v[112:113] op_sel_hi:[1,0,1]
	v_cvt_pk_f32_fp8_e32 v[188:189], v69
	v_cvt_pk_f32_fp8_sdwa v[190:191], v69 src0_sel:WORD_1
	v_pk_fma_f32 v[114:115], v[188:189], s[14:15], v[114:115] op_sel_hi:[1,0,1]
	v_pk_fma_f32 v[116:117], v[190:191], s[14:15], v[116:117] op_sel_hi:[1,0,1]
	v_cvt_pk_f32_fp8_e32 v[184:185], v70
	v_cvt_pk_f32_fp8_sdwa v[186:187], v70 src0_sel:WORD_1
	v_pk_fma_f32 v[118:119], v[184:185], s[14:15], v[118:119] op_sel_hi:[1,0,1]
	v_pk_fma_f32 v[120:121], v[186:187], s[14:15], v[120:121] op_sel_hi:[1,0,1]
	v_cvt_pk_f32_fp8_e32 v[188:189], v71
	v_cvt_pk_f32_fp8_sdwa v[190:191], v71 src0_sel:WORD_1
	v_pk_fma_f32 v[122:123], v[188:189], s[14:15], v[122:123] op_sel_hi:[1,0,1]
	v_pk_fma_f32 v[124:125], v[190:191], s[14:15], v[124:125] op_sel_hi:[1,0,1]
	v_readlane_b32 s14, v1, 8
	v_cvt_pk_f32_fp8_e32 v[184:185], v64
	v_cvt_pk_f32_fp8_sdwa v[186:187], v64 src0_sel:WORD_1
	v_pk_fma_f32 v[110:111], v[184:185], s[14:15], v[110:111] op_sel_hi:[1,0,1]
	v_pk_fma_f32 v[112:113], v[186:187], s[14:15], v[112:113] op_sel_hi:[1,0,1]
	v_cvt_pk_f32_fp8_e32 v[188:189], v65
	v_cvt_pk_f32_fp8_sdwa v[190:191], v65 src0_sel:WORD_1
	v_pk_fma_f32 v[114:115], v[188:189], s[14:15], v[114:115] op_sel_hi:[1,0,1]
	v_pk_fma_f32 v[116:117], v[190:191], s[14:15], v[116:117] op_sel_hi:[1,0,1]
	v_cvt_pk_f32_fp8_e32 v[184:185], v66
	v_cvt_pk_f32_fp8_sdwa v[186:187], v66 src0_sel:WORD_1
	v_pk_fma_f32 v[118:119], v[184:185], s[14:15], v[118:119] op_sel_hi:[1,0,1]
	v_pk_fma_f32 v[120:121], v[186:187], s[14:15], v[120:121] op_sel_hi:[1,0,1]
	v_cvt_pk_f32_fp8_e32 v[188:189], v67
	v_cvt_pk_f32_fp8_sdwa v[190:191], v67 src0_sel:WORD_1
	v_pk_fma_f32 v[122:123], v[188:189], s[14:15], v[122:123] op_sel_hi:[1,0,1]
	v_pk_fma_f32 v[124:125], v[190:191], s[14:15], v[124:125] op_sel_hi:[1,0,1]
	v_readlane_b32 s14, v1, 16
	v_cvt_pk_f32_fp8_e32 v[184:185], v60
	v_cvt_pk_f32_fp8_sdwa v[186:187], v60 src0_sel:WORD_1
	v_pk_fma_f32 v[110:111], v[184:185], s[14:15], v[110:111] op_sel_hi:[1,0,1]
	v_pk_fma_f32 v[112:113], v[186:187], s[14:15], v[112:113] op_sel_hi:[1,0,1]
	v_cvt_pk_f32_fp8_e32 v[188:189], v61
	v_cvt_pk_f32_fp8_sdwa v[190:191], v61 src0_sel:WORD_1
	v_pk_fma_f32 v[114:115], v[188:189], s[14:15], v[114:115] op_sel_hi:[1,0,1]
	v_pk_fma_f32 v[116:117], v[190:191], s[14:15], v[116:117] op_sel_hi:[1,0,1]
	v_cvt_pk_f32_fp8_e32 v[184:185], v62
	v_cvt_pk_f32_fp8_sdwa v[186:187], v62 src0_sel:WORD_1
	v_pk_fma_f32 v[118:119], v[184:185], s[14:15], v[118:119] op_sel_hi:[1,0,1]
	v_pk_fma_f32 v[120:121], v[186:187], s[14:15], v[120:121] op_sel_hi:[1,0,1]
	v_cvt_pk_f32_fp8_e32 v[188:189], v63
	v_cvt_pk_f32_fp8_sdwa v[190:191], v63 src0_sel:WORD_1
	v_pk_fma_f32 v[122:123], v[188:189], s[14:15], v[122:123] op_sel_hi:[1,0,1]
	v_pk_fma_f32 v[124:125], v[190:191], s[14:15], v[124:125] op_sel_hi:[1,0,1]
	v_readlane_b32 s14, v1, 24
	v_cvt_pk_f32_fp8_e32 v[184:185], v56
	v_cvt_pk_f32_fp8_sdwa v[186:187], v56 src0_sel:WORD_1
	v_pk_fma_f32 v[110:111], v[184:185], s[14:15], v[110:111] op_sel_hi:[1,0,1]
	v_pk_fma_f32 v[112:113], v[186:187], s[14:15], v[112:113] op_sel_hi:[1,0,1]
	v_cvt_pk_f32_fp8_e32 v[188:189], v57
	v_cvt_pk_f32_fp8_sdwa v[190:191], v57 src0_sel:WORD_1
	v_pk_fma_f32 v[114:115], v[188:189], s[14:15], v[114:115] op_sel_hi:[1,0,1]
	v_pk_fma_f32 v[116:117], v[190:191], s[14:15], v[116:117] op_sel_hi:[1,0,1]
	v_cvt_pk_f32_fp8_e32 v[184:185], v58
	v_cvt_pk_f32_fp8_sdwa v[186:187], v58 src0_sel:WORD_1
	v_pk_fma_f32 v[118:119], v[184:185], s[14:15], v[118:119] op_sel_hi:[1,0,1]
	v_pk_fma_f32 v[120:121], v[186:187], s[14:15], v[120:121] op_sel_hi:[1,0,1]
	v_cvt_pk_f32_fp8_e32 v[188:189], v59
	v_cvt_pk_f32_fp8_sdwa v[190:191], v59 src0_sel:WORD_1
	v_pk_fma_f32 v[122:123], v[188:189], s[14:15], v[122:123] op_sel_hi:[1,0,1]
	v_pk_fma_f32 v[124:125], v[190:191], s[14:15], v[124:125] op_sel_hi:[1,0,1]
	v_readlane_b32 s14, v1, 32
	v_cvt_pk_f32_fp8_e32 v[184:185], v48
	v_cvt_pk_f32_fp8_sdwa v[186:187], v48 src0_sel:WORD_1
	v_pk_fma_f32 v[110:111], v[184:185], s[14:15], v[110:111] op_sel_hi:[1,0,1]
	v_pk_fma_f32 v[112:113], v[186:187], s[14:15], v[112:113] op_sel_hi:[1,0,1]
	v_cvt_pk_f32_fp8_e32 v[188:189], v49
	v_cvt_pk_f32_fp8_sdwa v[190:191], v49 src0_sel:WORD_1
	v_pk_fma_f32 v[114:115], v[188:189], s[14:15], v[114:115] op_sel_hi:[1,0,1]
	v_pk_fma_f32 v[116:117], v[190:191], s[14:15], v[116:117] op_sel_hi:[1,0,1]
	v_cvt_pk_f32_fp8_e32 v[184:185], v50
	v_cvt_pk_f32_fp8_sdwa v[186:187], v50 src0_sel:WORD_1
	v_pk_fma_f32 v[118:119], v[184:185], s[14:15], v[118:119] op_sel_hi:[1,0,1]
	v_pk_fma_f32 v[120:121], v[186:187], s[14:15], v[120:121] op_sel_hi:[1,0,1]
	v_cvt_pk_f32_fp8_e32 v[188:189], v51
	v_cvt_pk_f32_fp8_sdwa v[190:191], v51 src0_sel:WORD_1
	v_pk_fma_f32 v[122:123], v[188:189], s[14:15], v[122:123] op_sel_hi:[1,0,1]
	v_pk_fma_f32 v[124:125], v[190:191], s[14:15], v[124:125] op_sel_hi:[1,0,1]
	v_readlane_b32 s14, v1, 40
	v_cvt_pk_f32_fp8_e32 v[184:185], v32
	v_cvt_pk_f32_fp8_sdwa v[186:187], v32 src0_sel:WORD_1
	v_pk_fma_f32 v[110:111], v[184:185], s[14:15], v[110:111] op_sel_hi:[1,0,1]
	v_pk_fma_f32 v[112:113], v[186:187], s[14:15], v[112:113] op_sel_hi:[1,0,1]
	v_cvt_pk_f32_fp8_e32 v[188:189], v33
	v_cvt_pk_f32_fp8_sdwa v[190:191], v33 src0_sel:WORD_1
	v_pk_fma_f32 v[114:115], v[188:189], s[14:15], v[114:115] op_sel_hi:[1,0,1]
	v_pk_fma_f32 v[116:117], v[190:191], s[14:15], v[116:117] op_sel_hi:[1,0,1]
	v_cvt_pk_f32_fp8_e32 v[184:185], v34
	v_cvt_pk_f32_fp8_sdwa v[186:187], v34 src0_sel:WORD_1
	v_pk_fma_f32 v[118:119], v[184:185], s[14:15], v[118:119] op_sel_hi:[1,0,1]
	v_pk_fma_f32 v[120:121], v[186:187], s[14:15], v[120:121] op_sel_hi:[1,0,1]
	v_cvt_pk_f32_fp8_e32 v[188:189], v35
	v_cvt_pk_f32_fp8_sdwa v[190:191], v35 src0_sel:WORD_1
	v_pk_fma_f32 v[122:123], v[188:189], s[14:15], v[122:123] op_sel_hi:[1,0,1]
	v_pk_fma_f32 v[124:125], v[190:191], s[14:15], v[124:125] op_sel_hi:[1,0,1]
	v_readlane_b32 s14, v1, 48
	v_cvt_pk_f32_fp8_e32 v[184:185], v16
	v_cvt_pk_f32_fp8_sdwa v[186:187], v16 src0_sel:WORD_1
	v_pk_fma_f32 v[110:111], v[184:185], s[14:15], v[110:111] op_sel_hi:[1,0,1]
	v_pk_fma_f32 v[112:113], v[186:187], s[14:15], v[112:113] op_sel_hi:[1,0,1]
	v_cvt_pk_f32_fp8_e32 v[188:189], v17
	v_cvt_pk_f32_fp8_sdwa v[190:191], v17 src0_sel:WORD_1
	v_pk_fma_f32 v[114:115], v[188:189], s[14:15], v[114:115] op_sel_hi:[1,0,1]
	v_pk_fma_f32 v[116:117], v[190:191], s[14:15], v[116:117] op_sel_hi:[1,0,1]
	v_cvt_pk_f32_fp8_e32 v[184:185], v18
	v_cvt_pk_f32_fp8_sdwa v[186:187], v18 src0_sel:WORD_1
	v_pk_fma_f32 v[118:119], v[184:185], s[14:15], v[118:119] op_sel_hi:[1,0,1]
	v_pk_fma_f32 v[120:121], v[186:187], s[14:15], v[120:121] op_sel_hi:[1,0,1]
	v_cvt_pk_f32_fp8_e32 v[188:189], v19
	v_cvt_pk_f32_fp8_sdwa v[190:191], v19 src0_sel:WORD_1
	v_pk_fma_f32 v[122:123], v[188:189], s[14:15], v[122:123] op_sel_hi:[1,0,1]
	v_pk_fma_f32 v[124:125], v[190:191], s[14:15], v[124:125] op_sel_hi:[1,0,1]
	v_readlane_b32 s14, v1, 56
	v_cvt_pk_f32_fp8_e32 v[184:185], v12
	v_cvt_pk_f32_fp8_sdwa v[186:187], v12 src0_sel:WORD_1
	v_pk_fma_f32 v[110:111], v[184:185], s[14:15], v[110:111] op_sel_hi:[1,0,1]
	v_pk_fma_f32 v[112:113], v[186:187], s[14:15], v[112:113] op_sel_hi:[1,0,1]
	v_cvt_pk_f32_fp8_e32 v[188:189], v13
	v_cvt_pk_f32_fp8_sdwa v[190:191], v13 src0_sel:WORD_1
	v_pk_fma_f32 v[114:115], v[188:189], s[14:15], v[114:115] op_sel_hi:[1,0,1]
	v_pk_fma_f32 v[116:117], v[190:191], s[14:15], v[116:117] op_sel_hi:[1,0,1]
	v_cvt_pk_f32_fp8_e32 v[184:185], v14
	v_cvt_pk_f32_fp8_sdwa v[186:187], v14 src0_sel:WORD_1
	v_pk_fma_f32 v[118:119], v[184:185], s[14:15], v[118:119] op_sel_hi:[1,0,1]
	v_pk_fma_f32 v[120:121], v[186:187], s[14:15], v[120:121] op_sel_hi:[1,0,1]
	v_cvt_pk_f32_fp8_e32 v[188:189], v15
	v_cvt_pk_f32_fp8_sdwa v[190:191], v15 src0_sel:WORD_1
	v_pk_fma_f32 v[122:123], v[188:189], s[14:15], v[122:123] op_sel_hi:[1,0,1]
	v_pk_fma_f32 v[124:125], v[190:191], s[14:15], v[124:125] op_sel_hi:[1,0,1]
	s_branch .Lp6c0_axdone
.Lp6c0_t2:
	v_readlane_b32 s14, v1, 0
	v_cvt_pk_f32_fp8_e32 v[184:185], v68
	v_cvt_pk_f32_fp8_sdwa v[186:187], v68 src0_sel:WORD_1
	v_pk_fma_f32 v[94:95], v[184:185], s[14:15], v[94:95] op_sel_hi:[1,0,1]
	v_pk_fma_f32 v[96:97], v[186:187], s[14:15], v[96:97] op_sel_hi:[1,0,1]
	v_cvt_pk_f32_fp8_e32 v[188:189], v69
	v_cvt_pk_f32_fp8_sdwa v[190:191], v69 src0_sel:WORD_1
	v_pk_fma_f32 v[98:99], v[188:189], s[14:15], v[98:99] op_sel_hi:[1,0,1]
	v_pk_fma_f32 v[100:101], v[190:191], s[14:15], v[100:101] op_sel_hi:[1,0,1]
	v_cvt_pk_f32_fp8_e32 v[184:185], v70
	v_cvt_pk_f32_fp8_sdwa v[186:187], v70 src0_sel:WORD_1
	v_pk_fma_f32 v[102:103], v[184:185], s[14:15], v[102:103] op_sel_hi:[1,0,1]
	v_pk_fma_f32 v[104:105], v[186:187], s[14:15], v[104:105] op_sel_hi:[1,0,1]
	v_cvt_pk_f32_fp8_e32 v[188:189], v71
	v_cvt_pk_f32_fp8_sdwa v[190:191], v71 src0_sel:WORD_1
	v_pk_fma_f32 v[106:107], v[188:189], s[14:15], v[106:107] op_sel_hi:[1,0,1]
	v_pk_fma_f32 v[108:109], v[190:191], s[14:15], v[108:109] op_sel_hi:[1,0,1]
	v_readlane_b32 s14, v1, 8
	v_cvt_pk_f32_fp8_e32 v[184:185], v64
	v_cvt_pk_f32_fp8_sdwa v[186:187], v64 src0_sel:WORD_1
	v_pk_fma_f32 v[94:95], v[184:185], s[14:15], v[94:95] op_sel_hi:[1,0,1]
	v_pk_fma_f32 v[96:97], v[186:187], s[14:15], v[96:97] op_sel_hi:[1,0,1]
	v_cvt_pk_f32_fp8_e32 v[188:189], v65
	v_cvt_pk_f32_fp8_sdwa v[190:191], v65 src0_sel:WORD_1
	v_pk_fma_f32 v[98:99], v[188:189], s[14:15], v[98:99] op_sel_hi:[1,0,1]
	v_pk_fma_f32 v[100:101], v[190:191], s[14:15], v[100:101] op_sel_hi:[1,0,1]
	v_cvt_pk_f32_fp8_e32 v[184:185], v66
	v_cvt_pk_f32_fp8_sdwa v[186:187], v66 src0_sel:WORD_1
	v_pk_fma_f32 v[102:103], v[184:185], s[14:15], v[102:103] op_sel_hi:[1,0,1]
	v_pk_fma_f32 v[104:105], v[186:187], s[14:15], v[104:105] op_sel_hi:[1,0,1]
	v_cvt_pk_f32_fp8_e32 v[188:189], v67
	v_cvt_pk_f32_fp8_sdwa v[190:191], v67 src0_sel:WORD_1
	v_pk_fma_f32 v[106:107], v[188:189], s[14:15], v[106:107] op_sel_hi:[1,0,1]
	v_pk_fma_f32 v[108:109], v[190:191], s[14:15], v[108:109] op_sel_hi:[1,0,1]
	v_readlane_b32 s14, v1, 16
	v_cvt_pk_f32_fp8_e32 v[184:185], v60
	v_cvt_pk_f32_fp8_sdwa v[186:187], v60 src0_sel:WORD_1
	v_pk_fma_f32 v[94:95], v[184:185], s[14:15], v[94:95] op_sel_hi:[1,0,1]
	v_pk_fma_f32 v[96:97], v[186:187], s[14:15], v[96:97] op_sel_hi:[1,0,1]
	v_cvt_pk_f32_fp8_e32 v[188:189], v61
	v_cvt_pk_f32_fp8_sdwa v[190:191], v61 src0_sel:WORD_1
	v_pk_fma_f32 v[98:99], v[188:189], s[14:15], v[98:99] op_sel_hi:[1,0,1]
	v_pk_fma_f32 v[100:101], v[190:191], s[14:15], v[100:101] op_sel_hi:[1,0,1]
	v_cvt_pk_f32_fp8_e32 v[184:185], v62
	v_cvt_pk_f32_fp8_sdwa v[186:187], v62 src0_sel:WORD_1
	v_pk_fma_f32 v[102:103], v[184:185], s[14:15], v[102:103] op_sel_hi:[1,0,1]
	v_pk_fma_f32 v[104:105], v[186:187], s[14:15], v[104:105] op_sel_hi:[1,0,1]
	v_cvt_pk_f32_fp8_e32 v[188:189], v63
	v_cvt_pk_f32_fp8_sdwa v[190:191], v63 src0_sel:WORD_1
	v_pk_fma_f32 v[106:107], v[188:189], s[14:15], v[106:107] op_sel_hi:[1,0,1]
	v_pk_fma_f32 v[108:109], v[190:191], s[14:15], v[108:109] op_sel_hi:[1,0,1]
	v_readlane_b32 s14, v1, 24
	v_cvt_pk_f32_fp8_e32 v[184:185], v56
	v_cvt_pk_f32_fp8_sdwa v[186:187], v56 src0_sel:WORD_1
	v_pk_fma_f32 v[94:95], v[184:185], s[14:15], v[94:95] op_sel_hi:[1,0,1]
	v_pk_fma_f32 v[96:97], v[186:187], s[14:15], v[96:97] op_sel_hi:[1,0,1]
	v_cvt_pk_f32_fp8_e32 v[188:189], v57
	v_cvt_pk_f32_fp8_sdwa v[190:191], v57 src0_sel:WORD_1
	v_pk_fma_f32 v[98:99], v[188:189], s[14:15], v[98:99] op_sel_hi:[1,0,1]
	v_pk_fma_f32 v[100:101], v[190:191], s[14:15], v[100:101] op_sel_hi:[1,0,1]
	v_cvt_pk_f32_fp8_e32 v[184:185], v58
	v_cvt_pk_f32_fp8_sdwa v[186:187], v58 src0_sel:WORD_1
	v_pk_fma_f32 v[102:103], v[184:185], s[14:15], v[102:103] op_sel_hi:[1,0,1]
	v_pk_fma_f32 v[104:105], v[186:187], s[14:15], v[104:105] op_sel_hi:[1,0,1]
	v_cvt_pk_f32_fp8_e32 v[188:189], v59
	v_cvt_pk_f32_fp8_sdwa v[190:191], v59 src0_sel:WORD_1
	v_pk_fma_f32 v[106:107], v[188:189], s[14:15], v[106:107] op_sel_hi:[1,0,1]
	v_pk_fma_f32 v[108:109], v[190:191], s[14:15], v[108:109] op_sel_hi:[1,0,1]
	v_readlane_b32 s14, v1, 32
	v_cvt_pk_f32_fp8_e32 v[184:185], v48
	v_cvt_pk_f32_fp8_sdwa v[186:187], v48 src0_sel:WORD_1
	v_pk_fma_f32 v[94:95], v[184:185], s[14:15], v[94:95] op_sel_hi:[1,0,1]
	v_pk_fma_f32 v[96:97], v[186:187], s[14:15], v[96:97] op_sel_hi:[1,0,1]
	v_cvt_pk_f32_fp8_e32 v[188:189], v49
	v_cvt_pk_f32_fp8_sdwa v[190:191], v49 src0_sel:WORD_1
	v_pk_fma_f32 v[98:99], v[188:189], s[14:15], v[98:99] op_sel_hi:[1,0,1]
	v_pk_fma_f32 v[100:101], v[190:191], s[14:15], v[100:101] op_sel_hi:[1,0,1]
	v_cvt_pk_f32_fp8_e32 v[184:185], v50
	v_cvt_pk_f32_fp8_sdwa v[186:187], v50 src0_sel:WORD_1
	v_pk_fma_f32 v[102:103], v[184:185], s[14:15], v[102:103] op_sel_hi:[1,0,1]
	v_pk_fma_f32 v[104:105], v[186:187], s[14:15], v[104:105] op_sel_hi:[1,0,1]
	v_cvt_pk_f32_fp8_e32 v[188:189], v51
	v_cvt_pk_f32_fp8_sdwa v[190:191], v51 src0_sel:WORD_1
	v_pk_fma_f32 v[106:107], v[188:189], s[14:15], v[106:107] op_sel_hi:[1,0,1]
	v_pk_fma_f32 v[108:109], v[190:191], s[14:15], v[108:109] op_sel_hi:[1,0,1]
	v_readlane_b32 s14, v1, 40
	v_cvt_pk_f32_fp8_e32 v[184:185], v32
	v_cvt_pk_f32_fp8_sdwa v[186:187], v32 src0_sel:WORD_1
	v_pk_fma_f32 v[94:95], v[184:185], s[14:15], v[94:95] op_sel_hi:[1,0,1]
	v_pk_fma_f32 v[96:97], v[186:187], s[14:15], v[96:97] op_sel_hi:[1,0,1]
	v_cvt_pk_f32_fp8_e32 v[188:189], v33
	v_cvt_pk_f32_fp8_sdwa v[190:191], v33 src0_sel:WORD_1
	v_pk_fma_f32 v[98:99], v[188:189], s[14:15], v[98:99] op_sel_hi:[1,0,1]
	v_pk_fma_f32 v[100:101], v[190:191], s[14:15], v[100:101] op_sel_hi:[1,0,1]
	v_cvt_pk_f32_fp8_e32 v[184:185], v34
	v_cvt_pk_f32_fp8_sdwa v[186:187], v34 src0_sel:WORD_1
	v_pk_fma_f32 v[102:103], v[184:185], s[14:15], v[102:103] op_sel_hi:[1,0,1]
	v_pk_fma_f32 v[104:105], v[186:187], s[14:15], v[104:105] op_sel_hi:[1,0,1]
	v_cvt_pk_f32_fp8_e32 v[188:189], v35
	v_cvt_pk_f32_fp8_sdwa v[190:191], v35 src0_sel:WORD_1
	v_pk_fma_f32 v[106:107], v[188:189], s[14:15], v[106:107] op_sel_hi:[1,0,1]
	v_pk_fma_f32 v[108:109], v[190:191], s[14:15], v[108:109] op_sel_hi:[1,0,1]
	v_readlane_b32 s14, v1, 48
	v_cvt_pk_f32_fp8_e32 v[184:185], v16
	v_cvt_pk_f32_fp8_sdwa v[186:187], v16 src0_sel:WORD_1
	v_pk_fma_f32 v[94:95], v[184:185], s[14:15], v[94:95] op_sel_hi:[1,0,1]
	v_pk_fma_f32 v[96:97], v[186:187], s[14:15], v[96:97] op_sel_hi:[1,0,1]
	v_cvt_pk_f32_fp8_e32 v[188:189], v17
	v_cvt_pk_f32_fp8_sdwa v[190:191], v17 src0_sel:WORD_1
	v_pk_fma_f32 v[98:99], v[188:189], s[14:15], v[98:99] op_sel_hi:[1,0,1]
	v_pk_fma_f32 v[100:101], v[190:191], s[14:15], v[100:101] op_sel_hi:[1,0,1]
	v_cvt_pk_f32_fp8_e32 v[184:185], v18
	v_cvt_pk_f32_fp8_sdwa v[186:187], v18 src0_sel:WORD_1
	v_pk_fma_f32 v[102:103], v[184:185], s[14:15], v[102:103] op_sel_hi:[1,0,1]
	v_pk_fma_f32 v[104:105], v[186:187], s[14:15], v[104:105] op_sel_hi:[1,0,1]
	v_cvt_pk_f32_fp8_e32 v[188:189], v19
	v_cvt_pk_f32_fp8_sdwa v[190:191], v19 src0_sel:WORD_1
	v_pk_fma_f32 v[106:107], v[188:189], s[14:15], v[106:107] op_sel_hi:[1,0,1]
	v_pk_fma_f32 v[108:109], v[190:191], s[14:15], v[108:109] op_sel_hi:[1,0,1]
	v_readlane_b32 s14, v1, 56
	v_cvt_pk_f32_fp8_e32 v[184:185], v12
	v_cvt_pk_f32_fp8_sdwa v[186:187], v12 src0_sel:WORD_1
	v_pk_fma_f32 v[94:95], v[184:185], s[14:15], v[94:95] op_sel_hi:[1,0,1]
	v_pk_fma_f32 v[96:97], v[186:187], s[14:15], v[96:97] op_sel_hi:[1,0,1]
	v_cvt_pk_f32_fp8_e32 v[188:189], v13
	v_cvt_pk_f32_fp8_sdwa v[190:191], v13 src0_sel:WORD_1
	v_pk_fma_f32 v[98:99], v[188:189], s[14:15], v[98:99] op_sel_hi:[1,0,1]
	v_pk_fma_f32 v[100:101], v[190:191], s[14:15], v[100:101] op_sel_hi:[1,0,1]
	v_cvt_pk_f32_fp8_e32 v[184:185], v14
	v_cvt_pk_f32_fp8_sdwa v[186:187], v14 src0_sel:WORD_1
	v_pk_fma_f32 v[102:103], v[184:185], s[14:15], v[102:103] op_sel_hi:[1,0,1]
	v_pk_fma_f32 v[104:105], v[186:187], s[14:15], v[104:105] op_sel_hi:[1,0,1]
	v_cvt_pk_f32_fp8_e32 v[188:189], v15
	v_cvt_pk_f32_fp8_sdwa v[190:191], v15 src0_sel:WORD_1
	v_pk_fma_f32 v[106:107], v[188:189], s[14:15], v[106:107] op_sel_hi:[1,0,1]
	v_pk_fma_f32 v[108:109], v[190:191], s[14:15], v[108:109] op_sel_hi:[1,0,1]
	s_branch .Lp6c0_axdone
.Lp6c0_t3:
	v_readlane_b32 s14, v1, 0
	v_cvt_pk_f32_fp8_e32 v[184:185], v68
	v_cvt_pk_f32_fp8_sdwa v[186:187], v68 src0_sel:WORD_1
	v_pk_fma_f32 v[78:79], v[184:185], s[14:15], v[78:79] op_sel_hi:[1,0,1]
	v_pk_fma_f32 v[80:81], v[186:187], s[14:15], v[80:81] op_sel_hi:[1,0,1]
	v_cvt_pk_f32_fp8_e32 v[188:189], v69
	v_cvt_pk_f32_fp8_sdwa v[190:191], v69 src0_sel:WORD_1
	v_pk_fma_f32 v[82:83], v[188:189], s[14:15], v[82:83] op_sel_hi:[1,0,1]
	v_pk_fma_f32 v[86:87], v[190:191], s[14:15], v[86:87] op_sel_hi:[1,0,1]
	v_cvt_pk_f32_fp8_e32 v[184:185], v70
	v_cvt_pk_f32_fp8_sdwa v[186:187], v70 src0_sel:WORD_1
	v_pk_fma_f32 v[88:89], v[184:185], s[14:15], v[88:89] op_sel_hi:[1,0,1]
	v_pk_fma_f32 v[90:91], v[186:187], s[14:15], v[90:91] op_sel_hi:[1,0,1]
	v_cvt_pk_f32_fp8_e32 v[188:189], v71
	v_cvt_pk_f32_fp8_sdwa v[190:191], v71 src0_sel:WORD_1
	v_pk_fma_f32 v[92:93], v[188:189], s[14:15], v[92:93] op_sel_hi:[1,0,1]
	v_pk_fma_f32 v[84:85], v[190:191], s[14:15], v[84:85] op_sel_hi:[1,0,1]
	v_readlane_b32 s14, v1, 8
	v_cvt_pk_f32_fp8_e32 v[184:185], v64
	v_cvt_pk_f32_fp8_sdwa v[186:187], v64 src0_sel:WORD_1
	v_pk_fma_f32 v[78:79], v[184:185], s[14:15], v[78:79] op_sel_hi:[1,0,1]
	v_pk_fma_f32 v[80:81], v[186:187], s[14:15], v[80:81] op_sel_hi:[1,0,1]
	v_cvt_pk_f32_fp8_e32 v[188:189], v65
	v_cvt_pk_f32_fp8_sdwa v[190:191], v65 src0_sel:WORD_1
	v_pk_fma_f32 v[82:83], v[188:189], s[14:15], v[82:83] op_sel_hi:[1,0,1]
	v_pk_fma_f32 v[86:87], v[190:191], s[14:15], v[86:87] op_sel_hi:[1,0,1]
	v_cvt_pk_f32_fp8_e32 v[184:185], v66
	v_cvt_pk_f32_fp8_sdwa v[186:187], v66 src0_sel:WORD_1
	v_pk_fma_f32 v[88:89], v[184:185], s[14:15], v[88:89] op_sel_hi:[1,0,1]
	v_pk_fma_f32 v[90:91], v[186:187], s[14:15], v[90:91] op_sel_hi:[1,0,1]
	v_cvt_pk_f32_fp8_e32 v[188:189], v67
	v_cvt_pk_f32_fp8_sdwa v[190:191], v67 src0_sel:WORD_1
	v_pk_fma_f32 v[92:93], v[188:189], s[14:15], v[92:93] op_sel_hi:[1,0,1]
	v_pk_fma_f32 v[84:85], v[190:191], s[14:15], v[84:85] op_sel_hi:[1,0,1]
	v_readlane_b32 s14, v1, 16
	v_cvt_pk_f32_fp8_e32 v[184:185], v60
	v_cvt_pk_f32_fp8_sdwa v[186:187], v60 src0_sel:WORD_1
	v_pk_fma_f32 v[78:79], v[184:185], s[14:15], v[78:79] op_sel_hi:[1,0,1]
	v_pk_fma_f32 v[80:81], v[186:187], s[14:15], v[80:81] op_sel_hi:[1,0,1]
	v_cvt_pk_f32_fp8_e32 v[188:189], v61
	v_cvt_pk_f32_fp8_sdwa v[190:191], v61 src0_sel:WORD_1
	v_pk_fma_f32 v[82:83], v[188:189], s[14:15], v[82:83] op_sel_hi:[1,0,1]
	v_pk_fma_f32 v[86:87], v[190:191], s[14:15], v[86:87] op_sel_hi:[1,0,1]
	v_cvt_pk_f32_fp8_e32 v[184:185], v62
	v_cvt_pk_f32_fp8_sdwa v[186:187], v62 src0_sel:WORD_1
	v_pk_fma_f32 v[88:89], v[184:185], s[14:15], v[88:89] op_sel_hi:[1,0,1]
	v_pk_fma_f32 v[90:91], v[186:187], s[14:15], v[90:91] op_sel_hi:[1,0,1]
	v_cvt_pk_f32_fp8_e32 v[188:189], v63
	v_cvt_pk_f32_fp8_sdwa v[190:191], v63 src0_sel:WORD_1
	v_pk_fma_f32 v[92:93], v[188:189], s[14:15], v[92:93] op_sel_hi:[1,0,1]
	v_pk_fma_f32 v[84:85], v[190:191], s[14:15], v[84:85] op_sel_hi:[1,0,1]
	v_readlane_b32 s14, v1, 24
	v_cvt_pk_f32_fp8_e32 v[184:185], v56
	v_cvt_pk_f32_fp8_sdwa v[186:187], v56 src0_sel:WORD_1
	v_pk_fma_f32 v[78:79], v[184:185], s[14:15], v[78:79] op_sel_hi:[1,0,1]
	v_pk_fma_f32 v[80:81], v[186:187], s[14:15], v[80:81] op_sel_hi:[1,0,1]
	v_cvt_pk_f32_fp8_e32 v[188:189], v57
	v_cvt_pk_f32_fp8_sdwa v[190:191], v57 src0_sel:WORD_1
	v_pk_fma_f32 v[82:83], v[188:189], s[14:15], v[82:83] op_sel_hi:[1,0,1]
	v_pk_fma_f32 v[86:87], v[190:191], s[14:15], v[86:87] op_sel_hi:[1,0,1]
	v_cvt_pk_f32_fp8_e32 v[184:185], v58
	v_cvt_pk_f32_fp8_sdwa v[186:187], v58 src0_sel:WORD_1
	v_pk_fma_f32 v[88:89], v[184:185], s[14:15], v[88:89] op_sel_hi:[1,0,1]
	v_pk_fma_f32 v[90:91], v[186:187], s[14:15], v[90:91] op_sel_hi:[1,0,1]
	v_cvt_pk_f32_fp8_e32 v[188:189], v59
	v_cvt_pk_f32_fp8_sdwa v[190:191], v59 src0_sel:WORD_1
	v_pk_fma_f32 v[92:93], v[188:189], s[14:15], v[92:93] op_sel_hi:[1,0,1]
	v_pk_fma_f32 v[84:85], v[190:191], s[14:15], v[84:85] op_sel_hi:[1,0,1]
	v_readlane_b32 s14, v1, 32
	v_cvt_pk_f32_fp8_e32 v[184:185], v48
	v_cvt_pk_f32_fp8_sdwa v[186:187], v48 src0_sel:WORD_1
	v_pk_fma_f32 v[78:79], v[184:185], s[14:15], v[78:79] op_sel_hi:[1,0,1]
	v_pk_fma_f32 v[80:81], v[186:187], s[14:15], v[80:81] op_sel_hi:[1,0,1]
	v_cvt_pk_f32_fp8_e32 v[188:189], v49
	v_cvt_pk_f32_fp8_sdwa v[190:191], v49 src0_sel:WORD_1
	v_pk_fma_f32 v[82:83], v[188:189], s[14:15], v[82:83] op_sel_hi:[1,0,1]
	v_pk_fma_f32 v[86:87], v[190:191], s[14:15], v[86:87] op_sel_hi:[1,0,1]
	v_cvt_pk_f32_fp8_e32 v[184:185], v50
	v_cvt_pk_f32_fp8_sdwa v[186:187], v50 src0_sel:WORD_1
	v_pk_fma_f32 v[88:89], v[184:185], s[14:15], v[88:89] op_sel_hi:[1,0,1]
	v_pk_fma_f32 v[90:91], v[186:187], s[14:15], v[90:91] op_sel_hi:[1,0,1]
	v_cvt_pk_f32_fp8_e32 v[188:189], v51
	v_cvt_pk_f32_fp8_sdwa v[190:191], v51 src0_sel:WORD_1
	v_pk_fma_f32 v[92:93], v[188:189], s[14:15], v[92:93] op_sel_hi:[1,0,1]
	v_pk_fma_f32 v[84:85], v[190:191], s[14:15], v[84:85] op_sel_hi:[1,0,1]
	v_readlane_b32 s14, v1, 40
	v_cvt_pk_f32_fp8_e32 v[184:185], v32
	v_cvt_pk_f32_fp8_sdwa v[186:187], v32 src0_sel:WORD_1
	v_pk_fma_f32 v[78:79], v[184:185], s[14:15], v[78:79] op_sel_hi:[1,0,1]
	v_pk_fma_f32 v[80:81], v[186:187], s[14:15], v[80:81] op_sel_hi:[1,0,1]
	v_cvt_pk_f32_fp8_e32 v[188:189], v33
	v_cvt_pk_f32_fp8_sdwa v[190:191], v33 src0_sel:WORD_1
	v_pk_fma_f32 v[82:83], v[188:189], s[14:15], v[82:83] op_sel_hi:[1,0,1]
	v_pk_fma_f32 v[86:87], v[190:191], s[14:15], v[86:87] op_sel_hi:[1,0,1]
	v_cvt_pk_f32_fp8_e32 v[184:185], v34
	v_cvt_pk_f32_fp8_sdwa v[186:187], v34 src0_sel:WORD_1
	v_pk_fma_f32 v[88:89], v[184:185], s[14:15], v[88:89] op_sel_hi:[1,0,1]
	v_pk_fma_f32 v[90:91], v[186:187], s[14:15], v[90:91] op_sel_hi:[1,0,1]
	v_cvt_pk_f32_fp8_e32 v[188:189], v35
	v_cvt_pk_f32_fp8_sdwa v[190:191], v35 src0_sel:WORD_1
	v_pk_fma_f32 v[92:93], v[188:189], s[14:15], v[92:93] op_sel_hi:[1,0,1]
	v_pk_fma_f32 v[84:85], v[190:191], s[14:15], v[84:85] op_sel_hi:[1,0,1]
	v_readlane_b32 s14, v1, 48
	v_cvt_pk_f32_fp8_e32 v[184:185], v16
	v_cvt_pk_f32_fp8_sdwa v[186:187], v16 src0_sel:WORD_1
	v_pk_fma_f32 v[78:79], v[184:185], s[14:15], v[78:79] op_sel_hi:[1,0,1]
	v_pk_fma_f32 v[80:81], v[186:187], s[14:15], v[80:81] op_sel_hi:[1,0,1]
	v_cvt_pk_f32_fp8_e32 v[188:189], v17
	v_cvt_pk_f32_fp8_sdwa v[190:191], v17 src0_sel:WORD_1
	v_pk_fma_f32 v[82:83], v[188:189], s[14:15], v[82:83] op_sel_hi:[1,0,1]
	v_pk_fma_f32 v[86:87], v[190:191], s[14:15], v[86:87] op_sel_hi:[1,0,1]
	v_cvt_pk_f32_fp8_e32 v[184:185], v18
	v_cvt_pk_f32_fp8_sdwa v[186:187], v18 src0_sel:WORD_1
	v_pk_fma_f32 v[88:89], v[184:185], s[14:15], v[88:89] op_sel_hi:[1,0,1]
	v_pk_fma_f32 v[90:91], v[186:187], s[14:15], v[90:91] op_sel_hi:[1,0,1]
	v_cvt_pk_f32_fp8_e32 v[188:189], v19
	v_cvt_pk_f32_fp8_sdwa v[190:191], v19 src0_sel:WORD_1
	v_pk_fma_f32 v[92:93], v[188:189], s[14:15], v[92:93] op_sel_hi:[1,0,1]
	v_pk_fma_f32 v[84:85], v[190:191], s[14:15], v[84:85] op_sel_hi:[1,0,1]
	v_readlane_b32 s14, v1, 56
	v_cvt_pk_f32_fp8_e32 v[184:185], v12
	v_cvt_pk_f32_fp8_sdwa v[186:187], v12 src0_sel:WORD_1
	v_pk_fma_f32 v[78:79], v[184:185], s[14:15], v[78:79] op_sel_hi:[1,0,1]
	v_pk_fma_f32 v[80:81], v[186:187], s[14:15], v[80:81] op_sel_hi:[1,0,1]
	v_cvt_pk_f32_fp8_e32 v[188:189], v13
	v_cvt_pk_f32_fp8_sdwa v[190:191], v13 src0_sel:WORD_1
	v_pk_fma_f32 v[82:83], v[188:189], s[14:15], v[82:83] op_sel_hi:[1,0,1]
	v_pk_fma_f32 v[86:87], v[190:191], s[14:15], v[86:87] op_sel_hi:[1,0,1]
	v_cvt_pk_f32_fp8_e32 v[184:185], v14
	v_cvt_pk_f32_fp8_sdwa v[186:187], v14 src0_sel:WORD_1
	v_pk_fma_f32 v[88:89], v[184:185], s[14:15], v[88:89] op_sel_hi:[1,0,1]
	v_pk_fma_f32 v[90:91], v[186:187], s[14:15], v[90:91] op_sel_hi:[1,0,1]
	v_cvt_pk_f32_fp8_e32 v[188:189], v15
	v_cvt_pk_f32_fp8_sdwa v[190:191], v15 src0_sel:WORD_1
	v_pk_fma_f32 v[92:93], v[188:189], s[14:15], v[92:93] op_sel_hi:[1,0,1]
	v_pk_fma_f32 v[84:85], v[190:191], s[14:15], v[84:85] op_sel_hi:[1,0,1]
	s_branch .Lp6c0_axdone
.Lp6c0_t4:
	v_readlane_b32 s14, v1, 0
	v_cvt_pk_f32_fp8_e32 v[184:185], v68
	v_cvt_pk_f32_fp8_sdwa v[186:187], v68 src0_sel:WORD_1
	v_pk_fma_f32 v[144:145], v[184:185], s[14:15], v[144:145] op_sel_hi:[1,0,1]
	v_pk_fma_f32 v[146:147], v[186:187], s[14:15], v[146:147] op_sel_hi:[1,0,1]
	v_cvt_pk_f32_fp8_e32 v[188:189], v69
	v_cvt_pk_f32_fp8_sdwa v[190:191], v69 src0_sel:WORD_1
	v_pk_fma_f32 v[148:149], v[188:189], s[14:15], v[148:149] op_sel_hi:[1,0,1]
	v_pk_fma_f32 v[150:151], v[190:191], s[14:15], v[150:151] op_sel_hi:[1,0,1]
	v_cvt_pk_f32_fp8_e32 v[184:185], v70
	v_cvt_pk_f32_fp8_sdwa v[186:187], v70 src0_sel:WORD_1
	v_pk_fma_f32 v[152:153], v[184:185], s[14:15], v[152:153] op_sel_hi:[1,0,1]
	v_pk_fma_f32 v[154:155], v[186:187], s[14:15], v[154:155] op_sel_hi:[1,0,1]
	v_cvt_pk_f32_fp8_e32 v[188:189], v71
	v_cvt_pk_f32_fp8_sdwa v[190:191], v71 src0_sel:WORD_1
	v_pk_fma_f32 v[156:157], v[188:189], s[14:15], v[156:157] op_sel_hi:[1,0,1]
	v_pk_fma_f32 v[158:159], v[190:191], s[14:15], v[158:159] op_sel_hi:[1,0,1]
	v_readlane_b32 s14, v1, 8
	v_cvt_pk_f32_fp8_e32 v[184:185], v64
	v_cvt_pk_f32_fp8_sdwa v[186:187], v64 src0_sel:WORD_1
	v_pk_fma_f32 v[144:145], v[184:185], s[14:15], v[144:145] op_sel_hi:[1,0,1]
	v_pk_fma_f32 v[146:147], v[186:187], s[14:15], v[146:147] op_sel_hi:[1,0,1]
	v_cvt_pk_f32_fp8_e32 v[188:189], v65
	v_cvt_pk_f32_fp8_sdwa v[190:191], v65 src0_sel:WORD_1
	v_pk_fma_f32 v[148:149], v[188:189], s[14:15], v[148:149] op_sel_hi:[1,0,1]
	v_pk_fma_f32 v[150:151], v[190:191], s[14:15], v[150:151] op_sel_hi:[1,0,1]
	v_cvt_pk_f32_fp8_e32 v[184:185], v66
	v_cvt_pk_f32_fp8_sdwa v[186:187], v66 src0_sel:WORD_1
	v_pk_fma_f32 v[152:153], v[184:185], s[14:15], v[152:153] op_sel_hi:[1,0,1]
	v_pk_fma_f32 v[154:155], v[186:187], s[14:15], v[154:155] op_sel_hi:[1,0,1]
	v_cvt_pk_f32_fp8_e32 v[188:189], v67
	v_cvt_pk_f32_fp8_sdwa v[190:191], v67 src0_sel:WORD_1
	v_pk_fma_f32 v[156:157], v[188:189], s[14:15], v[156:157] op_sel_hi:[1,0,1]
	v_pk_fma_f32 v[158:159], v[190:191], s[14:15], v[158:159] op_sel_hi:[1,0,1]
	v_readlane_b32 s14, v1, 16
	v_cvt_pk_f32_fp8_e32 v[184:185], v60
	v_cvt_pk_f32_fp8_sdwa v[186:187], v60 src0_sel:WORD_1
	v_pk_fma_f32 v[144:145], v[184:185], s[14:15], v[144:145] op_sel_hi:[1,0,1]
	v_pk_fma_f32 v[146:147], v[186:187], s[14:15], v[146:147] op_sel_hi:[1,0,1]
	v_cvt_pk_f32_fp8_e32 v[188:189], v61
	v_cvt_pk_f32_fp8_sdwa v[190:191], v61 src0_sel:WORD_1
	v_pk_fma_f32 v[148:149], v[188:189], s[14:15], v[148:149] op_sel_hi:[1,0,1]
	v_pk_fma_f32 v[150:151], v[190:191], s[14:15], v[150:151] op_sel_hi:[1,0,1]
	v_cvt_pk_f32_fp8_e32 v[184:185], v62
	v_cvt_pk_f32_fp8_sdwa v[186:187], v62 src0_sel:WORD_1
	v_pk_fma_f32 v[152:153], v[184:185], s[14:15], v[152:153] op_sel_hi:[1,0,1]
	v_pk_fma_f32 v[154:155], v[186:187], s[14:15], v[154:155] op_sel_hi:[1,0,1]
	v_cvt_pk_f32_fp8_e32 v[188:189], v63
	v_cvt_pk_f32_fp8_sdwa v[190:191], v63 src0_sel:WORD_1
	v_pk_fma_f32 v[156:157], v[188:189], s[14:15], v[156:157] op_sel_hi:[1,0,1]
	v_pk_fma_f32 v[158:159], v[190:191], s[14:15], v[158:159] op_sel_hi:[1,0,1]
	v_readlane_b32 s14, v1, 24
	v_cvt_pk_f32_fp8_e32 v[184:185], v56
	v_cvt_pk_f32_fp8_sdwa v[186:187], v56 src0_sel:WORD_1
	v_pk_fma_f32 v[144:145], v[184:185], s[14:15], v[144:145] op_sel_hi:[1,0,1]
	v_pk_fma_f32 v[146:147], v[186:187], s[14:15], v[146:147] op_sel_hi:[1,0,1]
	v_cvt_pk_f32_fp8_e32 v[188:189], v57
	v_cvt_pk_f32_fp8_sdwa v[190:191], v57 src0_sel:WORD_1
	v_pk_fma_f32 v[148:149], v[188:189], s[14:15], v[148:149] op_sel_hi:[1,0,1]
	v_pk_fma_f32 v[150:151], v[190:191], s[14:15], v[150:151] op_sel_hi:[1,0,1]
	v_cvt_pk_f32_fp8_e32 v[184:185], v58
	v_cvt_pk_f32_fp8_sdwa v[186:187], v58 src0_sel:WORD_1
	v_pk_fma_f32 v[152:153], v[184:185], s[14:15], v[152:153] op_sel_hi:[1,0,1]
	v_pk_fma_f32 v[154:155], v[186:187], s[14:15], v[154:155] op_sel_hi:[1,0,1]
	v_cvt_pk_f32_fp8_e32 v[188:189], v59
	v_cvt_pk_f32_fp8_sdwa v[190:191], v59 src0_sel:WORD_1
	v_pk_fma_f32 v[156:157], v[188:189], s[14:15], v[156:157] op_sel_hi:[1,0,1]
	v_pk_fma_f32 v[158:159], v[190:191], s[14:15], v[158:159] op_sel_hi:[1,0,1]
	v_readlane_b32 s14, v1, 32
	v_cvt_pk_f32_fp8_e32 v[184:185], v48
	v_cvt_pk_f32_fp8_sdwa v[186:187], v48 src0_sel:WORD_1
	v_pk_fma_f32 v[144:145], v[184:185], s[14:15], v[144:145] op_sel_hi:[1,0,1]
	v_pk_fma_f32 v[146:147], v[186:187], s[14:15], v[146:147] op_sel_hi:[1,0,1]
	v_cvt_pk_f32_fp8_e32 v[188:189], v49
	v_cvt_pk_f32_fp8_sdwa v[190:191], v49 src0_sel:WORD_1
	v_pk_fma_f32 v[148:149], v[188:189], s[14:15], v[148:149] op_sel_hi:[1,0,1]
	v_pk_fma_f32 v[150:151], v[190:191], s[14:15], v[150:151] op_sel_hi:[1,0,1]
	v_cvt_pk_f32_fp8_e32 v[184:185], v50
	v_cvt_pk_f32_fp8_sdwa v[186:187], v50 src0_sel:WORD_1
	v_pk_fma_f32 v[152:153], v[184:185], s[14:15], v[152:153] op_sel_hi:[1,0,1]
	v_pk_fma_f32 v[154:155], v[186:187], s[14:15], v[154:155] op_sel_hi:[1,0,1]
	v_cvt_pk_f32_fp8_e32 v[188:189], v51
	v_cvt_pk_f32_fp8_sdwa v[190:191], v51 src0_sel:WORD_1
	v_pk_fma_f32 v[156:157], v[188:189], s[14:15], v[156:157] op_sel_hi:[1,0,1]
	v_pk_fma_f32 v[158:159], v[190:191], s[14:15], v[158:159] op_sel_hi:[1,0,1]
	v_readlane_b32 s14, v1, 40
	v_cvt_pk_f32_fp8_e32 v[184:185], v32
	v_cvt_pk_f32_fp8_sdwa v[186:187], v32 src0_sel:WORD_1
	v_pk_fma_f32 v[144:145], v[184:185], s[14:15], v[144:145] op_sel_hi:[1,0,1]
	v_pk_fma_f32 v[146:147], v[186:187], s[14:15], v[146:147] op_sel_hi:[1,0,1]
	v_cvt_pk_f32_fp8_e32 v[188:189], v33
	v_cvt_pk_f32_fp8_sdwa v[190:191], v33 src0_sel:WORD_1
	v_pk_fma_f32 v[148:149], v[188:189], s[14:15], v[148:149] op_sel_hi:[1,0,1]
	v_pk_fma_f32 v[150:151], v[190:191], s[14:15], v[150:151] op_sel_hi:[1,0,1]
	v_cvt_pk_f32_fp8_e32 v[184:185], v34
	v_cvt_pk_f32_fp8_sdwa v[186:187], v34 src0_sel:WORD_1
	v_pk_fma_f32 v[152:153], v[184:185], s[14:15], v[152:153] op_sel_hi:[1,0,1]
	v_pk_fma_f32 v[154:155], v[186:187], s[14:15], v[154:155] op_sel_hi:[1,0,1]
	v_cvt_pk_f32_fp8_e32 v[188:189], v35
	v_cvt_pk_f32_fp8_sdwa v[190:191], v35 src0_sel:WORD_1
	v_pk_fma_f32 v[156:157], v[188:189], s[14:15], v[156:157] op_sel_hi:[1,0,1]
	v_pk_fma_f32 v[158:159], v[190:191], s[14:15], v[158:159] op_sel_hi:[1,0,1]
	v_readlane_b32 s14, v1, 48
	v_cvt_pk_f32_fp8_e32 v[184:185], v16
	v_cvt_pk_f32_fp8_sdwa v[186:187], v16 src0_sel:WORD_1
	v_pk_fma_f32 v[144:145], v[184:185], s[14:15], v[144:145] op_sel_hi:[1,0,1]
	v_pk_fma_f32 v[146:147], v[186:187], s[14:15], v[146:147] op_sel_hi:[1,0,1]
	v_cvt_pk_f32_fp8_e32 v[188:189], v17
	v_cvt_pk_f32_fp8_sdwa v[190:191], v17 src0_sel:WORD_1
	v_pk_fma_f32 v[148:149], v[188:189], s[14:15], v[148:149] op_sel_hi:[1,0,1]
	v_pk_fma_f32 v[150:151], v[190:191], s[14:15], v[150:151] op_sel_hi:[1,0,1]
	v_cvt_pk_f32_fp8_e32 v[184:185], v18
	v_cvt_pk_f32_fp8_sdwa v[186:187], v18 src0_sel:WORD_1
	v_pk_fma_f32 v[152:153], v[184:185], s[14:15], v[152:153] op_sel_hi:[1,0,1]
	v_pk_fma_f32 v[154:155], v[186:187], s[14:15], v[154:155] op_sel_hi:[1,0,1]
	v_cvt_pk_f32_fp8_e32 v[188:189], v19
	v_cvt_pk_f32_fp8_sdwa v[190:191], v19 src0_sel:WORD_1
	v_pk_fma_f32 v[156:157], v[188:189], s[14:15], v[156:157] op_sel_hi:[1,0,1]
	v_pk_fma_f32 v[158:159], v[190:191], s[14:15], v[158:159] op_sel_hi:[1,0,1]
	v_readlane_b32 s14, v1, 56
	v_cvt_pk_f32_fp8_e32 v[184:185], v12
	v_cvt_pk_f32_fp8_sdwa v[186:187], v12 src0_sel:WORD_1
	v_pk_fma_f32 v[144:145], v[184:185], s[14:15], v[144:145] op_sel_hi:[1,0,1]
	v_pk_fma_f32 v[146:147], v[186:187], s[14:15], v[146:147] op_sel_hi:[1,0,1]
	v_cvt_pk_f32_fp8_e32 v[188:189], v13
	v_cvt_pk_f32_fp8_sdwa v[190:191], v13 src0_sel:WORD_1
	v_pk_fma_f32 v[148:149], v[188:189], s[14:15], v[148:149] op_sel_hi:[1,0,1]
	v_pk_fma_f32 v[150:151], v[190:191], s[14:15], v[150:151] op_sel_hi:[1,0,1]
	v_cvt_pk_f32_fp8_e32 v[184:185], v14
	v_cvt_pk_f32_fp8_sdwa v[186:187], v14 src0_sel:WORD_1
	v_pk_fma_f32 v[152:153], v[184:185], s[14:15], v[152:153] op_sel_hi:[1,0,1]
	v_pk_fma_f32 v[154:155], v[186:187], s[14:15], v[154:155] op_sel_hi:[1,0,1]
	v_cvt_pk_f32_fp8_e32 v[188:189], v15
	v_cvt_pk_f32_fp8_sdwa v[190:191], v15 src0_sel:WORD_1
	v_pk_fma_f32 v[156:157], v[188:189], s[14:15], v[156:157] op_sel_hi:[1,0,1]
	v_pk_fma_f32 v[158:159], v[190:191], s[14:15], v[158:159] op_sel_hi:[1,0,1]
	s_branch .Lp6c0_axdone
.Lp6c0_t5:
	v_readlane_b32 s14, v1, 0
	v_cvt_pk_f32_fp8_e32 v[184:185], v68
	v_cvt_pk_f32_fp8_sdwa v[186:187], v68 src0_sel:WORD_1
	v_pk_fma_f32 v[160:161], v[184:185], s[14:15], v[160:161] op_sel_hi:[1,0,1]
	v_pk_fma_f32 v[162:163], v[186:187], s[14:15], v[162:163] op_sel_hi:[1,0,1]
	v_cvt_pk_f32_fp8_e32 v[188:189], v69
	v_cvt_pk_f32_fp8_sdwa v[190:191], v69 src0_sel:WORD_1
	v_pk_fma_f32 v[164:165], v[188:189], s[14:15], v[164:165] op_sel_hi:[1,0,1]
	v_pk_fma_f32 v[166:167], v[190:191], s[14:15], v[166:167] op_sel_hi:[1,0,1]
	v_cvt_pk_f32_fp8_e32 v[184:185], v70
	v_cvt_pk_f32_fp8_sdwa v[186:187], v70 src0_sel:WORD_1
	v_pk_fma_f32 v[168:169], v[184:185], s[14:15], v[168:169] op_sel_hi:[1,0,1]
	v_pk_fma_f32 v[170:171], v[186:187], s[14:15], v[170:171] op_sel_hi:[1,0,1]
	v_cvt_pk_f32_fp8_e32 v[188:189], v71
	v_cvt_pk_f32_fp8_sdwa v[190:191], v71 src0_sel:WORD_1
	v_pk_fma_f32 v[172:173], v[188:189], s[14:15], v[172:173] op_sel_hi:[1,0,1]
	v_pk_fma_f32 v[174:175], v[190:191], s[14:15], v[174:175] op_sel_hi:[1,0,1]
	v_readlane_b32 s14, v1, 8
	v_cvt_pk_f32_fp8_e32 v[184:185], v64
	v_cvt_pk_f32_fp8_sdwa v[186:187], v64 src0_sel:WORD_1
	v_pk_fma_f32 v[160:161], v[184:185], s[14:15], v[160:161] op_sel_hi:[1,0,1]
	v_pk_fma_f32 v[162:163], v[186:187], s[14:15], v[162:163] op_sel_hi:[1,0,1]
	v_cvt_pk_f32_fp8_e32 v[188:189], v65
	v_cvt_pk_f32_fp8_sdwa v[190:191], v65 src0_sel:WORD_1
	v_pk_fma_f32 v[164:165], v[188:189], s[14:15], v[164:165] op_sel_hi:[1,0,1]
	v_pk_fma_f32 v[166:167], v[190:191], s[14:15], v[166:167] op_sel_hi:[1,0,1]
	v_cvt_pk_f32_fp8_e32 v[184:185], v66
	v_cvt_pk_f32_fp8_sdwa v[186:187], v66 src0_sel:WORD_1
	v_pk_fma_f32 v[168:169], v[184:185], s[14:15], v[168:169] op_sel_hi:[1,0,1]
	v_pk_fma_f32 v[170:171], v[186:187], s[14:15], v[170:171] op_sel_hi:[1,0,1]
	v_cvt_pk_f32_fp8_e32 v[188:189], v67
	v_cvt_pk_f32_fp8_sdwa v[190:191], v67 src0_sel:WORD_1
	v_pk_fma_f32 v[172:173], v[188:189], s[14:15], v[172:173] op_sel_hi:[1,0,1]
	v_pk_fma_f32 v[174:175], v[190:191], s[14:15], v[174:175] op_sel_hi:[1,0,1]
	v_readlane_b32 s14, v1, 16
	v_cvt_pk_f32_fp8_e32 v[184:185], v60
	v_cvt_pk_f32_fp8_sdwa v[186:187], v60 src0_sel:WORD_1
	v_pk_fma_f32 v[160:161], v[184:185], s[14:15], v[160:161] op_sel_hi:[1,0,1]
	v_pk_fma_f32 v[162:163], v[186:187], s[14:15], v[162:163] op_sel_hi:[1,0,1]
	v_cvt_pk_f32_fp8_e32 v[188:189], v61
	v_cvt_pk_f32_fp8_sdwa v[190:191], v61 src0_sel:WORD_1
	v_pk_fma_f32 v[164:165], v[188:189], s[14:15], v[164:165] op_sel_hi:[1,0,1]
	v_pk_fma_f32 v[166:167], v[190:191], s[14:15], v[166:167] op_sel_hi:[1,0,1]
	v_cvt_pk_f32_fp8_e32 v[184:185], v62
	v_cvt_pk_f32_fp8_sdwa v[186:187], v62 src0_sel:WORD_1
	v_pk_fma_f32 v[168:169], v[184:185], s[14:15], v[168:169] op_sel_hi:[1,0,1]
	v_pk_fma_f32 v[170:171], v[186:187], s[14:15], v[170:171] op_sel_hi:[1,0,1]
	v_cvt_pk_f32_fp8_e32 v[188:189], v63
	v_cvt_pk_f32_fp8_sdwa v[190:191], v63 src0_sel:WORD_1
	v_pk_fma_f32 v[172:173], v[188:189], s[14:15], v[172:173] op_sel_hi:[1,0,1]
	v_pk_fma_f32 v[174:175], v[190:191], s[14:15], v[174:175] op_sel_hi:[1,0,1]
	v_readlane_b32 s14, v1, 24
	v_cvt_pk_f32_fp8_e32 v[184:185], v56
	v_cvt_pk_f32_fp8_sdwa v[186:187], v56 src0_sel:WORD_1
	v_pk_fma_f32 v[160:161], v[184:185], s[14:15], v[160:161] op_sel_hi:[1,0,1]
	v_pk_fma_f32 v[162:163], v[186:187], s[14:15], v[162:163] op_sel_hi:[1,0,1]
	v_cvt_pk_f32_fp8_e32 v[188:189], v57
	v_cvt_pk_f32_fp8_sdwa v[190:191], v57 src0_sel:WORD_1
	v_pk_fma_f32 v[164:165], v[188:189], s[14:15], v[164:165] op_sel_hi:[1,0,1]
	v_pk_fma_f32 v[166:167], v[190:191], s[14:15], v[166:167] op_sel_hi:[1,0,1]
	v_cvt_pk_f32_fp8_e32 v[184:185], v58
	v_cvt_pk_f32_fp8_sdwa v[186:187], v58 src0_sel:WORD_1
	v_pk_fma_f32 v[168:169], v[184:185], s[14:15], v[168:169] op_sel_hi:[1,0,1]
	v_pk_fma_f32 v[170:171], v[186:187], s[14:15], v[170:171] op_sel_hi:[1,0,1]
	v_cvt_pk_f32_fp8_e32 v[188:189], v59
	v_cvt_pk_f32_fp8_sdwa v[190:191], v59 src0_sel:WORD_1
	v_pk_fma_f32 v[172:173], v[188:189], s[14:15], v[172:173] op_sel_hi:[1,0,1]
	v_pk_fma_f32 v[174:175], v[190:191], s[14:15], v[174:175] op_sel_hi:[1,0,1]
	v_readlane_b32 s14, v1, 32
	v_cvt_pk_f32_fp8_e32 v[184:185], v48
	v_cvt_pk_f32_fp8_sdwa v[186:187], v48 src0_sel:WORD_1
	v_pk_fma_f32 v[160:161], v[184:185], s[14:15], v[160:161] op_sel_hi:[1,0,1]
	v_pk_fma_f32 v[162:163], v[186:187], s[14:15], v[162:163] op_sel_hi:[1,0,1]
	v_cvt_pk_f32_fp8_e32 v[188:189], v49
	v_cvt_pk_f32_fp8_sdwa v[190:191], v49 src0_sel:WORD_1
	v_pk_fma_f32 v[164:165], v[188:189], s[14:15], v[164:165] op_sel_hi:[1,0,1]
	v_pk_fma_f32 v[166:167], v[190:191], s[14:15], v[166:167] op_sel_hi:[1,0,1]
	v_cvt_pk_f32_fp8_e32 v[184:185], v50
	v_cvt_pk_f32_fp8_sdwa v[186:187], v50 src0_sel:WORD_1
	v_pk_fma_f32 v[168:169], v[184:185], s[14:15], v[168:169] op_sel_hi:[1,0,1]
	v_pk_fma_f32 v[170:171], v[186:187], s[14:15], v[170:171] op_sel_hi:[1,0,1]
	v_cvt_pk_f32_fp8_e32 v[188:189], v51
	v_cvt_pk_f32_fp8_sdwa v[190:191], v51 src0_sel:WORD_1
	v_pk_fma_f32 v[172:173], v[188:189], s[14:15], v[172:173] op_sel_hi:[1,0,1]
	v_pk_fma_f32 v[174:175], v[190:191], s[14:15], v[174:175] op_sel_hi:[1,0,1]
	v_readlane_b32 s14, v1, 40
	v_cvt_pk_f32_fp8_e32 v[184:185], v32
	v_cvt_pk_f32_fp8_sdwa v[186:187], v32 src0_sel:WORD_1
	v_pk_fma_f32 v[160:161], v[184:185], s[14:15], v[160:161] op_sel_hi:[1,0,1]
	v_pk_fma_f32 v[162:163], v[186:187], s[14:15], v[162:163] op_sel_hi:[1,0,1]
	v_cvt_pk_f32_fp8_e32 v[188:189], v33
	v_cvt_pk_f32_fp8_sdwa v[190:191], v33 src0_sel:WORD_1
	v_pk_fma_f32 v[164:165], v[188:189], s[14:15], v[164:165] op_sel_hi:[1,0,1]
	v_pk_fma_f32 v[166:167], v[190:191], s[14:15], v[166:167] op_sel_hi:[1,0,1]
	v_cvt_pk_f32_fp8_e32 v[184:185], v34
	v_cvt_pk_f32_fp8_sdwa v[186:187], v34 src0_sel:WORD_1
	v_pk_fma_f32 v[168:169], v[184:185], s[14:15], v[168:169] op_sel_hi:[1,0,1]
	v_pk_fma_f32 v[170:171], v[186:187], s[14:15], v[170:171] op_sel_hi:[1,0,1]
	v_cvt_pk_f32_fp8_e32 v[188:189], v35
	v_cvt_pk_f32_fp8_sdwa v[190:191], v35 src0_sel:WORD_1
	v_pk_fma_f32 v[172:173], v[188:189], s[14:15], v[172:173] op_sel_hi:[1,0,1]
	v_pk_fma_f32 v[174:175], v[190:191], s[14:15], v[174:175] op_sel_hi:[1,0,1]
	v_readlane_b32 s14, v1, 48
	v_cvt_pk_f32_fp8_e32 v[184:185], v16
	v_cvt_pk_f32_fp8_sdwa v[186:187], v16 src0_sel:WORD_1
	v_pk_fma_f32 v[160:161], v[184:185], s[14:15], v[160:161] op_sel_hi:[1,0,1]
	v_pk_fma_f32 v[162:163], v[186:187], s[14:15], v[162:163] op_sel_hi:[1,0,1]
	v_cvt_pk_f32_fp8_e32 v[188:189], v17
	v_cvt_pk_f32_fp8_sdwa v[190:191], v17 src0_sel:WORD_1
	v_pk_fma_f32 v[164:165], v[188:189], s[14:15], v[164:165] op_sel_hi:[1,0,1]
	v_pk_fma_f32 v[166:167], v[190:191], s[14:15], v[166:167] op_sel_hi:[1,0,1]
	v_cvt_pk_f32_fp8_e32 v[184:185], v18
	v_cvt_pk_f32_fp8_sdwa v[186:187], v18 src0_sel:WORD_1
	v_pk_fma_f32 v[168:169], v[184:185], s[14:15], v[168:169] op_sel_hi:[1,0,1]
	v_pk_fma_f32 v[170:171], v[186:187], s[14:15], v[170:171] op_sel_hi:[1,0,1]
	v_cvt_pk_f32_fp8_e32 v[188:189], v19
	v_cvt_pk_f32_fp8_sdwa v[190:191], v19 src0_sel:WORD_1
	v_pk_fma_f32 v[172:173], v[188:189], s[14:15], v[172:173] op_sel_hi:[1,0,1]
	v_pk_fma_f32 v[174:175], v[190:191], s[14:15], v[174:175] op_sel_hi:[1,0,1]
	v_readlane_b32 s14, v1, 56
	v_cvt_pk_f32_fp8_e32 v[184:185], v12
	v_cvt_pk_f32_fp8_sdwa v[186:187], v12 src0_sel:WORD_1
	v_pk_fma_f32 v[160:161], v[184:185], s[14:15], v[160:161] op_sel_hi:[1,0,1]
	v_pk_fma_f32 v[162:163], v[186:187], s[14:15], v[162:163] op_sel_hi:[1,0,1]
	v_cvt_pk_f32_fp8_e32 v[188:189], v13
	v_cvt_pk_f32_fp8_sdwa v[190:191], v13 src0_sel:WORD_1
	v_pk_fma_f32 v[164:165], v[188:189], s[14:15], v[164:165] op_sel_hi:[1,0,1]
	v_pk_fma_f32 v[166:167], v[190:191], s[14:15], v[166:167] op_sel_hi:[1,0,1]
	v_cvt_pk_f32_fp8_e32 v[184:185], v14
	v_cvt_pk_f32_fp8_sdwa v[186:187], v14 src0_sel:WORD_1
	v_pk_fma_f32 v[168:169], v[184:185], s[14:15], v[168:169] op_sel_hi:[1,0,1]
	v_pk_fma_f32 v[170:171], v[186:187], s[14:15], v[170:171] op_sel_hi:[1,0,1]
	v_cvt_pk_f32_fp8_e32 v[188:189], v15
	v_cvt_pk_f32_fp8_sdwa v[190:191], v15 src0_sel:WORD_1
	v_pk_fma_f32 v[172:173], v[188:189], s[14:15], v[172:173] op_sel_hi:[1,0,1]
	v_pk_fma_f32 v[174:175], v[190:191], s[14:15], v[174:175] op_sel_hi:[1,0,1]
	s_branch .Lp6c0_axdone
.Lp6c0_t6:
	v_readlane_b32 s14, v1, 0
	v_cvt_pk_f32_fp8_e32 v[184:185], v68
	v_cvt_pk_f32_fp8_sdwa v[186:187], v68 src0_sel:WORD_1
	v_pk_fma_f32 v[224:225], v[184:185], s[14:15], v[224:225] op_sel_hi:[1,0,1]
	v_pk_fma_f32 v[226:227], v[186:187], s[14:15], v[226:227] op_sel_hi:[1,0,1]
	v_cvt_pk_f32_fp8_e32 v[188:189], v69
	v_cvt_pk_f32_fp8_sdwa v[190:191], v69 src0_sel:WORD_1
	v_pk_fma_f32 v[228:229], v[188:189], s[14:15], v[228:229] op_sel_hi:[1,0,1]
	v_pk_fma_f32 v[230:231], v[190:191], s[14:15], v[230:231] op_sel_hi:[1,0,1]
	v_cvt_pk_f32_fp8_e32 v[184:185], v70
	v_cvt_pk_f32_fp8_sdwa v[186:187], v70 src0_sel:WORD_1
	v_pk_fma_f32 v[232:233], v[184:185], s[14:15], v[232:233] op_sel_hi:[1,0,1]
	v_pk_fma_f32 v[234:235], v[186:187], s[14:15], v[234:235] op_sel_hi:[1,0,1]
	v_cvt_pk_f32_fp8_e32 v[188:189], v71
	v_cvt_pk_f32_fp8_sdwa v[190:191], v71 src0_sel:WORD_1
	v_pk_fma_f32 v[236:237], v[188:189], s[14:15], v[236:237] op_sel_hi:[1,0,1]
	v_pk_fma_f32 v[238:239], v[190:191], s[14:15], v[238:239] op_sel_hi:[1,0,1]
	v_readlane_b32 s14, v1, 8
	v_cvt_pk_f32_fp8_e32 v[184:185], v64
	v_cvt_pk_f32_fp8_sdwa v[186:187], v64 src0_sel:WORD_1
	v_pk_fma_f32 v[224:225], v[184:185], s[14:15], v[224:225] op_sel_hi:[1,0,1]
	v_pk_fma_f32 v[226:227], v[186:187], s[14:15], v[226:227] op_sel_hi:[1,0,1]
	v_cvt_pk_f32_fp8_e32 v[188:189], v65
	v_cvt_pk_f32_fp8_sdwa v[190:191], v65 src0_sel:WORD_1
	v_pk_fma_f32 v[228:229], v[188:189], s[14:15], v[228:229] op_sel_hi:[1,0,1]
	v_pk_fma_f32 v[230:231], v[190:191], s[14:15], v[230:231] op_sel_hi:[1,0,1]
	v_cvt_pk_f32_fp8_e32 v[184:185], v66
	v_cvt_pk_f32_fp8_sdwa v[186:187], v66 src0_sel:WORD_1
	v_pk_fma_f32 v[232:233], v[184:185], s[14:15], v[232:233] op_sel_hi:[1,0,1]
	v_pk_fma_f32 v[234:235], v[186:187], s[14:15], v[234:235] op_sel_hi:[1,0,1]
	v_cvt_pk_f32_fp8_e32 v[188:189], v67
	v_cvt_pk_f32_fp8_sdwa v[190:191], v67 src0_sel:WORD_1
	v_pk_fma_f32 v[236:237], v[188:189], s[14:15], v[236:237] op_sel_hi:[1,0,1]
	v_pk_fma_f32 v[238:239], v[190:191], s[14:15], v[238:239] op_sel_hi:[1,0,1]
	v_readlane_b32 s14, v1, 16
	v_cvt_pk_f32_fp8_e32 v[184:185], v60
	v_cvt_pk_f32_fp8_sdwa v[186:187], v60 src0_sel:WORD_1
	v_pk_fma_f32 v[224:225], v[184:185], s[14:15], v[224:225] op_sel_hi:[1,0,1]
	v_pk_fma_f32 v[226:227], v[186:187], s[14:15], v[226:227] op_sel_hi:[1,0,1]
	v_cvt_pk_f32_fp8_e32 v[188:189], v61
	v_cvt_pk_f32_fp8_sdwa v[190:191], v61 src0_sel:WORD_1
	v_pk_fma_f32 v[228:229], v[188:189], s[14:15], v[228:229] op_sel_hi:[1,0,1]
	v_pk_fma_f32 v[230:231], v[190:191], s[14:15], v[230:231] op_sel_hi:[1,0,1]
	v_cvt_pk_f32_fp8_e32 v[184:185], v62
	v_cvt_pk_f32_fp8_sdwa v[186:187], v62 src0_sel:WORD_1
	v_pk_fma_f32 v[232:233], v[184:185], s[14:15], v[232:233] op_sel_hi:[1,0,1]
	v_pk_fma_f32 v[234:235], v[186:187], s[14:15], v[234:235] op_sel_hi:[1,0,1]
	v_cvt_pk_f32_fp8_e32 v[188:189], v63
	v_cvt_pk_f32_fp8_sdwa v[190:191], v63 src0_sel:WORD_1
	v_pk_fma_f32 v[236:237], v[188:189], s[14:15], v[236:237] op_sel_hi:[1,0,1]
	v_pk_fma_f32 v[238:239], v[190:191], s[14:15], v[238:239] op_sel_hi:[1,0,1]
	v_readlane_b32 s14, v1, 24
	v_cvt_pk_f32_fp8_e32 v[184:185], v56
	v_cvt_pk_f32_fp8_sdwa v[186:187], v56 src0_sel:WORD_1
	v_pk_fma_f32 v[224:225], v[184:185], s[14:15], v[224:225] op_sel_hi:[1,0,1]
	v_pk_fma_f32 v[226:227], v[186:187], s[14:15], v[226:227] op_sel_hi:[1,0,1]
	v_cvt_pk_f32_fp8_e32 v[188:189], v57
	v_cvt_pk_f32_fp8_sdwa v[190:191], v57 src0_sel:WORD_1
	v_pk_fma_f32 v[228:229], v[188:189], s[14:15], v[228:229] op_sel_hi:[1,0,1]
	v_pk_fma_f32 v[230:231], v[190:191], s[14:15], v[230:231] op_sel_hi:[1,0,1]
	v_cvt_pk_f32_fp8_e32 v[184:185], v58
	v_cvt_pk_f32_fp8_sdwa v[186:187], v58 src0_sel:WORD_1
	v_pk_fma_f32 v[232:233], v[184:185], s[14:15], v[232:233] op_sel_hi:[1,0,1]
	v_pk_fma_f32 v[234:235], v[186:187], s[14:15], v[234:235] op_sel_hi:[1,0,1]
	v_cvt_pk_f32_fp8_e32 v[188:189], v59
	v_cvt_pk_f32_fp8_sdwa v[190:191], v59 src0_sel:WORD_1
	v_pk_fma_f32 v[236:237], v[188:189], s[14:15], v[236:237] op_sel_hi:[1,0,1]
	v_pk_fma_f32 v[238:239], v[190:191], s[14:15], v[238:239] op_sel_hi:[1,0,1]
	v_readlane_b32 s14, v1, 32
	v_cvt_pk_f32_fp8_e32 v[184:185], v48
	v_cvt_pk_f32_fp8_sdwa v[186:187], v48 src0_sel:WORD_1
	v_pk_fma_f32 v[224:225], v[184:185], s[14:15], v[224:225] op_sel_hi:[1,0,1]
	v_pk_fma_f32 v[226:227], v[186:187], s[14:15], v[226:227] op_sel_hi:[1,0,1]
	v_cvt_pk_f32_fp8_e32 v[188:189], v49
	v_cvt_pk_f32_fp8_sdwa v[190:191], v49 src0_sel:WORD_1
	v_pk_fma_f32 v[228:229], v[188:189], s[14:15], v[228:229] op_sel_hi:[1,0,1]
	v_pk_fma_f32 v[230:231], v[190:191], s[14:15], v[230:231] op_sel_hi:[1,0,1]
	v_cvt_pk_f32_fp8_e32 v[184:185], v50
	v_cvt_pk_f32_fp8_sdwa v[186:187], v50 src0_sel:WORD_1
	v_pk_fma_f32 v[232:233], v[184:185], s[14:15], v[232:233] op_sel_hi:[1,0,1]
	v_pk_fma_f32 v[234:235], v[186:187], s[14:15], v[234:235] op_sel_hi:[1,0,1]
	v_cvt_pk_f32_fp8_e32 v[188:189], v51
	v_cvt_pk_f32_fp8_sdwa v[190:191], v51 src0_sel:WORD_1
	v_pk_fma_f32 v[236:237], v[188:189], s[14:15], v[236:237] op_sel_hi:[1,0,1]
	v_pk_fma_f32 v[238:239], v[190:191], s[14:15], v[238:239] op_sel_hi:[1,0,1]
	v_readlane_b32 s14, v1, 40
	v_cvt_pk_f32_fp8_e32 v[184:185], v32
	v_cvt_pk_f32_fp8_sdwa v[186:187], v32 src0_sel:WORD_1
	v_pk_fma_f32 v[224:225], v[184:185], s[14:15], v[224:225] op_sel_hi:[1,0,1]
	v_pk_fma_f32 v[226:227], v[186:187], s[14:15], v[226:227] op_sel_hi:[1,0,1]
	v_cvt_pk_f32_fp8_e32 v[188:189], v33
	v_cvt_pk_f32_fp8_sdwa v[190:191], v33 src0_sel:WORD_1
	v_pk_fma_f32 v[228:229], v[188:189], s[14:15], v[228:229] op_sel_hi:[1,0,1]
	v_pk_fma_f32 v[230:231], v[190:191], s[14:15], v[230:231] op_sel_hi:[1,0,1]
	v_cvt_pk_f32_fp8_e32 v[184:185], v34
	v_cvt_pk_f32_fp8_sdwa v[186:187], v34 src0_sel:WORD_1
	v_pk_fma_f32 v[232:233], v[184:185], s[14:15], v[232:233] op_sel_hi:[1,0,1]
	v_pk_fma_f32 v[234:235], v[186:187], s[14:15], v[234:235] op_sel_hi:[1,0,1]
	v_cvt_pk_f32_fp8_e32 v[188:189], v35
	v_cvt_pk_f32_fp8_sdwa v[190:191], v35 src0_sel:WORD_1
	v_pk_fma_f32 v[236:237], v[188:189], s[14:15], v[236:237] op_sel_hi:[1,0,1]
	v_pk_fma_f32 v[238:239], v[190:191], s[14:15], v[238:239] op_sel_hi:[1,0,1]
	v_readlane_b32 s14, v1, 48
	v_cvt_pk_f32_fp8_e32 v[184:185], v16
	v_cvt_pk_f32_fp8_sdwa v[186:187], v16 src0_sel:WORD_1
	v_pk_fma_f32 v[224:225], v[184:185], s[14:15], v[224:225] op_sel_hi:[1,0,1]
	v_pk_fma_f32 v[226:227], v[186:187], s[14:15], v[226:227] op_sel_hi:[1,0,1]
	v_cvt_pk_f32_fp8_e32 v[188:189], v17
	v_cvt_pk_f32_fp8_sdwa v[190:191], v17 src0_sel:WORD_1
	v_pk_fma_f32 v[228:229], v[188:189], s[14:15], v[228:229] op_sel_hi:[1,0,1]
	v_pk_fma_f32 v[230:231], v[190:191], s[14:15], v[230:231] op_sel_hi:[1,0,1]
	v_cvt_pk_f32_fp8_e32 v[184:185], v18
	v_cvt_pk_f32_fp8_sdwa v[186:187], v18 src0_sel:WORD_1
	v_pk_fma_f32 v[232:233], v[184:185], s[14:15], v[232:233] op_sel_hi:[1,0,1]
	v_pk_fma_f32 v[234:235], v[186:187], s[14:15], v[234:235] op_sel_hi:[1,0,1]
	v_cvt_pk_f32_fp8_e32 v[188:189], v19
	v_cvt_pk_f32_fp8_sdwa v[190:191], v19 src0_sel:WORD_1
	v_pk_fma_f32 v[236:237], v[188:189], s[14:15], v[236:237] op_sel_hi:[1,0,1]
	v_pk_fma_f32 v[238:239], v[190:191], s[14:15], v[238:239] op_sel_hi:[1,0,1]
	v_readlane_b32 s14, v1, 56
	v_cvt_pk_f32_fp8_e32 v[184:185], v12
	v_cvt_pk_f32_fp8_sdwa v[186:187], v12 src0_sel:WORD_1
	v_pk_fma_f32 v[224:225], v[184:185], s[14:15], v[224:225] op_sel_hi:[1,0,1]
	v_pk_fma_f32 v[226:227], v[186:187], s[14:15], v[226:227] op_sel_hi:[1,0,1]
	v_cvt_pk_f32_fp8_e32 v[188:189], v13
	v_cvt_pk_f32_fp8_sdwa v[190:191], v13 src0_sel:WORD_1
	v_pk_fma_f32 v[228:229], v[188:189], s[14:15], v[228:229] op_sel_hi:[1,0,1]
	v_pk_fma_f32 v[230:231], v[190:191], s[14:15], v[230:231] op_sel_hi:[1,0,1]
	v_cvt_pk_f32_fp8_e32 v[184:185], v14
	v_cvt_pk_f32_fp8_sdwa v[186:187], v14 src0_sel:WORD_1
	v_pk_fma_f32 v[232:233], v[184:185], s[14:15], v[232:233] op_sel_hi:[1,0,1]
	v_pk_fma_f32 v[234:235], v[186:187], s[14:15], v[234:235] op_sel_hi:[1,0,1]
	v_cvt_pk_f32_fp8_e32 v[188:189], v15
	v_cvt_pk_f32_fp8_sdwa v[190:191], v15 src0_sel:WORD_1
	v_pk_fma_f32 v[236:237], v[188:189], s[14:15], v[236:237] op_sel_hi:[1,0,1]
	v_pk_fma_f32 v[238:239], v[190:191], s[14:15], v[238:239] op_sel_hi:[1,0,1]
	s_branch .Lp6c0_axdone
.Lp6c0_t7:
	v_readlane_b32 s14, v1, 0
	v_cvt_pk_f32_fp8_e32 v[184:185], v68
	v_cvt_pk_f32_fp8_sdwa v[186:187], v68 src0_sel:WORD_1
	v_pk_fma_f32 v[240:241], v[184:185], s[14:15], v[240:241] op_sel_hi:[1,0,1]
	v_pk_fma_f32 v[242:243], v[186:187], s[14:15], v[242:243] op_sel_hi:[1,0,1]
	v_cvt_pk_f32_fp8_e32 v[188:189], v69
	v_cvt_pk_f32_fp8_sdwa v[190:191], v69 src0_sel:WORD_1
	v_pk_fma_f32 v[244:245], v[188:189], s[14:15], v[244:245] op_sel_hi:[1,0,1]
	v_pk_fma_f32 v[246:247], v[190:191], s[14:15], v[246:247] op_sel_hi:[1,0,1]
	v_cvt_pk_f32_fp8_e32 v[184:185], v70
	v_cvt_pk_f32_fp8_sdwa v[186:187], v70 src0_sel:WORD_1
	v_pk_fma_f32 v[248:249], v[184:185], s[14:15], v[248:249] op_sel_hi:[1,0,1]
	v_pk_fma_f32 v[250:251], v[186:187], s[14:15], v[250:251] op_sel_hi:[1,0,1]
	v_cvt_pk_f32_fp8_e32 v[188:189], v71
	v_cvt_pk_f32_fp8_sdwa v[190:191], v71 src0_sel:WORD_1
	v_pk_fma_f32 v[216:217], v[188:189], s[14:15], v[216:217] op_sel_hi:[1,0,1]
	v_pk_fma_f32 v[218:219], v[190:191], s[14:15], v[218:219] op_sel_hi:[1,0,1]
	v_readlane_b32 s14, v1, 8
	v_cvt_pk_f32_fp8_e32 v[184:185], v64
	v_cvt_pk_f32_fp8_sdwa v[186:187], v64 src0_sel:WORD_1
	v_pk_fma_f32 v[240:241], v[184:185], s[14:15], v[240:241] op_sel_hi:[1,0,1]
	v_pk_fma_f32 v[242:243], v[186:187], s[14:15], v[242:243] op_sel_hi:[1,0,1]
	v_cvt_pk_f32_fp8_e32 v[188:189], v65
	v_cvt_pk_f32_fp8_sdwa v[190:191], v65 src0_sel:WORD_1
	v_pk_fma_f32 v[244:245], v[188:189], s[14:15], v[244:245] op_sel_hi:[1,0,1]
	v_pk_fma_f32 v[246:247], v[190:191], s[14:15], v[246:247] op_sel_hi:[1,0,1]
	v_cvt_pk_f32_fp8_e32 v[184:185], v66
	v_cvt_pk_f32_fp8_sdwa v[186:187], v66 src0_sel:WORD_1
	v_pk_fma_f32 v[248:249], v[184:185], s[14:15], v[248:249] op_sel_hi:[1,0,1]
	v_pk_fma_f32 v[250:251], v[186:187], s[14:15], v[250:251] op_sel_hi:[1,0,1]
	v_cvt_pk_f32_fp8_e32 v[188:189], v67
	v_cvt_pk_f32_fp8_sdwa v[190:191], v67 src0_sel:WORD_1
	v_pk_fma_f32 v[216:217], v[188:189], s[14:15], v[216:217] op_sel_hi:[1,0,1]
	v_pk_fma_f32 v[218:219], v[190:191], s[14:15], v[218:219] op_sel_hi:[1,0,1]
	v_readlane_b32 s14, v1, 16
	v_cvt_pk_f32_fp8_e32 v[184:185], v60
	v_cvt_pk_f32_fp8_sdwa v[186:187], v60 src0_sel:WORD_1
	v_pk_fma_f32 v[240:241], v[184:185], s[14:15], v[240:241] op_sel_hi:[1,0,1]
	v_pk_fma_f32 v[242:243], v[186:187], s[14:15], v[242:243] op_sel_hi:[1,0,1]
	v_cvt_pk_f32_fp8_e32 v[188:189], v61
	v_cvt_pk_f32_fp8_sdwa v[190:191], v61 src0_sel:WORD_1
	v_pk_fma_f32 v[244:245], v[188:189], s[14:15], v[244:245] op_sel_hi:[1,0,1]
	v_pk_fma_f32 v[246:247], v[190:191], s[14:15], v[246:247] op_sel_hi:[1,0,1]
	v_cvt_pk_f32_fp8_e32 v[184:185], v62
	v_cvt_pk_f32_fp8_sdwa v[186:187], v62 src0_sel:WORD_1
	v_pk_fma_f32 v[248:249], v[184:185], s[14:15], v[248:249] op_sel_hi:[1,0,1]
	v_pk_fma_f32 v[250:251], v[186:187], s[14:15], v[250:251] op_sel_hi:[1,0,1]
	v_cvt_pk_f32_fp8_e32 v[188:189], v63
	v_cvt_pk_f32_fp8_sdwa v[190:191], v63 src0_sel:WORD_1
	v_pk_fma_f32 v[216:217], v[188:189], s[14:15], v[216:217] op_sel_hi:[1,0,1]
	v_pk_fma_f32 v[218:219], v[190:191], s[14:15], v[218:219] op_sel_hi:[1,0,1]
	v_readlane_b32 s14, v1, 24
	v_cvt_pk_f32_fp8_e32 v[184:185], v56
	v_cvt_pk_f32_fp8_sdwa v[186:187], v56 src0_sel:WORD_1
	v_pk_fma_f32 v[240:241], v[184:185], s[14:15], v[240:241] op_sel_hi:[1,0,1]
	v_pk_fma_f32 v[242:243], v[186:187], s[14:15], v[242:243] op_sel_hi:[1,0,1]
	v_cvt_pk_f32_fp8_e32 v[188:189], v57
	v_cvt_pk_f32_fp8_sdwa v[190:191], v57 src0_sel:WORD_1
	v_pk_fma_f32 v[244:245], v[188:189], s[14:15], v[244:245] op_sel_hi:[1,0,1]
	v_pk_fma_f32 v[246:247], v[190:191], s[14:15], v[246:247] op_sel_hi:[1,0,1]
	v_cvt_pk_f32_fp8_e32 v[184:185], v58
	v_cvt_pk_f32_fp8_sdwa v[186:187], v58 src0_sel:WORD_1
	v_pk_fma_f32 v[248:249], v[184:185], s[14:15], v[248:249] op_sel_hi:[1,0,1]
	v_pk_fma_f32 v[250:251], v[186:187], s[14:15], v[250:251] op_sel_hi:[1,0,1]
	v_cvt_pk_f32_fp8_e32 v[188:189], v59
	v_cvt_pk_f32_fp8_sdwa v[190:191], v59 src0_sel:WORD_1
	v_pk_fma_f32 v[216:217], v[188:189], s[14:15], v[216:217] op_sel_hi:[1,0,1]
	v_pk_fma_f32 v[218:219], v[190:191], s[14:15], v[218:219] op_sel_hi:[1,0,1]
	v_readlane_b32 s14, v1, 32
	v_cvt_pk_f32_fp8_e32 v[184:185], v48
	v_cvt_pk_f32_fp8_sdwa v[186:187], v48 src0_sel:WORD_1
	v_pk_fma_f32 v[240:241], v[184:185], s[14:15], v[240:241] op_sel_hi:[1,0,1]
	v_pk_fma_f32 v[242:243], v[186:187], s[14:15], v[242:243] op_sel_hi:[1,0,1]
	v_cvt_pk_f32_fp8_e32 v[188:189], v49
	v_cvt_pk_f32_fp8_sdwa v[190:191], v49 src0_sel:WORD_1
	v_pk_fma_f32 v[244:245], v[188:189], s[14:15], v[244:245] op_sel_hi:[1,0,1]
	v_pk_fma_f32 v[246:247], v[190:191], s[14:15], v[246:247] op_sel_hi:[1,0,1]
	v_cvt_pk_f32_fp8_e32 v[184:185], v50
	v_cvt_pk_f32_fp8_sdwa v[186:187], v50 src0_sel:WORD_1
	v_pk_fma_f32 v[248:249], v[184:185], s[14:15], v[248:249] op_sel_hi:[1,0,1]
	v_pk_fma_f32 v[250:251], v[186:187], s[14:15], v[250:251] op_sel_hi:[1,0,1]
	v_cvt_pk_f32_fp8_e32 v[188:189], v51
	v_cvt_pk_f32_fp8_sdwa v[190:191], v51 src0_sel:WORD_1
	v_pk_fma_f32 v[216:217], v[188:189], s[14:15], v[216:217] op_sel_hi:[1,0,1]
	v_pk_fma_f32 v[218:219], v[190:191], s[14:15], v[218:219] op_sel_hi:[1,0,1]
	v_readlane_b32 s14, v1, 40
	v_cvt_pk_f32_fp8_e32 v[184:185], v32
	v_cvt_pk_f32_fp8_sdwa v[186:187], v32 src0_sel:WORD_1
	v_pk_fma_f32 v[240:241], v[184:185], s[14:15], v[240:241] op_sel_hi:[1,0,1]
	v_pk_fma_f32 v[242:243], v[186:187], s[14:15], v[242:243] op_sel_hi:[1,0,1]
	v_cvt_pk_f32_fp8_e32 v[188:189], v33
	v_cvt_pk_f32_fp8_sdwa v[190:191], v33 src0_sel:WORD_1
	v_pk_fma_f32 v[244:245], v[188:189], s[14:15], v[244:245] op_sel_hi:[1,0,1]
	v_pk_fma_f32 v[246:247], v[190:191], s[14:15], v[246:247] op_sel_hi:[1,0,1]
	v_cvt_pk_f32_fp8_e32 v[184:185], v34
	v_cvt_pk_f32_fp8_sdwa v[186:187], v34 src0_sel:WORD_1
	v_pk_fma_f32 v[248:249], v[184:185], s[14:15], v[248:249] op_sel_hi:[1,0,1]
	v_pk_fma_f32 v[250:251], v[186:187], s[14:15], v[250:251] op_sel_hi:[1,0,1]
	v_cvt_pk_f32_fp8_e32 v[188:189], v35
	v_cvt_pk_f32_fp8_sdwa v[190:191], v35 src0_sel:WORD_1
	v_pk_fma_f32 v[216:217], v[188:189], s[14:15], v[216:217] op_sel_hi:[1,0,1]
	v_pk_fma_f32 v[218:219], v[190:191], s[14:15], v[218:219] op_sel_hi:[1,0,1]
	v_readlane_b32 s14, v1, 48
	v_cvt_pk_f32_fp8_e32 v[184:185], v16
	v_cvt_pk_f32_fp8_sdwa v[186:187], v16 src0_sel:WORD_1
	v_pk_fma_f32 v[240:241], v[184:185], s[14:15], v[240:241] op_sel_hi:[1,0,1]
	v_pk_fma_f32 v[242:243], v[186:187], s[14:15], v[242:243] op_sel_hi:[1,0,1]
	v_cvt_pk_f32_fp8_e32 v[188:189], v17
	v_cvt_pk_f32_fp8_sdwa v[190:191], v17 src0_sel:WORD_1
	v_pk_fma_f32 v[244:245], v[188:189], s[14:15], v[244:245] op_sel_hi:[1,0,1]
	v_pk_fma_f32 v[246:247], v[190:191], s[14:15], v[246:247] op_sel_hi:[1,0,1]
	v_cvt_pk_f32_fp8_e32 v[184:185], v18
	v_cvt_pk_f32_fp8_sdwa v[186:187], v18 src0_sel:WORD_1
	v_pk_fma_f32 v[248:249], v[184:185], s[14:15], v[248:249] op_sel_hi:[1,0,1]
	v_pk_fma_f32 v[250:251], v[186:187], s[14:15], v[250:251] op_sel_hi:[1,0,1]
	v_cvt_pk_f32_fp8_e32 v[188:189], v19
	v_cvt_pk_f32_fp8_sdwa v[190:191], v19 src0_sel:WORD_1
	v_pk_fma_f32 v[216:217], v[188:189], s[14:15], v[216:217] op_sel_hi:[1,0,1]
	v_pk_fma_f32 v[218:219], v[190:191], s[14:15], v[218:219] op_sel_hi:[1,0,1]
	v_readlane_b32 s14, v1, 56
	v_cvt_pk_f32_fp8_e32 v[184:185], v12
	v_cvt_pk_f32_fp8_sdwa v[186:187], v12 src0_sel:WORD_1
	v_pk_fma_f32 v[240:241], v[184:185], s[14:15], v[240:241] op_sel_hi:[1,0,1]
	v_pk_fma_f32 v[242:243], v[186:187], s[14:15], v[242:243] op_sel_hi:[1,0,1]
	v_cvt_pk_f32_fp8_e32 v[188:189], v13
	v_cvt_pk_f32_fp8_sdwa v[190:191], v13 src0_sel:WORD_1
	v_pk_fma_f32 v[244:245], v[188:189], s[14:15], v[244:245] op_sel_hi:[1,0,1]
	v_pk_fma_f32 v[246:247], v[190:191], s[14:15], v[246:247] op_sel_hi:[1,0,1]
	v_cvt_pk_f32_fp8_e32 v[184:185], v14
	v_cvt_pk_f32_fp8_sdwa v[186:187], v14 src0_sel:WORD_1
	v_pk_fma_f32 v[248:249], v[184:185], s[14:15], v[248:249] op_sel_hi:[1,0,1]
	v_pk_fma_f32 v[250:251], v[186:187], s[14:15], v[250:251] op_sel_hi:[1,0,1]
	v_cvt_pk_f32_fp8_e32 v[188:189], v15
	v_cvt_pk_f32_fp8_sdwa v[190:191], v15 src0_sel:WORD_1
	v_pk_fma_f32 v[216:217], v[188:189], s[14:15], v[216:217] op_sel_hi:[1,0,1]
	v_pk_fma_f32 v[218:219], v[190:191], s[14:15], v[218:219] op_sel_hi:[1,0,1]
	s_branch .Lp6c0_axdone

.Lp6c1_t0:
	v_readlane_b32 s14, v1, 0
	v_cvt_pk_f32_fp8_e32 v[184:185], v72
	v_cvt_pk_f32_fp8_sdwa v[186:187], v72 src0_sel:WORD_1
	v_pk_fma_f32 v[126:127], v[184:185], s[14:15], v[126:127] op_sel_hi:[1,0,1]
	v_pk_fma_f32 v[128:129], v[186:187], s[14:15], v[128:129] op_sel_hi:[1,0,1]
	v_cvt_pk_f32_fp8_e32 v[188:189], v73
	v_cvt_pk_f32_fp8_sdwa v[190:191], v73 src0_sel:WORD_1
	v_pk_fma_f32 v[130:131], v[188:189], s[14:15], v[130:131] op_sel_hi:[1,0,1]
	v_pk_fma_f32 v[132:133], v[190:191], s[14:15], v[132:133] op_sel_hi:[1,0,1]
	v_cvt_pk_f32_fp8_e32 v[184:185], v74
	v_cvt_pk_f32_fp8_sdwa v[186:187], v74 src0_sel:WORD_1
	v_pk_fma_f32 v[134:135], v[184:185], s[14:15], v[134:135] op_sel_hi:[1,0,1]
	v_pk_fma_f32 v[136:137], v[186:187], s[14:15], v[136:137] op_sel_hi:[1,0,1]
	v_cvt_pk_f32_fp8_e32 v[188:189], v75
	v_cvt_pk_f32_fp8_sdwa v[190:191], v75 src0_sel:WORD_1
	v_pk_fma_f32 v[138:139], v[188:189], s[14:15], v[138:139] op_sel_hi:[1,0,1]
	v_pk_fma_f32 v[140:141], v[190:191], s[14:15], v[140:141] op_sel_hi:[1,0,1]
	v_readlane_b32 s14, v1, 8
	v_cvt_pk_f32_fp8_e32 v[184:185], v52
	v_cvt_pk_f32_fp8_sdwa v[186:187], v52 src0_sel:WORD_1
	v_pk_fma_f32 v[126:127], v[184:185], s[14:15], v[126:127] op_sel_hi:[1,0,1]
	v_pk_fma_f32 v[128:129], v[186:187], s[14:15], v[128:129] op_sel_hi:[1,0,1]
	v_cvt_pk_f32_fp8_e32 v[188:189], v53
	v_cvt_pk_f32_fp8_sdwa v[190:191], v53 src0_sel:WORD_1
	v_pk_fma_f32 v[130:131], v[188:189], s[14:15], v[130:131] op_sel_hi:[1,0,1]
	v_pk_fma_f32 v[132:133], v[190:191], s[14:15], v[132:133] op_sel_hi:[1,0,1]
	v_cvt_pk_f32_fp8_e32 v[184:185], v54
	v_cvt_pk_f32_fp8_sdwa v[186:187], v54 src0_sel:WORD_1
	v_pk_fma_f32 v[134:135], v[184:185], s[14:15], v[134:135] op_sel_hi:[1,0,1]
	v_pk_fma_f32 v[136:137], v[186:187], s[14:15], v[136:137] op_sel_hi:[1,0,1]
	v_cvt_pk_f32_fp8_e32 v[188:189], v55
	v_cvt_pk_f32_fp8_sdwa v[190:191], v55 src0_sel:WORD_1
	v_pk_fma_f32 v[138:139], v[188:189], s[14:15], v[138:139] op_sel_hi:[1,0,1]
	v_pk_fma_f32 v[140:141], v[190:191], s[14:15], v[140:141] op_sel_hi:[1,0,1]
	v_readlane_b32 s14, v1, 16
	v_cvt_pk_f32_fp8_e32 v[184:185], v44
	v_cvt_pk_f32_fp8_sdwa v[186:187], v44 src0_sel:WORD_1
	v_pk_fma_f32 v[126:127], v[184:185], s[14:15], v[126:127] op_sel_hi:[1,0,1]
	v_pk_fma_f32 v[128:129], v[186:187], s[14:15], v[128:129] op_sel_hi:[1,0,1]
	v_cvt_pk_f32_fp8_e32 v[188:189], v45
	v_cvt_pk_f32_fp8_sdwa v[190:191], v45 src0_sel:WORD_1
	v_pk_fma_f32 v[130:131], v[188:189], s[14:15], v[130:131] op_sel_hi:[1,0,1]
	v_pk_fma_f32 v[132:133], v[190:191], s[14:15], v[132:133] op_sel_hi:[1,0,1]
	v_cvt_pk_f32_fp8_e32 v[184:185], v46
	v_cvt_pk_f32_fp8_sdwa v[186:187], v46 src0_sel:WORD_1
	v_pk_fma_f32 v[134:135], v[184:185], s[14:15], v[134:135] op_sel_hi:[1,0,1]
	v_pk_fma_f32 v[136:137], v[186:187], s[14:15], v[136:137] op_sel_hi:[1,0,1]
	v_cvt_pk_f32_fp8_e32 v[188:189], v47
	v_cvt_pk_f32_fp8_sdwa v[190:191], v47 src0_sel:WORD_1
	v_pk_fma_f32 v[138:139], v[188:189], s[14:15], v[138:139] op_sel_hi:[1,0,1]
	v_pk_fma_f32 v[140:141], v[190:191], s[14:15], v[140:141] op_sel_hi:[1,0,1]
	v_readlane_b32 s14, v1, 24
	v_cvt_pk_f32_fp8_e32 v[184:185], v40
	v_cvt_pk_f32_fp8_sdwa v[186:187], v40 src0_sel:WORD_1
	v_pk_fma_f32 v[126:127], v[184:185], s[14:15], v[126:127] op_sel_hi:[1,0,1]
	v_pk_fma_f32 v[128:129], v[186:187], s[14:15], v[128:129] op_sel_hi:[1,0,1]
	v_cvt_pk_f32_fp8_e32 v[188:189], v41
	v_cvt_pk_f32_fp8_sdwa v[190:191], v41 src0_sel:WORD_1
	v_pk_fma_f32 v[130:131], v[188:189], s[14:15], v[130:131] op_sel_hi:[1,0,1]
	v_pk_fma_f32 v[132:133], v[190:191], s[14:15], v[132:133] op_sel_hi:[1,0,1]
	v_cvt_pk_f32_fp8_e32 v[184:185], v42
	v_cvt_pk_f32_fp8_sdwa v[186:187], v42 src0_sel:WORD_1
	v_pk_fma_f32 v[134:135], v[184:185], s[14:15], v[134:135] op_sel_hi:[1,0,1]
	v_pk_fma_f32 v[136:137], v[186:187], s[14:15], v[136:137] op_sel_hi:[1,0,1]
	v_cvt_pk_f32_fp8_e32 v[188:189], v43
	v_cvt_pk_f32_fp8_sdwa v[190:191], v43 src0_sel:WORD_1
	v_pk_fma_f32 v[138:139], v[188:189], s[14:15], v[138:139] op_sel_hi:[1,0,1]
	v_pk_fma_f32 v[140:141], v[190:191], s[14:15], v[140:141] op_sel_hi:[1,0,1]
	v_readlane_b32 s14, v1, 32
	v_cvt_pk_f32_fp8_e32 v[184:185], v36
	v_cvt_pk_f32_fp8_sdwa v[186:187], v36 src0_sel:WORD_1
	v_pk_fma_f32 v[126:127], v[184:185], s[14:15], v[126:127] op_sel_hi:[1,0,1]
	v_pk_fma_f32 v[128:129], v[186:187], s[14:15], v[128:129] op_sel_hi:[1,0,1]
	v_cvt_pk_f32_fp8_e32 v[188:189], v37
	v_cvt_pk_f32_fp8_sdwa v[190:191], v37 src0_sel:WORD_1
	v_pk_fma_f32 v[130:131], v[188:189], s[14:15], v[130:131] op_sel_hi:[1,0,1]
	v_pk_fma_f32 v[132:133], v[190:191], s[14:15], v[132:133] op_sel_hi:[1,0,1]
	v_cvt_pk_f32_fp8_e32 v[184:185], v38
	v_cvt_pk_f32_fp8_sdwa v[186:187], v38 src0_sel:WORD_1
	v_pk_fma_f32 v[134:135], v[184:185], s[14:15], v[134:135] op_sel_hi:[1,0,1]
	v_pk_fma_f32 v[136:137], v[186:187], s[14:15], v[136:137] op_sel_hi:[1,0,1]
	v_cvt_pk_f32_fp8_e32 v[188:189], v39
	v_cvt_pk_f32_fp8_sdwa v[190:191], v39 src0_sel:WORD_1
	v_pk_fma_f32 v[138:139], v[188:189], s[14:15], v[138:139] op_sel_hi:[1,0,1]
	v_pk_fma_f32 v[140:141], v[190:191], s[14:15], v[140:141] op_sel_hi:[1,0,1]
	v_readlane_b32 s14, v1, 40
	v_cvt_pk_f32_fp8_e32 v[184:185], v28
	v_cvt_pk_f32_fp8_sdwa v[186:187], v28 src0_sel:WORD_1
	v_pk_fma_f32 v[126:127], v[184:185], s[14:15], v[126:127] op_sel_hi:[1,0,1]
	v_pk_fma_f32 v[128:129], v[186:187], s[14:15], v[128:129] op_sel_hi:[1,0,1]
	v_cvt_pk_f32_fp8_e32 v[188:189], v29
	v_cvt_pk_f32_fp8_sdwa v[190:191], v29 src0_sel:WORD_1
	v_pk_fma_f32 v[130:131], v[188:189], s[14:15], v[130:131] op_sel_hi:[1,0,1]
	v_pk_fma_f32 v[132:133], v[190:191], s[14:15], v[132:133] op_sel_hi:[1,0,1]
	v_cvt_pk_f32_fp8_e32 v[184:185], v30
	v_cvt_pk_f32_fp8_sdwa v[186:187], v30 src0_sel:WORD_1
	v_pk_fma_f32 v[134:135], v[184:185], s[14:15], v[134:135] op_sel_hi:[1,0,1]
	v_pk_fma_f32 v[136:137], v[186:187], s[14:15], v[136:137] op_sel_hi:[1,0,1]
	v_cvt_pk_f32_fp8_e32 v[188:189], v31
	v_cvt_pk_f32_fp8_sdwa v[190:191], v31 src0_sel:WORD_1
	v_pk_fma_f32 v[138:139], v[188:189], s[14:15], v[138:139] op_sel_hi:[1,0,1]
	v_pk_fma_f32 v[140:141], v[190:191], s[14:15], v[140:141] op_sel_hi:[1,0,1]
	v_readlane_b32 s14, v1, 48
	v_cvt_pk_f32_fp8_e32 v[184:185], v24
	v_cvt_pk_f32_fp8_sdwa v[186:187], v24 src0_sel:WORD_1
	v_pk_fma_f32 v[126:127], v[184:185], s[14:15], v[126:127] op_sel_hi:[1,0,1]
	v_pk_fma_f32 v[128:129], v[186:187], s[14:15], v[128:129] op_sel_hi:[1,0,1]
	v_cvt_pk_f32_fp8_e32 v[188:189], v25
	v_cvt_pk_f32_fp8_sdwa v[190:191], v25 src0_sel:WORD_1
	v_pk_fma_f32 v[130:131], v[188:189], s[14:15], v[130:131] op_sel_hi:[1,0,1]
	v_pk_fma_f32 v[132:133], v[190:191], s[14:15], v[132:133] op_sel_hi:[1,0,1]
	v_cvt_pk_f32_fp8_e32 v[184:185], v26
	v_cvt_pk_f32_fp8_sdwa v[186:187], v26 src0_sel:WORD_1
	v_pk_fma_f32 v[134:135], v[184:185], s[14:15], v[134:135] op_sel_hi:[1,0,1]
	v_pk_fma_f32 v[136:137], v[186:187], s[14:15], v[136:137] op_sel_hi:[1,0,1]
	v_cvt_pk_f32_fp8_e32 v[188:189], v27
	v_cvt_pk_f32_fp8_sdwa v[190:191], v27 src0_sel:WORD_1
	v_pk_fma_f32 v[138:139], v[188:189], s[14:15], v[138:139] op_sel_hi:[1,0,1]
	v_pk_fma_f32 v[140:141], v[190:191], s[14:15], v[140:141] op_sel_hi:[1,0,1]
	v_readlane_b32 s14, v1, 56
	v_cvt_pk_f32_fp8_e32 v[184:185], v20
	v_cvt_pk_f32_fp8_sdwa v[186:187], v20 src0_sel:WORD_1
	v_pk_fma_f32 v[126:127], v[184:185], s[14:15], v[126:127] op_sel_hi:[1,0,1]
	v_pk_fma_f32 v[128:129], v[186:187], s[14:15], v[128:129] op_sel_hi:[1,0,1]
	v_cvt_pk_f32_fp8_e32 v[188:189], v21
	v_cvt_pk_f32_fp8_sdwa v[190:191], v21 src0_sel:WORD_1
	v_pk_fma_f32 v[130:131], v[188:189], s[14:15], v[130:131] op_sel_hi:[1,0,1]
	v_pk_fma_f32 v[132:133], v[190:191], s[14:15], v[132:133] op_sel_hi:[1,0,1]
	v_cvt_pk_f32_fp8_e32 v[184:185], v22
	v_cvt_pk_f32_fp8_sdwa v[186:187], v22 src0_sel:WORD_1
	v_pk_fma_f32 v[134:135], v[184:185], s[14:15], v[134:135] op_sel_hi:[1,0,1]
	v_pk_fma_f32 v[136:137], v[186:187], s[14:15], v[136:137] op_sel_hi:[1,0,1]
	v_cvt_pk_f32_fp8_e32 v[188:189], v23
	v_cvt_pk_f32_fp8_sdwa v[190:191], v23 src0_sel:WORD_1
	v_pk_fma_f32 v[138:139], v[188:189], s[14:15], v[138:139] op_sel_hi:[1,0,1]
	v_pk_fma_f32 v[140:141], v[190:191], s[14:15], v[140:141] op_sel_hi:[1,0,1]
	s_branch .Lp6c1_axdone
.Lp6c1_t1:
	v_readlane_b32 s14, v1, 0
	v_cvt_pk_f32_fp8_e32 v[184:185], v72
	v_cvt_pk_f32_fp8_sdwa v[186:187], v72 src0_sel:WORD_1
	v_pk_fma_f32 v[110:111], v[184:185], s[14:15], v[110:111] op_sel_hi:[1,0,1]
	v_pk_fma_f32 v[112:113], v[186:187], s[14:15], v[112:113] op_sel_hi:[1,0,1]
	v_cvt_pk_f32_fp8_e32 v[188:189], v73
	v_cvt_pk_f32_fp8_sdwa v[190:191], v73 src0_sel:WORD_1
	v_pk_fma_f32 v[114:115], v[188:189], s[14:15], v[114:115] op_sel_hi:[1,0,1]
	v_pk_fma_f32 v[116:117], v[190:191], s[14:15], v[116:117] op_sel_hi:[1,0,1]
	v_cvt_pk_f32_fp8_e32 v[184:185], v74
	v_cvt_pk_f32_fp8_sdwa v[186:187], v74 src0_sel:WORD_1
	v_pk_fma_f32 v[118:119], v[184:185], s[14:15], v[118:119] op_sel_hi:[1,0,1]
	v_pk_fma_f32 v[120:121], v[186:187], s[14:15], v[120:121] op_sel_hi:[1,0,1]
	v_cvt_pk_f32_fp8_e32 v[188:189], v75
	v_cvt_pk_f32_fp8_sdwa v[190:191], v75 src0_sel:WORD_1
	v_pk_fma_f32 v[122:123], v[188:189], s[14:15], v[122:123] op_sel_hi:[1,0,1]
	v_pk_fma_f32 v[124:125], v[190:191], s[14:15], v[124:125] op_sel_hi:[1,0,1]
	v_readlane_b32 s14, v1, 8
	v_cvt_pk_f32_fp8_e32 v[184:185], v52
	v_cvt_pk_f32_fp8_sdwa v[186:187], v52 src0_sel:WORD_1
	v_pk_fma_f32 v[110:111], v[184:185], s[14:15], v[110:111] op_sel_hi:[1,0,1]
	v_pk_fma_f32 v[112:113], v[186:187], s[14:15], v[112:113] op_sel_hi:[1,0,1]
	v_cvt_pk_f32_fp8_e32 v[188:189], v53
	v_cvt_pk_f32_fp8_sdwa v[190:191], v53 src0_sel:WORD_1
	v_pk_fma_f32 v[114:115], v[188:189], s[14:15], v[114:115] op_sel_hi:[1,0,1]
	v_pk_fma_f32 v[116:117], v[190:191], s[14:15], v[116:117] op_sel_hi:[1,0,1]
	v_cvt_pk_f32_fp8_e32 v[184:185], v54
	v_cvt_pk_f32_fp8_sdwa v[186:187], v54 src0_sel:WORD_1
	v_pk_fma_f32 v[118:119], v[184:185], s[14:15], v[118:119] op_sel_hi:[1,0,1]
	v_pk_fma_f32 v[120:121], v[186:187], s[14:15], v[120:121] op_sel_hi:[1,0,1]
	v_cvt_pk_f32_fp8_e32 v[188:189], v55
	v_cvt_pk_f32_fp8_sdwa v[190:191], v55 src0_sel:WORD_1
	v_pk_fma_f32 v[122:123], v[188:189], s[14:15], v[122:123] op_sel_hi:[1,0,1]
	v_pk_fma_f32 v[124:125], v[190:191], s[14:15], v[124:125] op_sel_hi:[1,0,1]
	v_readlane_b32 s14, v1, 16
	v_cvt_pk_f32_fp8_e32 v[184:185], v44
	v_cvt_pk_f32_fp8_sdwa v[186:187], v44 src0_sel:WORD_1
	v_pk_fma_f32 v[110:111], v[184:185], s[14:15], v[110:111] op_sel_hi:[1,0,1]
	v_pk_fma_f32 v[112:113], v[186:187], s[14:15], v[112:113] op_sel_hi:[1,0,1]
	v_cvt_pk_f32_fp8_e32 v[188:189], v45
	v_cvt_pk_f32_fp8_sdwa v[190:191], v45 src0_sel:WORD_1
	v_pk_fma_f32 v[114:115], v[188:189], s[14:15], v[114:115] op_sel_hi:[1,0,1]
	v_pk_fma_f32 v[116:117], v[190:191], s[14:15], v[116:117] op_sel_hi:[1,0,1]
	v_cvt_pk_f32_fp8_e32 v[184:185], v46
	v_cvt_pk_f32_fp8_sdwa v[186:187], v46 src0_sel:WORD_1
	v_pk_fma_f32 v[118:119], v[184:185], s[14:15], v[118:119] op_sel_hi:[1,0,1]
	v_pk_fma_f32 v[120:121], v[186:187], s[14:15], v[120:121] op_sel_hi:[1,0,1]
	v_cvt_pk_f32_fp8_e32 v[188:189], v47
	v_cvt_pk_f32_fp8_sdwa v[190:191], v47 src0_sel:WORD_1
	v_pk_fma_f32 v[122:123], v[188:189], s[14:15], v[122:123] op_sel_hi:[1,0,1]
	v_pk_fma_f32 v[124:125], v[190:191], s[14:15], v[124:125] op_sel_hi:[1,0,1]
	v_readlane_b32 s14, v1, 24
	v_cvt_pk_f32_fp8_e32 v[184:185], v40
	v_cvt_pk_f32_fp8_sdwa v[186:187], v40 src0_sel:WORD_1
	v_pk_fma_f32 v[110:111], v[184:185], s[14:15], v[110:111] op_sel_hi:[1,0,1]
	v_pk_fma_f32 v[112:113], v[186:187], s[14:15], v[112:113] op_sel_hi:[1,0,1]
	v_cvt_pk_f32_fp8_e32 v[188:189], v41
	v_cvt_pk_f32_fp8_sdwa v[190:191], v41 src0_sel:WORD_1
	v_pk_fma_f32 v[114:115], v[188:189], s[14:15], v[114:115] op_sel_hi:[1,0,1]
	v_pk_fma_f32 v[116:117], v[190:191], s[14:15], v[116:117] op_sel_hi:[1,0,1]
	v_cvt_pk_f32_fp8_e32 v[184:185], v42
	v_cvt_pk_f32_fp8_sdwa v[186:187], v42 src0_sel:WORD_1
	v_pk_fma_f32 v[118:119], v[184:185], s[14:15], v[118:119] op_sel_hi:[1,0,1]
	v_pk_fma_f32 v[120:121], v[186:187], s[14:15], v[120:121] op_sel_hi:[1,0,1]
	v_cvt_pk_f32_fp8_e32 v[188:189], v43
	v_cvt_pk_f32_fp8_sdwa v[190:191], v43 src0_sel:WORD_1
	v_pk_fma_f32 v[122:123], v[188:189], s[14:15], v[122:123] op_sel_hi:[1,0,1]
	v_pk_fma_f32 v[124:125], v[190:191], s[14:15], v[124:125] op_sel_hi:[1,0,1]
	v_readlane_b32 s14, v1, 32
	v_cvt_pk_f32_fp8_e32 v[184:185], v36
	v_cvt_pk_f32_fp8_sdwa v[186:187], v36 src0_sel:WORD_1
	v_pk_fma_f32 v[110:111], v[184:185], s[14:15], v[110:111] op_sel_hi:[1,0,1]
	v_pk_fma_f32 v[112:113], v[186:187], s[14:15], v[112:113] op_sel_hi:[1,0,1]
	v_cvt_pk_f32_fp8_e32 v[188:189], v37
	v_cvt_pk_f32_fp8_sdwa v[190:191], v37 src0_sel:WORD_1
	v_pk_fma_f32 v[114:115], v[188:189], s[14:15], v[114:115] op_sel_hi:[1,0,1]
	v_pk_fma_f32 v[116:117], v[190:191], s[14:15], v[116:117] op_sel_hi:[1,0,1]
	v_cvt_pk_f32_fp8_e32 v[184:185], v38
	v_cvt_pk_f32_fp8_sdwa v[186:187], v38 src0_sel:WORD_1
	v_pk_fma_f32 v[118:119], v[184:185], s[14:15], v[118:119] op_sel_hi:[1,0,1]
	v_pk_fma_f32 v[120:121], v[186:187], s[14:15], v[120:121] op_sel_hi:[1,0,1]
	v_cvt_pk_f32_fp8_e32 v[188:189], v39
	v_cvt_pk_f32_fp8_sdwa v[190:191], v39 src0_sel:WORD_1
	v_pk_fma_f32 v[122:123], v[188:189], s[14:15], v[122:123] op_sel_hi:[1,0,1]
	v_pk_fma_f32 v[124:125], v[190:191], s[14:15], v[124:125] op_sel_hi:[1,0,1]
	v_readlane_b32 s14, v1, 40
	v_cvt_pk_f32_fp8_e32 v[184:185], v28
	v_cvt_pk_f32_fp8_sdwa v[186:187], v28 src0_sel:WORD_1
	v_pk_fma_f32 v[110:111], v[184:185], s[14:15], v[110:111] op_sel_hi:[1,0,1]
	v_pk_fma_f32 v[112:113], v[186:187], s[14:15], v[112:113] op_sel_hi:[1,0,1]
	v_cvt_pk_f32_fp8_e32 v[188:189], v29
	v_cvt_pk_f32_fp8_sdwa v[190:191], v29 src0_sel:WORD_1
	v_pk_fma_f32 v[114:115], v[188:189], s[14:15], v[114:115] op_sel_hi:[1,0,1]
	v_pk_fma_f32 v[116:117], v[190:191], s[14:15], v[116:117] op_sel_hi:[1,0,1]
	v_cvt_pk_f32_fp8_e32 v[184:185], v30
	v_cvt_pk_f32_fp8_sdwa v[186:187], v30 src0_sel:WORD_1
	v_pk_fma_f32 v[118:119], v[184:185], s[14:15], v[118:119] op_sel_hi:[1,0,1]
	v_pk_fma_f32 v[120:121], v[186:187], s[14:15], v[120:121] op_sel_hi:[1,0,1]
	v_cvt_pk_f32_fp8_e32 v[188:189], v31
	v_cvt_pk_f32_fp8_sdwa v[190:191], v31 src0_sel:WORD_1
	v_pk_fma_f32 v[122:123], v[188:189], s[14:15], v[122:123] op_sel_hi:[1,0,1]
	v_pk_fma_f32 v[124:125], v[190:191], s[14:15], v[124:125] op_sel_hi:[1,0,1]
	v_readlane_b32 s14, v1, 48
	v_cvt_pk_f32_fp8_e32 v[184:185], v24
	v_cvt_pk_f32_fp8_sdwa v[186:187], v24 src0_sel:WORD_1
	v_pk_fma_f32 v[110:111], v[184:185], s[14:15], v[110:111] op_sel_hi:[1,0,1]
	v_pk_fma_f32 v[112:113], v[186:187], s[14:15], v[112:113] op_sel_hi:[1,0,1]
	v_cvt_pk_f32_fp8_e32 v[188:189], v25
	v_cvt_pk_f32_fp8_sdwa v[190:191], v25 src0_sel:WORD_1
	v_pk_fma_f32 v[114:115], v[188:189], s[14:15], v[114:115] op_sel_hi:[1,0,1]
	v_pk_fma_f32 v[116:117], v[190:191], s[14:15], v[116:117] op_sel_hi:[1,0,1]
	v_cvt_pk_f32_fp8_e32 v[184:185], v26
	v_cvt_pk_f32_fp8_sdwa v[186:187], v26 src0_sel:WORD_1
	v_pk_fma_f32 v[118:119], v[184:185], s[14:15], v[118:119] op_sel_hi:[1,0,1]
	v_pk_fma_f32 v[120:121], v[186:187], s[14:15], v[120:121] op_sel_hi:[1,0,1]
	v_cvt_pk_f32_fp8_e32 v[188:189], v27
	v_cvt_pk_f32_fp8_sdwa v[190:191], v27 src0_sel:WORD_1
	v_pk_fma_f32 v[122:123], v[188:189], s[14:15], v[122:123] op_sel_hi:[1,0,1]
	v_pk_fma_f32 v[124:125], v[190:191], s[14:15], v[124:125] op_sel_hi:[1,0,1]
	v_readlane_b32 s14, v1, 56
	v_cvt_pk_f32_fp8_e32 v[184:185], v20
	v_cvt_pk_f32_fp8_sdwa v[186:187], v20 src0_sel:WORD_1
	v_pk_fma_f32 v[110:111], v[184:185], s[14:15], v[110:111] op_sel_hi:[1,0,1]
	v_pk_fma_f32 v[112:113], v[186:187], s[14:15], v[112:113] op_sel_hi:[1,0,1]
	v_cvt_pk_f32_fp8_e32 v[188:189], v21
	v_cvt_pk_f32_fp8_sdwa v[190:191], v21 src0_sel:WORD_1
	v_pk_fma_f32 v[114:115], v[188:189], s[14:15], v[114:115] op_sel_hi:[1,0,1]
	v_pk_fma_f32 v[116:117], v[190:191], s[14:15], v[116:117] op_sel_hi:[1,0,1]
	v_cvt_pk_f32_fp8_e32 v[184:185], v22
	v_cvt_pk_f32_fp8_sdwa v[186:187], v22 src0_sel:WORD_1
	v_pk_fma_f32 v[118:119], v[184:185], s[14:15], v[118:119] op_sel_hi:[1,0,1]
	v_pk_fma_f32 v[120:121], v[186:187], s[14:15], v[120:121] op_sel_hi:[1,0,1]
	v_cvt_pk_f32_fp8_e32 v[188:189], v23
	v_cvt_pk_f32_fp8_sdwa v[190:191], v23 src0_sel:WORD_1
	v_pk_fma_f32 v[122:123], v[188:189], s[14:15], v[122:123] op_sel_hi:[1,0,1]
	v_pk_fma_f32 v[124:125], v[190:191], s[14:15], v[124:125] op_sel_hi:[1,0,1]
	s_branch .Lp6c1_axdone
.Lp6c1_t2:
	v_readlane_b32 s14, v1, 0
	v_cvt_pk_f32_fp8_e32 v[184:185], v72
	v_cvt_pk_f32_fp8_sdwa v[186:187], v72 src0_sel:WORD_1
	v_pk_fma_f32 v[94:95], v[184:185], s[14:15], v[94:95] op_sel_hi:[1,0,1]
	v_pk_fma_f32 v[96:97], v[186:187], s[14:15], v[96:97] op_sel_hi:[1,0,1]
	v_cvt_pk_f32_fp8_e32 v[188:189], v73
	v_cvt_pk_f32_fp8_sdwa v[190:191], v73 src0_sel:WORD_1
	v_pk_fma_f32 v[98:99], v[188:189], s[14:15], v[98:99] op_sel_hi:[1,0,1]
	v_pk_fma_f32 v[100:101], v[190:191], s[14:15], v[100:101] op_sel_hi:[1,0,1]
	v_cvt_pk_f32_fp8_e32 v[184:185], v74
	v_cvt_pk_f32_fp8_sdwa v[186:187], v74 src0_sel:WORD_1
	v_pk_fma_f32 v[102:103], v[184:185], s[14:15], v[102:103] op_sel_hi:[1,0,1]
	v_pk_fma_f32 v[104:105], v[186:187], s[14:15], v[104:105] op_sel_hi:[1,0,1]
	v_cvt_pk_f32_fp8_e32 v[188:189], v75
	v_cvt_pk_f32_fp8_sdwa v[190:191], v75 src0_sel:WORD_1
	v_pk_fma_f32 v[106:107], v[188:189], s[14:15], v[106:107] op_sel_hi:[1,0,1]
	v_pk_fma_f32 v[108:109], v[190:191], s[14:15], v[108:109] op_sel_hi:[1,0,1]
	v_readlane_b32 s14, v1, 8
	v_cvt_pk_f32_fp8_e32 v[184:185], v52
	v_cvt_pk_f32_fp8_sdwa v[186:187], v52 src0_sel:WORD_1
	v_pk_fma_f32 v[94:95], v[184:185], s[14:15], v[94:95] op_sel_hi:[1,0,1]
	v_pk_fma_f32 v[96:97], v[186:187], s[14:15], v[96:97] op_sel_hi:[1,0,1]
	v_cvt_pk_f32_fp8_e32 v[188:189], v53
	v_cvt_pk_f32_fp8_sdwa v[190:191], v53 src0_sel:WORD_1
	v_pk_fma_f32 v[98:99], v[188:189], s[14:15], v[98:99] op_sel_hi:[1,0,1]
	v_pk_fma_f32 v[100:101], v[190:191], s[14:15], v[100:101] op_sel_hi:[1,0,1]
	v_cvt_pk_f32_fp8_e32 v[184:185], v54
	v_cvt_pk_f32_fp8_sdwa v[186:187], v54 src0_sel:WORD_1
	v_pk_fma_f32 v[102:103], v[184:185], s[14:15], v[102:103] op_sel_hi:[1,0,1]
	v_pk_fma_f32 v[104:105], v[186:187], s[14:15], v[104:105] op_sel_hi:[1,0,1]
	v_cvt_pk_f32_fp8_e32 v[188:189], v55
	v_cvt_pk_f32_fp8_sdwa v[190:191], v55 src0_sel:WORD_1
	v_pk_fma_f32 v[106:107], v[188:189], s[14:15], v[106:107] op_sel_hi:[1,0,1]
	v_pk_fma_f32 v[108:109], v[190:191], s[14:15], v[108:109] op_sel_hi:[1,0,1]
	v_readlane_b32 s14, v1, 16
	v_cvt_pk_f32_fp8_e32 v[184:185], v44
	v_cvt_pk_f32_fp8_sdwa v[186:187], v44 src0_sel:WORD_1
	v_pk_fma_f32 v[94:95], v[184:185], s[14:15], v[94:95] op_sel_hi:[1,0,1]
	v_pk_fma_f32 v[96:97], v[186:187], s[14:15], v[96:97] op_sel_hi:[1,0,1]
	v_cvt_pk_f32_fp8_e32 v[188:189], v45
	v_cvt_pk_f32_fp8_sdwa v[190:191], v45 src0_sel:WORD_1
	v_pk_fma_f32 v[98:99], v[188:189], s[14:15], v[98:99] op_sel_hi:[1,0,1]
	v_pk_fma_f32 v[100:101], v[190:191], s[14:15], v[100:101] op_sel_hi:[1,0,1]
	v_cvt_pk_f32_fp8_e32 v[184:185], v46
	v_cvt_pk_f32_fp8_sdwa v[186:187], v46 src0_sel:WORD_1
	v_pk_fma_f32 v[102:103], v[184:185], s[14:15], v[102:103] op_sel_hi:[1,0,1]
	v_pk_fma_f32 v[104:105], v[186:187], s[14:15], v[104:105] op_sel_hi:[1,0,1]
	v_cvt_pk_f32_fp8_e32 v[188:189], v47
	v_cvt_pk_f32_fp8_sdwa v[190:191], v47 src0_sel:WORD_1
	v_pk_fma_f32 v[106:107], v[188:189], s[14:15], v[106:107] op_sel_hi:[1,0,1]
	v_pk_fma_f32 v[108:109], v[190:191], s[14:15], v[108:109] op_sel_hi:[1,0,1]
	v_readlane_b32 s14, v1, 24
	v_cvt_pk_f32_fp8_e32 v[184:185], v40
	v_cvt_pk_f32_fp8_sdwa v[186:187], v40 src0_sel:WORD_1
	v_pk_fma_f32 v[94:95], v[184:185], s[14:15], v[94:95] op_sel_hi:[1,0,1]
	v_pk_fma_f32 v[96:97], v[186:187], s[14:15], v[96:97] op_sel_hi:[1,0,1]
	v_cvt_pk_f32_fp8_e32 v[188:189], v41
	v_cvt_pk_f32_fp8_sdwa v[190:191], v41 src0_sel:WORD_1
	v_pk_fma_f32 v[98:99], v[188:189], s[14:15], v[98:99] op_sel_hi:[1,0,1]
	v_pk_fma_f32 v[100:101], v[190:191], s[14:15], v[100:101] op_sel_hi:[1,0,1]
	v_cvt_pk_f32_fp8_e32 v[184:185], v42
	v_cvt_pk_f32_fp8_sdwa v[186:187], v42 src0_sel:WORD_1
	v_pk_fma_f32 v[102:103], v[184:185], s[14:15], v[102:103] op_sel_hi:[1,0,1]
	v_pk_fma_f32 v[104:105], v[186:187], s[14:15], v[104:105] op_sel_hi:[1,0,1]
	v_cvt_pk_f32_fp8_e32 v[188:189], v43
	v_cvt_pk_f32_fp8_sdwa v[190:191], v43 src0_sel:WORD_1
	v_pk_fma_f32 v[106:107], v[188:189], s[14:15], v[106:107] op_sel_hi:[1,0,1]
	v_pk_fma_f32 v[108:109], v[190:191], s[14:15], v[108:109] op_sel_hi:[1,0,1]
	v_readlane_b32 s14, v1, 32
	v_cvt_pk_f32_fp8_e32 v[184:185], v36
	v_cvt_pk_f32_fp8_sdwa v[186:187], v36 src0_sel:WORD_1
	v_pk_fma_f32 v[94:95], v[184:185], s[14:15], v[94:95] op_sel_hi:[1,0,1]
	v_pk_fma_f32 v[96:97], v[186:187], s[14:15], v[96:97] op_sel_hi:[1,0,1]
	v_cvt_pk_f32_fp8_e32 v[188:189], v37
	v_cvt_pk_f32_fp8_sdwa v[190:191], v37 src0_sel:WORD_1
	v_pk_fma_f32 v[98:99], v[188:189], s[14:15], v[98:99] op_sel_hi:[1,0,1]
	v_pk_fma_f32 v[100:101], v[190:191], s[14:15], v[100:101] op_sel_hi:[1,0,1]
	v_cvt_pk_f32_fp8_e32 v[184:185], v38
	v_cvt_pk_f32_fp8_sdwa v[186:187], v38 src0_sel:WORD_1
	v_pk_fma_f32 v[102:103], v[184:185], s[14:15], v[102:103] op_sel_hi:[1,0,1]
	v_pk_fma_f32 v[104:105], v[186:187], s[14:15], v[104:105] op_sel_hi:[1,0,1]
	v_cvt_pk_f32_fp8_e32 v[188:189], v39
	v_cvt_pk_f32_fp8_sdwa v[190:191], v39 src0_sel:WORD_1
	v_pk_fma_f32 v[106:107], v[188:189], s[14:15], v[106:107] op_sel_hi:[1,0,1]
	v_pk_fma_f32 v[108:109], v[190:191], s[14:15], v[108:109] op_sel_hi:[1,0,1]
	v_readlane_b32 s14, v1, 40
	v_cvt_pk_f32_fp8_e32 v[184:185], v28
	v_cvt_pk_f32_fp8_sdwa v[186:187], v28 src0_sel:WORD_1
	v_pk_fma_f32 v[94:95], v[184:185], s[14:15], v[94:95] op_sel_hi:[1,0,1]
	v_pk_fma_f32 v[96:97], v[186:187], s[14:15], v[96:97] op_sel_hi:[1,0,1]
	v_cvt_pk_f32_fp8_e32 v[188:189], v29
	v_cvt_pk_f32_fp8_sdwa v[190:191], v29 src0_sel:WORD_1
	v_pk_fma_f32 v[98:99], v[188:189], s[14:15], v[98:99] op_sel_hi:[1,0,1]
	v_pk_fma_f32 v[100:101], v[190:191], s[14:15], v[100:101] op_sel_hi:[1,0,1]
	v_cvt_pk_f32_fp8_e32 v[184:185], v30
	v_cvt_pk_f32_fp8_sdwa v[186:187], v30 src0_sel:WORD_1
	v_pk_fma_f32 v[102:103], v[184:185], s[14:15], v[102:103] op_sel_hi:[1,0,1]
	v_pk_fma_f32 v[104:105], v[186:187], s[14:15], v[104:105] op_sel_hi:[1,0,1]
	v_cvt_pk_f32_fp8_e32 v[188:189], v31
	v_cvt_pk_f32_fp8_sdwa v[190:191], v31 src0_sel:WORD_1
	v_pk_fma_f32 v[106:107], v[188:189], s[14:15], v[106:107] op_sel_hi:[1,0,1]
	v_pk_fma_f32 v[108:109], v[190:191], s[14:15], v[108:109] op_sel_hi:[1,0,1]
	v_readlane_b32 s14, v1, 48
	v_cvt_pk_f32_fp8_e32 v[184:185], v24
	v_cvt_pk_f32_fp8_sdwa v[186:187], v24 src0_sel:WORD_1
	v_pk_fma_f32 v[94:95], v[184:185], s[14:15], v[94:95] op_sel_hi:[1,0,1]
	v_pk_fma_f32 v[96:97], v[186:187], s[14:15], v[96:97] op_sel_hi:[1,0,1]
	v_cvt_pk_f32_fp8_e32 v[188:189], v25
	v_cvt_pk_f32_fp8_sdwa v[190:191], v25 src0_sel:WORD_1
	v_pk_fma_f32 v[98:99], v[188:189], s[14:15], v[98:99] op_sel_hi:[1,0,1]
	v_pk_fma_f32 v[100:101], v[190:191], s[14:15], v[100:101] op_sel_hi:[1,0,1]
	v_cvt_pk_f32_fp8_e32 v[184:185], v26
	v_cvt_pk_f32_fp8_sdwa v[186:187], v26 src0_sel:WORD_1
	v_pk_fma_f32 v[102:103], v[184:185], s[14:15], v[102:103] op_sel_hi:[1,0,1]
	v_pk_fma_f32 v[104:105], v[186:187], s[14:15], v[104:105] op_sel_hi:[1,0,1]
	v_cvt_pk_f32_fp8_e32 v[188:189], v27
	v_cvt_pk_f32_fp8_sdwa v[190:191], v27 src0_sel:WORD_1
	v_pk_fma_f32 v[106:107], v[188:189], s[14:15], v[106:107] op_sel_hi:[1,0,1]
	v_pk_fma_f32 v[108:109], v[190:191], s[14:15], v[108:109] op_sel_hi:[1,0,1]
	v_readlane_b32 s14, v1, 56
	v_cvt_pk_f32_fp8_e32 v[184:185], v20
	v_cvt_pk_f32_fp8_sdwa v[186:187], v20 src0_sel:WORD_1
	v_pk_fma_f32 v[94:95], v[184:185], s[14:15], v[94:95] op_sel_hi:[1,0,1]
	v_pk_fma_f32 v[96:97], v[186:187], s[14:15], v[96:97] op_sel_hi:[1,0,1]
	v_cvt_pk_f32_fp8_e32 v[188:189], v21
	v_cvt_pk_f32_fp8_sdwa v[190:191], v21 src0_sel:WORD_1
	v_pk_fma_f32 v[98:99], v[188:189], s[14:15], v[98:99] op_sel_hi:[1,0,1]
	v_pk_fma_f32 v[100:101], v[190:191], s[14:15], v[100:101] op_sel_hi:[1,0,1]
	v_cvt_pk_f32_fp8_e32 v[184:185], v22
	v_cvt_pk_f32_fp8_sdwa v[186:187], v22 src0_sel:WORD_1
	v_pk_fma_f32 v[102:103], v[184:185], s[14:15], v[102:103] op_sel_hi:[1,0,1]
	v_pk_fma_f32 v[104:105], v[186:187], s[14:15], v[104:105] op_sel_hi:[1,0,1]
	v_cvt_pk_f32_fp8_e32 v[188:189], v23
	v_cvt_pk_f32_fp8_sdwa v[190:191], v23 src0_sel:WORD_1
	v_pk_fma_f32 v[106:107], v[188:189], s[14:15], v[106:107] op_sel_hi:[1,0,1]
	v_pk_fma_f32 v[108:109], v[190:191], s[14:15], v[108:109] op_sel_hi:[1,0,1]
	s_branch .Lp6c1_axdone
.Lp6c1_t3:
	v_readlane_b32 s14, v1, 0
	v_cvt_pk_f32_fp8_e32 v[184:185], v72
	v_cvt_pk_f32_fp8_sdwa v[186:187], v72 src0_sel:WORD_1
	v_pk_fma_f32 v[78:79], v[184:185], s[14:15], v[78:79] op_sel_hi:[1,0,1]
	v_pk_fma_f32 v[80:81], v[186:187], s[14:15], v[80:81] op_sel_hi:[1,0,1]
	v_cvt_pk_f32_fp8_e32 v[188:189], v73
	v_cvt_pk_f32_fp8_sdwa v[190:191], v73 src0_sel:WORD_1
	v_pk_fma_f32 v[82:83], v[188:189], s[14:15], v[82:83] op_sel_hi:[1,0,1]
	v_pk_fma_f32 v[86:87], v[190:191], s[14:15], v[86:87] op_sel_hi:[1,0,1]
	v_cvt_pk_f32_fp8_e32 v[184:185], v74
	v_cvt_pk_f32_fp8_sdwa v[186:187], v74 src0_sel:WORD_1
	v_pk_fma_f32 v[88:89], v[184:185], s[14:15], v[88:89] op_sel_hi:[1,0,1]
	v_pk_fma_f32 v[90:91], v[186:187], s[14:15], v[90:91] op_sel_hi:[1,0,1]
	v_cvt_pk_f32_fp8_e32 v[188:189], v75
	v_cvt_pk_f32_fp8_sdwa v[190:191], v75 src0_sel:WORD_1
	v_pk_fma_f32 v[92:93], v[188:189], s[14:15], v[92:93] op_sel_hi:[1,0,1]
	v_pk_fma_f32 v[84:85], v[190:191], s[14:15], v[84:85] op_sel_hi:[1,0,1]
	v_readlane_b32 s14, v1, 8
	v_cvt_pk_f32_fp8_e32 v[184:185], v52
	v_cvt_pk_f32_fp8_sdwa v[186:187], v52 src0_sel:WORD_1
	v_pk_fma_f32 v[78:79], v[184:185], s[14:15], v[78:79] op_sel_hi:[1,0,1]
	v_pk_fma_f32 v[80:81], v[186:187], s[14:15], v[80:81] op_sel_hi:[1,0,1]
	v_cvt_pk_f32_fp8_e32 v[188:189], v53
	v_cvt_pk_f32_fp8_sdwa v[190:191], v53 src0_sel:WORD_1
	v_pk_fma_f32 v[82:83], v[188:189], s[14:15], v[82:83] op_sel_hi:[1,0,1]
	v_pk_fma_f32 v[86:87], v[190:191], s[14:15], v[86:87] op_sel_hi:[1,0,1]
	v_cvt_pk_f32_fp8_e32 v[184:185], v54
	v_cvt_pk_f32_fp8_sdwa v[186:187], v54 src0_sel:WORD_1
	v_pk_fma_f32 v[88:89], v[184:185], s[14:15], v[88:89] op_sel_hi:[1,0,1]
	v_pk_fma_f32 v[90:91], v[186:187], s[14:15], v[90:91] op_sel_hi:[1,0,1]
	v_cvt_pk_f32_fp8_e32 v[188:189], v55
	v_cvt_pk_f32_fp8_sdwa v[190:191], v55 src0_sel:WORD_1
	v_pk_fma_f32 v[92:93], v[188:189], s[14:15], v[92:93] op_sel_hi:[1,0,1]
	v_pk_fma_f32 v[84:85], v[190:191], s[14:15], v[84:85] op_sel_hi:[1,0,1]
	v_readlane_b32 s14, v1, 16
	v_cvt_pk_f32_fp8_e32 v[184:185], v44
	v_cvt_pk_f32_fp8_sdwa v[186:187], v44 src0_sel:WORD_1
	v_pk_fma_f32 v[78:79], v[184:185], s[14:15], v[78:79] op_sel_hi:[1,0,1]
	v_pk_fma_f32 v[80:81], v[186:187], s[14:15], v[80:81] op_sel_hi:[1,0,1]
	v_cvt_pk_f32_fp8_e32 v[188:189], v45
	v_cvt_pk_f32_fp8_sdwa v[190:191], v45 src0_sel:WORD_1
	v_pk_fma_f32 v[82:83], v[188:189], s[14:15], v[82:83] op_sel_hi:[1,0,1]
	v_pk_fma_f32 v[86:87], v[190:191], s[14:15], v[86:87] op_sel_hi:[1,0,1]
	v_cvt_pk_f32_fp8_e32 v[184:185], v46
	v_cvt_pk_f32_fp8_sdwa v[186:187], v46 src0_sel:WORD_1
	v_pk_fma_f32 v[88:89], v[184:185], s[14:15], v[88:89] op_sel_hi:[1,0,1]
	v_pk_fma_f32 v[90:91], v[186:187], s[14:15], v[90:91] op_sel_hi:[1,0,1]
	v_cvt_pk_f32_fp8_e32 v[188:189], v47
	v_cvt_pk_f32_fp8_sdwa v[190:191], v47 src0_sel:WORD_1
	v_pk_fma_f32 v[92:93], v[188:189], s[14:15], v[92:93] op_sel_hi:[1,0,1]
	v_pk_fma_f32 v[84:85], v[190:191], s[14:15], v[84:85] op_sel_hi:[1,0,1]
	v_readlane_b32 s14, v1, 24
	v_cvt_pk_f32_fp8_e32 v[184:185], v40
	v_cvt_pk_f32_fp8_sdwa v[186:187], v40 src0_sel:WORD_1
	v_pk_fma_f32 v[78:79], v[184:185], s[14:15], v[78:79] op_sel_hi:[1,0,1]
	v_pk_fma_f32 v[80:81], v[186:187], s[14:15], v[80:81] op_sel_hi:[1,0,1]
	v_cvt_pk_f32_fp8_e32 v[188:189], v41
	v_cvt_pk_f32_fp8_sdwa v[190:191], v41 src0_sel:WORD_1
	v_pk_fma_f32 v[82:83], v[188:189], s[14:15], v[82:83] op_sel_hi:[1,0,1]
	v_pk_fma_f32 v[86:87], v[190:191], s[14:15], v[86:87] op_sel_hi:[1,0,1]
	v_cvt_pk_f32_fp8_e32 v[184:185], v42
	v_cvt_pk_f32_fp8_sdwa v[186:187], v42 src0_sel:WORD_1
	v_pk_fma_f32 v[88:89], v[184:185], s[14:15], v[88:89] op_sel_hi:[1,0,1]
	v_pk_fma_f32 v[90:91], v[186:187], s[14:15], v[90:91] op_sel_hi:[1,0,1]
	v_cvt_pk_f32_fp8_e32 v[188:189], v43
	v_cvt_pk_f32_fp8_sdwa v[190:191], v43 src0_sel:WORD_1
	v_pk_fma_f32 v[92:93], v[188:189], s[14:15], v[92:93] op_sel_hi:[1,0,1]
	v_pk_fma_f32 v[84:85], v[190:191], s[14:15], v[84:85] op_sel_hi:[1,0,1]
	v_readlane_b32 s14, v1, 32
	v_cvt_pk_f32_fp8_e32 v[184:185], v36
	v_cvt_pk_f32_fp8_sdwa v[186:187], v36 src0_sel:WORD_1
	v_pk_fma_f32 v[78:79], v[184:185], s[14:15], v[78:79] op_sel_hi:[1,0,1]
	v_pk_fma_f32 v[80:81], v[186:187], s[14:15], v[80:81] op_sel_hi:[1,0,1]
	v_cvt_pk_f32_fp8_e32 v[188:189], v37
	v_cvt_pk_f32_fp8_sdwa v[190:191], v37 src0_sel:WORD_1
	v_pk_fma_f32 v[82:83], v[188:189], s[14:15], v[82:83] op_sel_hi:[1,0,1]
	v_pk_fma_f32 v[86:87], v[190:191], s[14:15], v[86:87] op_sel_hi:[1,0,1]
	v_cvt_pk_f32_fp8_e32 v[184:185], v38
	v_cvt_pk_f32_fp8_sdwa v[186:187], v38 src0_sel:WORD_1
	v_pk_fma_f32 v[88:89], v[184:185], s[14:15], v[88:89] op_sel_hi:[1,0,1]
	v_pk_fma_f32 v[90:91], v[186:187], s[14:15], v[90:91] op_sel_hi:[1,0,1]
	v_cvt_pk_f32_fp8_e32 v[188:189], v39
	v_cvt_pk_f32_fp8_sdwa v[190:191], v39 src0_sel:WORD_1
	v_pk_fma_f32 v[92:93], v[188:189], s[14:15], v[92:93] op_sel_hi:[1,0,1]
	v_pk_fma_f32 v[84:85], v[190:191], s[14:15], v[84:85] op_sel_hi:[1,0,1]
	v_readlane_b32 s14, v1, 40
	v_cvt_pk_f32_fp8_e32 v[184:185], v28
	v_cvt_pk_f32_fp8_sdwa v[186:187], v28 src0_sel:WORD_1
	v_pk_fma_f32 v[78:79], v[184:185], s[14:15], v[78:79] op_sel_hi:[1,0,1]
	v_pk_fma_f32 v[80:81], v[186:187], s[14:15], v[80:81] op_sel_hi:[1,0,1]
	v_cvt_pk_f32_fp8_e32 v[188:189], v29
	v_cvt_pk_f32_fp8_sdwa v[190:191], v29 src0_sel:WORD_1
	v_pk_fma_f32 v[82:83], v[188:189], s[14:15], v[82:83] op_sel_hi:[1,0,1]
	v_pk_fma_f32 v[86:87], v[190:191], s[14:15], v[86:87] op_sel_hi:[1,0,1]
	v_cvt_pk_f32_fp8_e32 v[184:185], v30
	v_cvt_pk_f32_fp8_sdwa v[186:187], v30 src0_sel:WORD_1
	v_pk_fma_f32 v[88:89], v[184:185], s[14:15], v[88:89] op_sel_hi:[1,0,1]
	v_pk_fma_f32 v[90:91], v[186:187], s[14:15], v[90:91] op_sel_hi:[1,0,1]
	v_cvt_pk_f32_fp8_e32 v[188:189], v31
	v_cvt_pk_f32_fp8_sdwa v[190:191], v31 src0_sel:WORD_1
	v_pk_fma_f32 v[92:93], v[188:189], s[14:15], v[92:93] op_sel_hi:[1,0,1]
	v_pk_fma_f32 v[84:85], v[190:191], s[14:15], v[84:85] op_sel_hi:[1,0,1]
	v_readlane_b32 s14, v1, 48
	v_cvt_pk_f32_fp8_e32 v[184:185], v24
	v_cvt_pk_f32_fp8_sdwa v[186:187], v24 src0_sel:WORD_1
	v_pk_fma_f32 v[78:79], v[184:185], s[14:15], v[78:79] op_sel_hi:[1,0,1]
	v_pk_fma_f32 v[80:81], v[186:187], s[14:15], v[80:81] op_sel_hi:[1,0,1]
	v_cvt_pk_f32_fp8_e32 v[188:189], v25
	v_cvt_pk_f32_fp8_sdwa v[190:191], v25 src0_sel:WORD_1
	v_pk_fma_f32 v[82:83], v[188:189], s[14:15], v[82:83] op_sel_hi:[1,0,1]
	v_pk_fma_f32 v[86:87], v[190:191], s[14:15], v[86:87] op_sel_hi:[1,0,1]
	v_cvt_pk_f32_fp8_e32 v[184:185], v26
	v_cvt_pk_f32_fp8_sdwa v[186:187], v26 src0_sel:WORD_1
	v_pk_fma_f32 v[88:89], v[184:185], s[14:15], v[88:89] op_sel_hi:[1,0,1]
	v_pk_fma_f32 v[90:91], v[186:187], s[14:15], v[90:91] op_sel_hi:[1,0,1]
	v_cvt_pk_f32_fp8_e32 v[188:189], v27
	v_cvt_pk_f32_fp8_sdwa v[190:191], v27 src0_sel:WORD_1
	v_pk_fma_f32 v[92:93], v[188:189], s[14:15], v[92:93] op_sel_hi:[1,0,1]
	v_pk_fma_f32 v[84:85], v[190:191], s[14:15], v[84:85] op_sel_hi:[1,0,1]
	v_readlane_b32 s14, v1, 56
	v_cvt_pk_f32_fp8_e32 v[184:185], v20
	v_cvt_pk_f32_fp8_sdwa v[186:187], v20 src0_sel:WORD_1
	v_pk_fma_f32 v[78:79], v[184:185], s[14:15], v[78:79] op_sel_hi:[1,0,1]
	v_pk_fma_f32 v[80:81], v[186:187], s[14:15], v[80:81] op_sel_hi:[1,0,1]
	v_cvt_pk_f32_fp8_e32 v[188:189], v21
	v_cvt_pk_f32_fp8_sdwa v[190:191], v21 src0_sel:WORD_1
	v_pk_fma_f32 v[82:83], v[188:189], s[14:15], v[82:83] op_sel_hi:[1,0,1]
	v_pk_fma_f32 v[86:87], v[190:191], s[14:15], v[86:87] op_sel_hi:[1,0,1]
	v_cvt_pk_f32_fp8_e32 v[184:185], v22
	v_cvt_pk_f32_fp8_sdwa v[186:187], v22 src0_sel:WORD_1
	v_pk_fma_f32 v[88:89], v[184:185], s[14:15], v[88:89] op_sel_hi:[1,0,1]
	v_pk_fma_f32 v[90:91], v[186:187], s[14:15], v[90:91] op_sel_hi:[1,0,1]
	v_cvt_pk_f32_fp8_e32 v[188:189], v23
	v_cvt_pk_f32_fp8_sdwa v[190:191], v23 src0_sel:WORD_1
	v_pk_fma_f32 v[92:93], v[188:189], s[14:15], v[92:93] op_sel_hi:[1,0,1]
	v_pk_fma_f32 v[84:85], v[190:191], s[14:15], v[84:85] op_sel_hi:[1,0,1]
	s_branch .Lp6c1_axdone
.Lp6c1_t4:
	v_readlane_b32 s14, v1, 0
	v_cvt_pk_f32_fp8_e32 v[184:185], v72
	v_cvt_pk_f32_fp8_sdwa v[186:187], v72 src0_sel:WORD_1
	v_pk_fma_f32 v[144:145], v[184:185], s[14:15], v[144:145] op_sel_hi:[1,0,1]
	v_pk_fma_f32 v[146:147], v[186:187], s[14:15], v[146:147] op_sel_hi:[1,0,1]
	v_cvt_pk_f32_fp8_e32 v[188:189], v73
	v_cvt_pk_f32_fp8_sdwa v[190:191], v73 src0_sel:WORD_1
	v_pk_fma_f32 v[148:149], v[188:189], s[14:15], v[148:149] op_sel_hi:[1,0,1]
	v_pk_fma_f32 v[150:151], v[190:191], s[14:15], v[150:151] op_sel_hi:[1,0,1]
	v_cvt_pk_f32_fp8_e32 v[184:185], v74
	v_cvt_pk_f32_fp8_sdwa v[186:187], v74 src0_sel:WORD_1
	v_pk_fma_f32 v[152:153], v[184:185], s[14:15], v[152:153] op_sel_hi:[1,0,1]
	v_pk_fma_f32 v[154:155], v[186:187], s[14:15], v[154:155] op_sel_hi:[1,0,1]
	v_cvt_pk_f32_fp8_e32 v[188:189], v75
	v_cvt_pk_f32_fp8_sdwa v[190:191], v75 src0_sel:WORD_1
	v_pk_fma_f32 v[156:157], v[188:189], s[14:15], v[156:157] op_sel_hi:[1,0,1]
	v_pk_fma_f32 v[158:159], v[190:191], s[14:15], v[158:159] op_sel_hi:[1,0,1]
	v_readlane_b32 s14, v1, 8
	v_cvt_pk_f32_fp8_e32 v[184:185], v52
	v_cvt_pk_f32_fp8_sdwa v[186:187], v52 src0_sel:WORD_1
	v_pk_fma_f32 v[144:145], v[184:185], s[14:15], v[144:145] op_sel_hi:[1,0,1]
	v_pk_fma_f32 v[146:147], v[186:187], s[14:15], v[146:147] op_sel_hi:[1,0,1]
	v_cvt_pk_f32_fp8_e32 v[188:189], v53
	v_cvt_pk_f32_fp8_sdwa v[190:191], v53 src0_sel:WORD_1
	v_pk_fma_f32 v[148:149], v[188:189], s[14:15], v[148:149] op_sel_hi:[1,0,1]
	v_pk_fma_f32 v[150:151], v[190:191], s[14:15], v[150:151] op_sel_hi:[1,0,1]
	v_cvt_pk_f32_fp8_e32 v[184:185], v54
	v_cvt_pk_f32_fp8_sdwa v[186:187], v54 src0_sel:WORD_1
	v_pk_fma_f32 v[152:153], v[184:185], s[14:15], v[152:153] op_sel_hi:[1,0,1]
	v_pk_fma_f32 v[154:155], v[186:187], s[14:15], v[154:155] op_sel_hi:[1,0,1]
	v_cvt_pk_f32_fp8_e32 v[188:189], v55
	v_cvt_pk_f32_fp8_sdwa v[190:191], v55 src0_sel:WORD_1
	v_pk_fma_f32 v[156:157], v[188:189], s[14:15], v[156:157] op_sel_hi:[1,0,1]
	v_pk_fma_f32 v[158:159], v[190:191], s[14:15], v[158:159] op_sel_hi:[1,0,1]
	v_readlane_b32 s14, v1, 16
	v_cvt_pk_f32_fp8_e32 v[184:185], v44
	v_cvt_pk_f32_fp8_sdwa v[186:187], v44 src0_sel:WORD_1
	v_pk_fma_f32 v[144:145], v[184:185], s[14:15], v[144:145] op_sel_hi:[1,0,1]
	v_pk_fma_f32 v[146:147], v[186:187], s[14:15], v[146:147] op_sel_hi:[1,0,1]
	v_cvt_pk_f32_fp8_e32 v[188:189], v45
	v_cvt_pk_f32_fp8_sdwa v[190:191], v45 src0_sel:WORD_1
	v_pk_fma_f32 v[148:149], v[188:189], s[14:15], v[148:149] op_sel_hi:[1,0,1]
	v_pk_fma_f32 v[150:151], v[190:191], s[14:15], v[150:151] op_sel_hi:[1,0,1]
	v_cvt_pk_f32_fp8_e32 v[184:185], v46
	v_cvt_pk_f32_fp8_sdwa v[186:187], v46 src0_sel:WORD_1
	v_pk_fma_f32 v[152:153], v[184:185], s[14:15], v[152:153] op_sel_hi:[1,0,1]
	v_pk_fma_f32 v[154:155], v[186:187], s[14:15], v[154:155] op_sel_hi:[1,0,1]
	v_cvt_pk_f32_fp8_e32 v[188:189], v47
	v_cvt_pk_f32_fp8_sdwa v[190:191], v47 src0_sel:WORD_1
	v_pk_fma_f32 v[156:157], v[188:189], s[14:15], v[156:157] op_sel_hi:[1,0,1]
	v_pk_fma_f32 v[158:159], v[190:191], s[14:15], v[158:159] op_sel_hi:[1,0,1]
	v_readlane_b32 s14, v1, 24
	v_cvt_pk_f32_fp8_e32 v[184:185], v40
	v_cvt_pk_f32_fp8_sdwa v[186:187], v40 src0_sel:WORD_1
	v_pk_fma_f32 v[144:145], v[184:185], s[14:15], v[144:145] op_sel_hi:[1,0,1]
	v_pk_fma_f32 v[146:147], v[186:187], s[14:15], v[146:147] op_sel_hi:[1,0,1]
	v_cvt_pk_f32_fp8_e32 v[188:189], v41
	v_cvt_pk_f32_fp8_sdwa v[190:191], v41 src0_sel:WORD_1
	v_pk_fma_f32 v[148:149], v[188:189], s[14:15], v[148:149] op_sel_hi:[1,0,1]
	v_pk_fma_f32 v[150:151], v[190:191], s[14:15], v[150:151] op_sel_hi:[1,0,1]
	v_cvt_pk_f32_fp8_e32 v[184:185], v42
	v_cvt_pk_f32_fp8_sdwa v[186:187], v42 src0_sel:WORD_1
	v_pk_fma_f32 v[152:153], v[184:185], s[14:15], v[152:153] op_sel_hi:[1,0,1]
	v_pk_fma_f32 v[154:155], v[186:187], s[14:15], v[154:155] op_sel_hi:[1,0,1]
	v_cvt_pk_f32_fp8_e32 v[188:189], v43
	v_cvt_pk_f32_fp8_sdwa v[190:191], v43 src0_sel:WORD_1
	v_pk_fma_f32 v[156:157], v[188:189], s[14:15], v[156:157] op_sel_hi:[1,0,1]
	v_pk_fma_f32 v[158:159], v[190:191], s[14:15], v[158:159] op_sel_hi:[1,0,1]
	v_readlane_b32 s14, v1, 32
	v_cvt_pk_f32_fp8_e32 v[184:185], v36
	v_cvt_pk_f32_fp8_sdwa v[186:187], v36 src0_sel:WORD_1
	v_pk_fma_f32 v[144:145], v[184:185], s[14:15], v[144:145] op_sel_hi:[1,0,1]
	v_pk_fma_f32 v[146:147], v[186:187], s[14:15], v[146:147] op_sel_hi:[1,0,1]
	v_cvt_pk_f32_fp8_e32 v[188:189], v37
	v_cvt_pk_f32_fp8_sdwa v[190:191], v37 src0_sel:WORD_1
	v_pk_fma_f32 v[148:149], v[188:189], s[14:15], v[148:149] op_sel_hi:[1,0,1]
	v_pk_fma_f32 v[150:151], v[190:191], s[14:15], v[150:151] op_sel_hi:[1,0,1]
	v_cvt_pk_f32_fp8_e32 v[184:185], v38
	v_cvt_pk_f32_fp8_sdwa v[186:187], v38 src0_sel:WORD_1
	v_pk_fma_f32 v[152:153], v[184:185], s[14:15], v[152:153] op_sel_hi:[1,0,1]
	v_pk_fma_f32 v[154:155], v[186:187], s[14:15], v[154:155] op_sel_hi:[1,0,1]
	v_cvt_pk_f32_fp8_e32 v[188:189], v39
	v_cvt_pk_f32_fp8_sdwa v[190:191], v39 src0_sel:WORD_1
	v_pk_fma_f32 v[156:157], v[188:189], s[14:15], v[156:157] op_sel_hi:[1,0,1]
	v_pk_fma_f32 v[158:159], v[190:191], s[14:15], v[158:159] op_sel_hi:[1,0,1]
	v_readlane_b32 s14, v1, 40
	v_cvt_pk_f32_fp8_e32 v[184:185], v28
	v_cvt_pk_f32_fp8_sdwa v[186:187], v28 src0_sel:WORD_1
	v_pk_fma_f32 v[144:145], v[184:185], s[14:15], v[144:145] op_sel_hi:[1,0,1]
	v_pk_fma_f32 v[146:147], v[186:187], s[14:15], v[146:147] op_sel_hi:[1,0,1]
	v_cvt_pk_f32_fp8_e32 v[188:189], v29
	v_cvt_pk_f32_fp8_sdwa v[190:191], v29 src0_sel:WORD_1
	v_pk_fma_f32 v[148:149], v[188:189], s[14:15], v[148:149] op_sel_hi:[1,0,1]
	v_pk_fma_f32 v[150:151], v[190:191], s[14:15], v[150:151] op_sel_hi:[1,0,1]
	v_cvt_pk_f32_fp8_e32 v[184:185], v30
	v_cvt_pk_f32_fp8_sdwa v[186:187], v30 src0_sel:WORD_1
	v_pk_fma_f32 v[152:153], v[184:185], s[14:15], v[152:153] op_sel_hi:[1,0,1]
	v_pk_fma_f32 v[154:155], v[186:187], s[14:15], v[154:155] op_sel_hi:[1,0,1]
	v_cvt_pk_f32_fp8_e32 v[188:189], v31
	v_cvt_pk_f32_fp8_sdwa v[190:191], v31 src0_sel:WORD_1
	v_pk_fma_f32 v[156:157], v[188:189], s[14:15], v[156:157] op_sel_hi:[1,0,1]
	v_pk_fma_f32 v[158:159], v[190:191], s[14:15], v[158:159] op_sel_hi:[1,0,1]
	v_readlane_b32 s14, v1, 48
	v_cvt_pk_f32_fp8_e32 v[184:185], v24
	v_cvt_pk_f32_fp8_sdwa v[186:187], v24 src0_sel:WORD_1
	v_pk_fma_f32 v[144:145], v[184:185], s[14:15], v[144:145] op_sel_hi:[1,0,1]
	v_pk_fma_f32 v[146:147], v[186:187], s[14:15], v[146:147] op_sel_hi:[1,0,1]
	v_cvt_pk_f32_fp8_e32 v[188:189], v25
	v_cvt_pk_f32_fp8_sdwa v[190:191], v25 src0_sel:WORD_1
	v_pk_fma_f32 v[148:149], v[188:189], s[14:15], v[148:149] op_sel_hi:[1,0,1]
	v_pk_fma_f32 v[150:151], v[190:191], s[14:15], v[150:151] op_sel_hi:[1,0,1]
	v_cvt_pk_f32_fp8_e32 v[184:185], v26
	v_cvt_pk_f32_fp8_sdwa v[186:187], v26 src0_sel:WORD_1
	v_pk_fma_f32 v[152:153], v[184:185], s[14:15], v[152:153] op_sel_hi:[1,0,1]
	v_pk_fma_f32 v[154:155], v[186:187], s[14:15], v[154:155] op_sel_hi:[1,0,1]
	v_cvt_pk_f32_fp8_e32 v[188:189], v27
	v_cvt_pk_f32_fp8_sdwa v[190:191], v27 src0_sel:WORD_1
	v_pk_fma_f32 v[156:157], v[188:189], s[14:15], v[156:157] op_sel_hi:[1,0,1]
	v_pk_fma_f32 v[158:159], v[190:191], s[14:15], v[158:159] op_sel_hi:[1,0,1]
	v_readlane_b32 s14, v1, 56
	v_cvt_pk_f32_fp8_e32 v[184:185], v20
	v_cvt_pk_f32_fp8_sdwa v[186:187], v20 src0_sel:WORD_1
	v_pk_fma_f32 v[144:145], v[184:185], s[14:15], v[144:145] op_sel_hi:[1,0,1]
	v_pk_fma_f32 v[146:147], v[186:187], s[14:15], v[146:147] op_sel_hi:[1,0,1]
	v_cvt_pk_f32_fp8_e32 v[188:189], v21
	v_cvt_pk_f32_fp8_sdwa v[190:191], v21 src0_sel:WORD_1
	v_pk_fma_f32 v[148:149], v[188:189], s[14:15], v[148:149] op_sel_hi:[1,0,1]
	v_pk_fma_f32 v[150:151], v[190:191], s[14:15], v[150:151] op_sel_hi:[1,0,1]
	v_cvt_pk_f32_fp8_e32 v[184:185], v22
	v_cvt_pk_f32_fp8_sdwa v[186:187], v22 src0_sel:WORD_1
	v_pk_fma_f32 v[152:153], v[184:185], s[14:15], v[152:153] op_sel_hi:[1,0,1]
	v_pk_fma_f32 v[154:155], v[186:187], s[14:15], v[154:155] op_sel_hi:[1,0,1]
	v_cvt_pk_f32_fp8_e32 v[188:189], v23
	v_cvt_pk_f32_fp8_sdwa v[190:191], v23 src0_sel:WORD_1
	v_pk_fma_f32 v[156:157], v[188:189], s[14:15], v[156:157] op_sel_hi:[1,0,1]
	v_pk_fma_f32 v[158:159], v[190:191], s[14:15], v[158:159] op_sel_hi:[1,0,1]
	s_branch .Lp6c1_axdone
.Lp6c1_t5:
	v_readlane_b32 s14, v1, 0
	v_cvt_pk_f32_fp8_e32 v[184:185], v72
	v_cvt_pk_f32_fp8_sdwa v[186:187], v72 src0_sel:WORD_1
	v_pk_fma_f32 v[160:161], v[184:185], s[14:15], v[160:161] op_sel_hi:[1,0,1]
	v_pk_fma_f32 v[162:163], v[186:187], s[14:15], v[162:163] op_sel_hi:[1,0,1]
	v_cvt_pk_f32_fp8_e32 v[188:189], v73
	v_cvt_pk_f32_fp8_sdwa v[190:191], v73 src0_sel:WORD_1
	v_pk_fma_f32 v[164:165], v[188:189], s[14:15], v[164:165] op_sel_hi:[1,0,1]
	v_pk_fma_f32 v[166:167], v[190:191], s[14:15], v[166:167] op_sel_hi:[1,0,1]
	v_cvt_pk_f32_fp8_e32 v[184:185], v74
	v_cvt_pk_f32_fp8_sdwa v[186:187], v74 src0_sel:WORD_1
	v_pk_fma_f32 v[168:169], v[184:185], s[14:15], v[168:169] op_sel_hi:[1,0,1]
	v_pk_fma_f32 v[170:171], v[186:187], s[14:15], v[170:171] op_sel_hi:[1,0,1]
	v_cvt_pk_f32_fp8_e32 v[188:189], v75
	v_cvt_pk_f32_fp8_sdwa v[190:191], v75 src0_sel:WORD_1
	v_pk_fma_f32 v[172:173], v[188:189], s[14:15], v[172:173] op_sel_hi:[1,0,1]
	v_pk_fma_f32 v[174:175], v[190:191], s[14:15], v[174:175] op_sel_hi:[1,0,1]
	v_readlane_b32 s14, v1, 8
	v_cvt_pk_f32_fp8_e32 v[184:185], v52
	v_cvt_pk_f32_fp8_sdwa v[186:187], v52 src0_sel:WORD_1
	v_pk_fma_f32 v[160:161], v[184:185], s[14:15], v[160:161] op_sel_hi:[1,0,1]
	v_pk_fma_f32 v[162:163], v[186:187], s[14:15], v[162:163] op_sel_hi:[1,0,1]
	v_cvt_pk_f32_fp8_e32 v[188:189], v53
	v_cvt_pk_f32_fp8_sdwa v[190:191], v53 src0_sel:WORD_1
	v_pk_fma_f32 v[164:165], v[188:189], s[14:15], v[164:165] op_sel_hi:[1,0,1]
	v_pk_fma_f32 v[166:167], v[190:191], s[14:15], v[166:167] op_sel_hi:[1,0,1]
	v_cvt_pk_f32_fp8_e32 v[184:185], v54
	v_cvt_pk_f32_fp8_sdwa v[186:187], v54 src0_sel:WORD_1
	v_pk_fma_f32 v[168:169], v[184:185], s[14:15], v[168:169] op_sel_hi:[1,0,1]
	v_pk_fma_f32 v[170:171], v[186:187], s[14:15], v[170:171] op_sel_hi:[1,0,1]
	v_cvt_pk_f32_fp8_e32 v[188:189], v55
	v_cvt_pk_f32_fp8_sdwa v[190:191], v55 src0_sel:WORD_1
	v_pk_fma_f32 v[172:173], v[188:189], s[14:15], v[172:173] op_sel_hi:[1,0,1]
	v_pk_fma_f32 v[174:175], v[190:191], s[14:15], v[174:175] op_sel_hi:[1,0,1]
	v_readlane_b32 s14, v1, 16
	v_cvt_pk_f32_fp8_e32 v[184:185], v44
	v_cvt_pk_f32_fp8_sdwa v[186:187], v44 src0_sel:WORD_1
	v_pk_fma_f32 v[160:161], v[184:185], s[14:15], v[160:161] op_sel_hi:[1,0,1]
	v_pk_fma_f32 v[162:163], v[186:187], s[14:15], v[162:163] op_sel_hi:[1,0,1]
	v_cvt_pk_f32_fp8_e32 v[188:189], v45
	v_cvt_pk_f32_fp8_sdwa v[190:191], v45 src0_sel:WORD_1
	v_pk_fma_f32 v[164:165], v[188:189], s[14:15], v[164:165] op_sel_hi:[1,0,1]
	v_pk_fma_f32 v[166:167], v[190:191], s[14:15], v[166:167] op_sel_hi:[1,0,1]
	v_cvt_pk_f32_fp8_e32 v[184:185], v46
	v_cvt_pk_f32_fp8_sdwa v[186:187], v46 src0_sel:WORD_1
	v_pk_fma_f32 v[168:169], v[184:185], s[14:15], v[168:169] op_sel_hi:[1,0,1]
	v_pk_fma_f32 v[170:171], v[186:187], s[14:15], v[170:171] op_sel_hi:[1,0,1]
	v_cvt_pk_f32_fp8_e32 v[188:189], v47
	v_cvt_pk_f32_fp8_sdwa v[190:191], v47 src0_sel:WORD_1
	v_pk_fma_f32 v[172:173], v[188:189], s[14:15], v[172:173] op_sel_hi:[1,0,1]
	v_pk_fma_f32 v[174:175], v[190:191], s[14:15], v[174:175] op_sel_hi:[1,0,1]
	v_readlane_b32 s14, v1, 24
	v_cvt_pk_f32_fp8_e32 v[184:185], v40
	v_cvt_pk_f32_fp8_sdwa v[186:187], v40 src0_sel:WORD_1
	v_pk_fma_f32 v[160:161], v[184:185], s[14:15], v[160:161] op_sel_hi:[1,0,1]
	v_pk_fma_f32 v[162:163], v[186:187], s[14:15], v[162:163] op_sel_hi:[1,0,1]
	v_cvt_pk_f32_fp8_e32 v[188:189], v41
	v_cvt_pk_f32_fp8_sdwa v[190:191], v41 src0_sel:WORD_1
	v_pk_fma_f32 v[164:165], v[188:189], s[14:15], v[164:165] op_sel_hi:[1,0,1]
	v_pk_fma_f32 v[166:167], v[190:191], s[14:15], v[166:167] op_sel_hi:[1,0,1]
	v_cvt_pk_f32_fp8_e32 v[184:185], v42
	v_cvt_pk_f32_fp8_sdwa v[186:187], v42 src0_sel:WORD_1
	v_pk_fma_f32 v[168:169], v[184:185], s[14:15], v[168:169] op_sel_hi:[1,0,1]
	v_pk_fma_f32 v[170:171], v[186:187], s[14:15], v[170:171] op_sel_hi:[1,0,1]
	v_cvt_pk_f32_fp8_e32 v[188:189], v43
	v_cvt_pk_f32_fp8_sdwa v[190:191], v43 src0_sel:WORD_1
	v_pk_fma_f32 v[172:173], v[188:189], s[14:15], v[172:173] op_sel_hi:[1,0,1]
	v_pk_fma_f32 v[174:175], v[190:191], s[14:15], v[174:175] op_sel_hi:[1,0,1]
	v_readlane_b32 s14, v1, 32
	v_cvt_pk_f32_fp8_e32 v[184:185], v36
	v_cvt_pk_f32_fp8_sdwa v[186:187], v36 src0_sel:WORD_1
	v_pk_fma_f32 v[160:161], v[184:185], s[14:15], v[160:161] op_sel_hi:[1,0,1]
	v_pk_fma_f32 v[162:163], v[186:187], s[14:15], v[162:163] op_sel_hi:[1,0,1]
	v_cvt_pk_f32_fp8_e32 v[188:189], v37
	v_cvt_pk_f32_fp8_sdwa v[190:191], v37 src0_sel:WORD_1
	v_pk_fma_f32 v[164:165], v[188:189], s[14:15], v[164:165] op_sel_hi:[1,0,1]
	v_pk_fma_f32 v[166:167], v[190:191], s[14:15], v[166:167] op_sel_hi:[1,0,1]
	v_cvt_pk_f32_fp8_e32 v[184:185], v38
	v_cvt_pk_f32_fp8_sdwa v[186:187], v38 src0_sel:WORD_1
	v_pk_fma_f32 v[168:169], v[184:185], s[14:15], v[168:169] op_sel_hi:[1,0,1]
	v_pk_fma_f32 v[170:171], v[186:187], s[14:15], v[170:171] op_sel_hi:[1,0,1]
	v_cvt_pk_f32_fp8_e32 v[188:189], v39
	v_cvt_pk_f32_fp8_sdwa v[190:191], v39 src0_sel:WORD_1
	v_pk_fma_f32 v[172:173], v[188:189], s[14:15], v[172:173] op_sel_hi:[1,0,1]
	v_pk_fma_f32 v[174:175], v[190:191], s[14:15], v[174:175] op_sel_hi:[1,0,1]
	v_readlane_b32 s14, v1, 40
	v_cvt_pk_f32_fp8_e32 v[184:185], v28
	v_cvt_pk_f32_fp8_sdwa v[186:187], v28 src0_sel:WORD_1
	v_pk_fma_f32 v[160:161], v[184:185], s[14:15], v[160:161] op_sel_hi:[1,0,1]
	v_pk_fma_f32 v[162:163], v[186:187], s[14:15], v[162:163] op_sel_hi:[1,0,1]
	v_cvt_pk_f32_fp8_e32 v[188:189], v29
	v_cvt_pk_f32_fp8_sdwa v[190:191], v29 src0_sel:WORD_1
	v_pk_fma_f32 v[164:165], v[188:189], s[14:15], v[164:165] op_sel_hi:[1,0,1]
	v_pk_fma_f32 v[166:167], v[190:191], s[14:15], v[166:167] op_sel_hi:[1,0,1]
	v_cvt_pk_f32_fp8_e32 v[184:185], v30
	v_cvt_pk_f32_fp8_sdwa v[186:187], v30 src0_sel:WORD_1
	v_pk_fma_f32 v[168:169], v[184:185], s[14:15], v[168:169] op_sel_hi:[1,0,1]
	v_pk_fma_f32 v[170:171], v[186:187], s[14:15], v[170:171] op_sel_hi:[1,0,1]
	v_cvt_pk_f32_fp8_e32 v[188:189], v31
	v_cvt_pk_f32_fp8_sdwa v[190:191], v31 src0_sel:WORD_1
	v_pk_fma_f32 v[172:173], v[188:189], s[14:15], v[172:173] op_sel_hi:[1,0,1]
	v_pk_fma_f32 v[174:175], v[190:191], s[14:15], v[174:175] op_sel_hi:[1,0,1]
	v_readlane_b32 s14, v1, 48
	v_cvt_pk_f32_fp8_e32 v[184:185], v24
	v_cvt_pk_f32_fp8_sdwa v[186:187], v24 src0_sel:WORD_1
	v_pk_fma_f32 v[160:161], v[184:185], s[14:15], v[160:161] op_sel_hi:[1,0,1]
	v_pk_fma_f32 v[162:163], v[186:187], s[14:15], v[162:163] op_sel_hi:[1,0,1]
	v_cvt_pk_f32_fp8_e32 v[188:189], v25
	v_cvt_pk_f32_fp8_sdwa v[190:191], v25 src0_sel:WORD_1
	v_pk_fma_f32 v[164:165], v[188:189], s[14:15], v[164:165] op_sel_hi:[1,0,1]
	v_pk_fma_f32 v[166:167], v[190:191], s[14:15], v[166:167] op_sel_hi:[1,0,1]
	v_cvt_pk_f32_fp8_e32 v[184:185], v26
	v_cvt_pk_f32_fp8_sdwa v[186:187], v26 src0_sel:WORD_1
	v_pk_fma_f32 v[168:169], v[184:185], s[14:15], v[168:169] op_sel_hi:[1,0,1]
	v_pk_fma_f32 v[170:171], v[186:187], s[14:15], v[170:171] op_sel_hi:[1,0,1]
	v_cvt_pk_f32_fp8_e32 v[188:189], v27
	v_cvt_pk_f32_fp8_sdwa v[190:191], v27 src0_sel:WORD_1
	v_pk_fma_f32 v[172:173], v[188:189], s[14:15], v[172:173] op_sel_hi:[1,0,1]
	v_pk_fma_f32 v[174:175], v[190:191], s[14:15], v[174:175] op_sel_hi:[1,0,1]
	v_readlane_b32 s14, v1, 56
	v_cvt_pk_f32_fp8_e32 v[184:185], v20
	v_cvt_pk_f32_fp8_sdwa v[186:187], v20 src0_sel:WORD_1
	v_pk_fma_f32 v[160:161], v[184:185], s[14:15], v[160:161] op_sel_hi:[1,0,1]
	v_pk_fma_f32 v[162:163], v[186:187], s[14:15], v[162:163] op_sel_hi:[1,0,1]
	v_cvt_pk_f32_fp8_e32 v[188:189], v21
	v_cvt_pk_f32_fp8_sdwa v[190:191], v21 src0_sel:WORD_1
	v_pk_fma_f32 v[164:165], v[188:189], s[14:15], v[164:165] op_sel_hi:[1,0,1]
	v_pk_fma_f32 v[166:167], v[190:191], s[14:15], v[166:167] op_sel_hi:[1,0,1]
	v_cvt_pk_f32_fp8_e32 v[184:185], v22
	v_cvt_pk_f32_fp8_sdwa v[186:187], v22 src0_sel:WORD_1
	v_pk_fma_f32 v[168:169], v[184:185], s[14:15], v[168:169] op_sel_hi:[1,0,1]
	v_pk_fma_f32 v[170:171], v[186:187], s[14:15], v[170:171] op_sel_hi:[1,0,1]
	v_cvt_pk_f32_fp8_e32 v[188:189], v23
	v_cvt_pk_f32_fp8_sdwa v[190:191], v23 src0_sel:WORD_1
	v_pk_fma_f32 v[172:173], v[188:189], s[14:15], v[172:173] op_sel_hi:[1,0,1]
	v_pk_fma_f32 v[174:175], v[190:191], s[14:15], v[174:175] op_sel_hi:[1,0,1]
	s_branch .Lp6c1_axdone
.Lp6c1_t6:
	v_readlane_b32 s14, v1, 0
	v_cvt_pk_f32_fp8_e32 v[184:185], v72
	v_cvt_pk_f32_fp8_sdwa v[186:187], v72 src0_sel:WORD_1
	v_pk_fma_f32 v[224:225], v[184:185], s[14:15], v[224:225] op_sel_hi:[1,0,1]
	v_pk_fma_f32 v[226:227], v[186:187], s[14:15], v[226:227] op_sel_hi:[1,0,1]
	v_cvt_pk_f32_fp8_e32 v[188:189], v73
	v_cvt_pk_f32_fp8_sdwa v[190:191], v73 src0_sel:WORD_1
	v_pk_fma_f32 v[228:229], v[188:189], s[14:15], v[228:229] op_sel_hi:[1,0,1]
	v_pk_fma_f32 v[230:231], v[190:191], s[14:15], v[230:231] op_sel_hi:[1,0,1]
	v_cvt_pk_f32_fp8_e32 v[184:185], v74
	v_cvt_pk_f32_fp8_sdwa v[186:187], v74 src0_sel:WORD_1
	v_pk_fma_f32 v[232:233], v[184:185], s[14:15], v[232:233] op_sel_hi:[1,0,1]
	v_pk_fma_f32 v[234:235], v[186:187], s[14:15], v[234:235] op_sel_hi:[1,0,1]
	v_cvt_pk_f32_fp8_e32 v[188:189], v75
	v_cvt_pk_f32_fp8_sdwa v[190:191], v75 src0_sel:WORD_1
	v_pk_fma_f32 v[236:237], v[188:189], s[14:15], v[236:237] op_sel_hi:[1,0,1]
	v_pk_fma_f32 v[238:239], v[190:191], s[14:15], v[238:239] op_sel_hi:[1,0,1]
	v_readlane_b32 s14, v1, 8
	v_cvt_pk_f32_fp8_e32 v[184:185], v52
	v_cvt_pk_f32_fp8_sdwa v[186:187], v52 src0_sel:WORD_1
	v_pk_fma_f32 v[224:225], v[184:185], s[14:15], v[224:225] op_sel_hi:[1,0,1]
	v_pk_fma_f32 v[226:227], v[186:187], s[14:15], v[226:227] op_sel_hi:[1,0,1]
	v_cvt_pk_f32_fp8_e32 v[188:189], v53
	v_cvt_pk_f32_fp8_sdwa v[190:191], v53 src0_sel:WORD_1
	v_pk_fma_f32 v[228:229], v[188:189], s[14:15], v[228:229] op_sel_hi:[1,0,1]
	v_pk_fma_f32 v[230:231], v[190:191], s[14:15], v[230:231] op_sel_hi:[1,0,1]
	v_cvt_pk_f32_fp8_e32 v[184:185], v54
	v_cvt_pk_f32_fp8_sdwa v[186:187], v54 src0_sel:WORD_1
	v_pk_fma_f32 v[232:233], v[184:185], s[14:15], v[232:233] op_sel_hi:[1,0,1]
	v_pk_fma_f32 v[234:235], v[186:187], s[14:15], v[234:235] op_sel_hi:[1,0,1]
	v_cvt_pk_f32_fp8_e32 v[188:189], v55
	v_cvt_pk_f32_fp8_sdwa v[190:191], v55 src0_sel:WORD_1
	v_pk_fma_f32 v[236:237], v[188:189], s[14:15], v[236:237] op_sel_hi:[1,0,1]
	v_pk_fma_f32 v[238:239], v[190:191], s[14:15], v[238:239] op_sel_hi:[1,0,1]
	v_readlane_b32 s14, v1, 16
	v_cvt_pk_f32_fp8_e32 v[184:185], v44
	v_cvt_pk_f32_fp8_sdwa v[186:187], v44 src0_sel:WORD_1
	v_pk_fma_f32 v[224:225], v[184:185], s[14:15], v[224:225] op_sel_hi:[1,0,1]
	v_pk_fma_f32 v[226:227], v[186:187], s[14:15], v[226:227] op_sel_hi:[1,0,1]
	v_cvt_pk_f32_fp8_e32 v[188:189], v45
	v_cvt_pk_f32_fp8_sdwa v[190:191], v45 src0_sel:WORD_1
	v_pk_fma_f32 v[228:229], v[188:189], s[14:15], v[228:229] op_sel_hi:[1,0,1]
	v_pk_fma_f32 v[230:231], v[190:191], s[14:15], v[230:231] op_sel_hi:[1,0,1]
	v_cvt_pk_f32_fp8_e32 v[184:185], v46
	v_cvt_pk_f32_fp8_sdwa v[186:187], v46 src0_sel:WORD_1
	v_pk_fma_f32 v[232:233], v[184:185], s[14:15], v[232:233] op_sel_hi:[1,0,1]
	v_pk_fma_f32 v[234:235], v[186:187], s[14:15], v[234:235] op_sel_hi:[1,0,1]
	v_cvt_pk_f32_fp8_e32 v[188:189], v47
	v_cvt_pk_f32_fp8_sdwa v[190:191], v47 src0_sel:WORD_1
	v_pk_fma_f32 v[236:237], v[188:189], s[14:15], v[236:237] op_sel_hi:[1,0,1]
	v_pk_fma_f32 v[238:239], v[190:191], s[14:15], v[238:239] op_sel_hi:[1,0,1]
	v_readlane_b32 s14, v1, 24
	v_cvt_pk_f32_fp8_e32 v[184:185], v40
	v_cvt_pk_f32_fp8_sdwa v[186:187], v40 src0_sel:WORD_1
	v_pk_fma_f32 v[224:225], v[184:185], s[14:15], v[224:225] op_sel_hi:[1,0,1]
	v_pk_fma_f32 v[226:227], v[186:187], s[14:15], v[226:227] op_sel_hi:[1,0,1]
	v_cvt_pk_f32_fp8_e32 v[188:189], v41
	v_cvt_pk_f32_fp8_sdwa v[190:191], v41 src0_sel:WORD_1
	v_pk_fma_f32 v[228:229], v[188:189], s[14:15], v[228:229] op_sel_hi:[1,0,1]
	v_pk_fma_f32 v[230:231], v[190:191], s[14:15], v[230:231] op_sel_hi:[1,0,1]
	v_cvt_pk_f32_fp8_e32 v[184:185], v42
	v_cvt_pk_f32_fp8_sdwa v[186:187], v42 src0_sel:WORD_1
	v_pk_fma_f32 v[232:233], v[184:185], s[14:15], v[232:233] op_sel_hi:[1,0,1]
	v_pk_fma_f32 v[234:235], v[186:187], s[14:15], v[234:235] op_sel_hi:[1,0,1]
	v_cvt_pk_f32_fp8_e32 v[188:189], v43
	v_cvt_pk_f32_fp8_sdwa v[190:191], v43 src0_sel:WORD_1
	v_pk_fma_f32 v[236:237], v[188:189], s[14:15], v[236:237] op_sel_hi:[1,0,1]
	v_pk_fma_f32 v[238:239], v[190:191], s[14:15], v[238:239] op_sel_hi:[1,0,1]
	v_readlane_b32 s14, v1, 32
	v_cvt_pk_f32_fp8_e32 v[184:185], v36
	v_cvt_pk_f32_fp8_sdwa v[186:187], v36 src0_sel:WORD_1
	v_pk_fma_f32 v[224:225], v[184:185], s[14:15], v[224:225] op_sel_hi:[1,0,1]
	v_pk_fma_f32 v[226:227], v[186:187], s[14:15], v[226:227] op_sel_hi:[1,0,1]
	v_cvt_pk_f32_fp8_e32 v[188:189], v37
	v_cvt_pk_f32_fp8_sdwa v[190:191], v37 src0_sel:WORD_1
	v_pk_fma_f32 v[228:229], v[188:189], s[14:15], v[228:229] op_sel_hi:[1,0,1]
	v_pk_fma_f32 v[230:231], v[190:191], s[14:15], v[230:231] op_sel_hi:[1,0,1]
	v_cvt_pk_f32_fp8_e32 v[184:185], v38
	v_cvt_pk_f32_fp8_sdwa v[186:187], v38 src0_sel:WORD_1
	v_pk_fma_f32 v[232:233], v[184:185], s[14:15], v[232:233] op_sel_hi:[1,0,1]
	v_pk_fma_f32 v[234:235], v[186:187], s[14:15], v[234:235] op_sel_hi:[1,0,1]
	v_cvt_pk_f32_fp8_e32 v[188:189], v39
	v_cvt_pk_f32_fp8_sdwa v[190:191], v39 src0_sel:WORD_1
	v_pk_fma_f32 v[236:237], v[188:189], s[14:15], v[236:237] op_sel_hi:[1,0,1]
	v_pk_fma_f32 v[238:239], v[190:191], s[14:15], v[238:239] op_sel_hi:[1,0,1]
	v_readlane_b32 s14, v1, 40
	v_cvt_pk_f32_fp8_e32 v[184:185], v28
	v_cvt_pk_f32_fp8_sdwa v[186:187], v28 src0_sel:WORD_1
	v_pk_fma_f32 v[224:225], v[184:185], s[14:15], v[224:225] op_sel_hi:[1,0,1]
	v_pk_fma_f32 v[226:227], v[186:187], s[14:15], v[226:227] op_sel_hi:[1,0,1]
	v_cvt_pk_f32_fp8_e32 v[188:189], v29
	v_cvt_pk_f32_fp8_sdwa v[190:191], v29 src0_sel:WORD_1
	v_pk_fma_f32 v[228:229], v[188:189], s[14:15], v[228:229] op_sel_hi:[1,0,1]
	v_pk_fma_f32 v[230:231], v[190:191], s[14:15], v[230:231] op_sel_hi:[1,0,1]
	v_cvt_pk_f32_fp8_e32 v[184:185], v30
	v_cvt_pk_f32_fp8_sdwa v[186:187], v30 src0_sel:WORD_1
	v_pk_fma_f32 v[232:233], v[184:185], s[14:15], v[232:233] op_sel_hi:[1,0,1]
	v_pk_fma_f32 v[234:235], v[186:187], s[14:15], v[234:235] op_sel_hi:[1,0,1]
	v_cvt_pk_f32_fp8_e32 v[188:189], v31
	v_cvt_pk_f32_fp8_sdwa v[190:191], v31 src0_sel:WORD_1
	v_pk_fma_f32 v[236:237], v[188:189], s[14:15], v[236:237] op_sel_hi:[1,0,1]
	v_pk_fma_f32 v[238:239], v[190:191], s[14:15], v[238:239] op_sel_hi:[1,0,1]
	v_readlane_b32 s14, v1, 48
	v_cvt_pk_f32_fp8_e32 v[184:185], v24
	v_cvt_pk_f32_fp8_sdwa v[186:187], v24 src0_sel:WORD_1
	v_pk_fma_f32 v[224:225], v[184:185], s[14:15], v[224:225] op_sel_hi:[1,0,1]
	v_pk_fma_f32 v[226:227], v[186:187], s[14:15], v[226:227] op_sel_hi:[1,0,1]
	v_cvt_pk_f32_fp8_e32 v[188:189], v25
	v_cvt_pk_f32_fp8_sdwa v[190:191], v25 src0_sel:WORD_1
	v_pk_fma_f32 v[228:229], v[188:189], s[14:15], v[228:229] op_sel_hi:[1,0,1]
	v_pk_fma_f32 v[230:231], v[190:191], s[14:15], v[230:231] op_sel_hi:[1,0,1]
	v_cvt_pk_f32_fp8_e32 v[184:185], v26
	v_cvt_pk_f32_fp8_sdwa v[186:187], v26 src0_sel:WORD_1
	v_pk_fma_f32 v[232:233], v[184:185], s[14:15], v[232:233] op_sel_hi:[1,0,1]
	v_pk_fma_f32 v[234:235], v[186:187], s[14:15], v[234:235] op_sel_hi:[1,0,1]
	v_cvt_pk_f32_fp8_e32 v[188:189], v27
	v_cvt_pk_f32_fp8_sdwa v[190:191], v27 src0_sel:WORD_1
	v_pk_fma_f32 v[236:237], v[188:189], s[14:15], v[236:237] op_sel_hi:[1,0,1]
	v_pk_fma_f32 v[238:239], v[190:191], s[14:15], v[238:239] op_sel_hi:[1,0,1]
	v_readlane_b32 s14, v1, 56
	v_cvt_pk_f32_fp8_e32 v[184:185], v20
	v_cvt_pk_f32_fp8_sdwa v[186:187], v20 src0_sel:WORD_1
	v_pk_fma_f32 v[224:225], v[184:185], s[14:15], v[224:225] op_sel_hi:[1,0,1]
	v_pk_fma_f32 v[226:227], v[186:187], s[14:15], v[226:227] op_sel_hi:[1,0,1]
	v_cvt_pk_f32_fp8_e32 v[188:189], v21
	v_cvt_pk_f32_fp8_sdwa v[190:191], v21 src0_sel:WORD_1
	v_pk_fma_f32 v[228:229], v[188:189], s[14:15], v[228:229] op_sel_hi:[1,0,1]
	v_pk_fma_f32 v[230:231], v[190:191], s[14:15], v[230:231] op_sel_hi:[1,0,1]
	v_cvt_pk_f32_fp8_e32 v[184:185], v22
	v_cvt_pk_f32_fp8_sdwa v[186:187], v22 src0_sel:WORD_1
	v_pk_fma_f32 v[232:233], v[184:185], s[14:15], v[232:233] op_sel_hi:[1,0,1]
	v_pk_fma_f32 v[234:235], v[186:187], s[14:15], v[234:235] op_sel_hi:[1,0,1]
	v_cvt_pk_f32_fp8_e32 v[188:189], v23
	v_cvt_pk_f32_fp8_sdwa v[190:191], v23 src0_sel:WORD_1
	v_pk_fma_f32 v[236:237], v[188:189], s[14:15], v[236:237] op_sel_hi:[1,0,1]
	v_pk_fma_f32 v[238:239], v[190:191], s[14:15], v[238:239] op_sel_hi:[1,0,1]
	s_branch .Lp6c1_axdone
.Lp6c1_t7:
	v_readlane_b32 s14, v1, 0
	v_cvt_pk_f32_fp8_e32 v[184:185], v72
	v_cvt_pk_f32_fp8_sdwa v[186:187], v72 src0_sel:WORD_1
	v_pk_fma_f32 v[240:241], v[184:185], s[14:15], v[240:241] op_sel_hi:[1,0,1]
	v_pk_fma_f32 v[242:243], v[186:187], s[14:15], v[242:243] op_sel_hi:[1,0,1]
	v_cvt_pk_f32_fp8_e32 v[188:189], v73
	v_cvt_pk_f32_fp8_sdwa v[190:191], v73 src0_sel:WORD_1
	v_pk_fma_f32 v[244:245], v[188:189], s[14:15], v[244:245] op_sel_hi:[1,0,1]
	v_pk_fma_f32 v[246:247], v[190:191], s[14:15], v[246:247] op_sel_hi:[1,0,1]
	v_cvt_pk_f32_fp8_e32 v[184:185], v74
	v_cvt_pk_f32_fp8_sdwa v[186:187], v74 src0_sel:WORD_1
	v_pk_fma_f32 v[248:249], v[184:185], s[14:15], v[248:249] op_sel_hi:[1,0,1]
	v_pk_fma_f32 v[250:251], v[186:187], s[14:15], v[250:251] op_sel_hi:[1,0,1]
	v_cvt_pk_f32_fp8_e32 v[188:189], v75
	v_cvt_pk_f32_fp8_sdwa v[190:191], v75 src0_sel:WORD_1
	v_pk_fma_f32 v[216:217], v[188:189], s[14:15], v[216:217] op_sel_hi:[1,0,1]
	v_pk_fma_f32 v[218:219], v[190:191], s[14:15], v[218:219] op_sel_hi:[1,0,1]
	v_readlane_b32 s14, v1, 8
	v_cvt_pk_f32_fp8_e32 v[184:185], v52
	v_cvt_pk_f32_fp8_sdwa v[186:187], v52 src0_sel:WORD_1
	v_pk_fma_f32 v[240:241], v[184:185], s[14:15], v[240:241] op_sel_hi:[1,0,1]
	v_pk_fma_f32 v[242:243], v[186:187], s[14:15], v[242:243] op_sel_hi:[1,0,1]
	v_cvt_pk_f32_fp8_e32 v[188:189], v53
	v_cvt_pk_f32_fp8_sdwa v[190:191], v53 src0_sel:WORD_1
	v_pk_fma_f32 v[244:245], v[188:189], s[14:15], v[244:245] op_sel_hi:[1,0,1]
	v_pk_fma_f32 v[246:247], v[190:191], s[14:15], v[246:247] op_sel_hi:[1,0,1]
	v_cvt_pk_f32_fp8_e32 v[184:185], v54
	v_cvt_pk_f32_fp8_sdwa v[186:187], v54 src0_sel:WORD_1
	v_pk_fma_f32 v[248:249], v[184:185], s[14:15], v[248:249] op_sel_hi:[1,0,1]
	v_pk_fma_f32 v[250:251], v[186:187], s[14:15], v[250:251] op_sel_hi:[1,0,1]
	v_cvt_pk_f32_fp8_e32 v[188:189], v55
	v_cvt_pk_f32_fp8_sdwa v[190:191], v55 src0_sel:WORD_1
	v_pk_fma_f32 v[216:217], v[188:189], s[14:15], v[216:217] op_sel_hi:[1,0,1]
	v_pk_fma_f32 v[218:219], v[190:191], s[14:15], v[218:219] op_sel_hi:[1,0,1]
	v_readlane_b32 s14, v1, 16
	v_cvt_pk_f32_fp8_e32 v[184:185], v44
	v_cvt_pk_f32_fp8_sdwa v[186:187], v44 src0_sel:WORD_1
	v_pk_fma_f32 v[240:241], v[184:185], s[14:15], v[240:241] op_sel_hi:[1,0,1]
	v_pk_fma_f32 v[242:243], v[186:187], s[14:15], v[242:243] op_sel_hi:[1,0,1]
	v_cvt_pk_f32_fp8_e32 v[188:189], v45
	v_cvt_pk_f32_fp8_sdwa v[190:191], v45 src0_sel:WORD_1
	v_pk_fma_f32 v[244:245], v[188:189], s[14:15], v[244:245] op_sel_hi:[1,0,1]
	v_pk_fma_f32 v[246:247], v[190:191], s[14:15], v[246:247] op_sel_hi:[1,0,1]
	v_cvt_pk_f32_fp8_e32 v[184:185], v46
	v_cvt_pk_f32_fp8_sdwa v[186:187], v46 src0_sel:WORD_1
	v_pk_fma_f32 v[248:249], v[184:185], s[14:15], v[248:249] op_sel_hi:[1,0,1]
	v_pk_fma_f32 v[250:251], v[186:187], s[14:15], v[250:251] op_sel_hi:[1,0,1]
	v_cvt_pk_f32_fp8_e32 v[188:189], v47
	v_cvt_pk_f32_fp8_sdwa v[190:191], v47 src0_sel:WORD_1
	v_pk_fma_f32 v[216:217], v[188:189], s[14:15], v[216:217] op_sel_hi:[1,0,1]
	v_pk_fma_f32 v[218:219], v[190:191], s[14:15], v[218:219] op_sel_hi:[1,0,1]
	v_readlane_b32 s14, v1, 24
	v_cvt_pk_f32_fp8_e32 v[184:185], v40
	v_cvt_pk_f32_fp8_sdwa v[186:187], v40 src0_sel:WORD_1
	v_pk_fma_f32 v[240:241], v[184:185], s[14:15], v[240:241] op_sel_hi:[1,0,1]
	v_pk_fma_f32 v[242:243], v[186:187], s[14:15], v[242:243] op_sel_hi:[1,0,1]
	v_cvt_pk_f32_fp8_e32 v[188:189], v41
	v_cvt_pk_f32_fp8_sdwa v[190:191], v41 src0_sel:WORD_1
	v_pk_fma_f32 v[244:245], v[188:189], s[14:15], v[244:245] op_sel_hi:[1,0,1]
	v_pk_fma_f32 v[246:247], v[190:191], s[14:15], v[246:247] op_sel_hi:[1,0,1]
	v_cvt_pk_f32_fp8_e32 v[184:185], v42
	v_cvt_pk_f32_fp8_sdwa v[186:187], v42 src0_sel:WORD_1
	v_pk_fma_f32 v[248:249], v[184:185], s[14:15], v[248:249] op_sel_hi:[1,0,1]
	v_pk_fma_f32 v[250:251], v[186:187], s[14:15], v[250:251] op_sel_hi:[1,0,1]
	v_cvt_pk_f32_fp8_e32 v[188:189], v43
	v_cvt_pk_f32_fp8_sdwa v[190:191], v43 src0_sel:WORD_1
	v_pk_fma_f32 v[216:217], v[188:189], s[14:15], v[216:217] op_sel_hi:[1,0,1]
	v_pk_fma_f32 v[218:219], v[190:191], s[14:15], v[218:219] op_sel_hi:[1,0,1]
	v_readlane_b32 s14, v1, 32
	v_cvt_pk_f32_fp8_e32 v[184:185], v36
	v_cvt_pk_f32_fp8_sdwa v[186:187], v36 src0_sel:WORD_1
	v_pk_fma_f32 v[240:241], v[184:185], s[14:15], v[240:241] op_sel_hi:[1,0,1]
	v_pk_fma_f32 v[242:243], v[186:187], s[14:15], v[242:243] op_sel_hi:[1,0,1]
	v_cvt_pk_f32_fp8_e32 v[188:189], v37
	v_cvt_pk_f32_fp8_sdwa v[190:191], v37 src0_sel:WORD_1
	v_pk_fma_f32 v[244:245], v[188:189], s[14:15], v[244:245] op_sel_hi:[1,0,1]
	v_pk_fma_f32 v[246:247], v[190:191], s[14:15], v[246:247] op_sel_hi:[1,0,1]
	v_cvt_pk_f32_fp8_e32 v[184:185], v38
	v_cvt_pk_f32_fp8_sdwa v[186:187], v38 src0_sel:WORD_1
	v_pk_fma_f32 v[248:249], v[184:185], s[14:15], v[248:249] op_sel_hi:[1,0,1]
	v_pk_fma_f32 v[250:251], v[186:187], s[14:15], v[250:251] op_sel_hi:[1,0,1]
	v_cvt_pk_f32_fp8_e32 v[188:189], v39
	v_cvt_pk_f32_fp8_sdwa v[190:191], v39 src0_sel:WORD_1
	v_pk_fma_f32 v[216:217], v[188:189], s[14:15], v[216:217] op_sel_hi:[1,0,1]
	v_pk_fma_f32 v[218:219], v[190:191], s[14:15], v[218:219] op_sel_hi:[1,0,1]
	v_readlane_b32 s14, v1, 40
	v_cvt_pk_f32_fp8_e32 v[184:185], v28
	v_cvt_pk_f32_fp8_sdwa v[186:187], v28 src0_sel:WORD_1
	v_pk_fma_f32 v[240:241], v[184:185], s[14:15], v[240:241] op_sel_hi:[1,0,1]
	v_pk_fma_f32 v[242:243], v[186:187], s[14:15], v[242:243] op_sel_hi:[1,0,1]
	v_cvt_pk_f32_fp8_e32 v[188:189], v29
	v_cvt_pk_f32_fp8_sdwa v[190:191], v29 src0_sel:WORD_1
	v_pk_fma_f32 v[244:245], v[188:189], s[14:15], v[244:245] op_sel_hi:[1,0,1]
	v_pk_fma_f32 v[246:247], v[190:191], s[14:15], v[246:247] op_sel_hi:[1,0,1]
	v_cvt_pk_f32_fp8_e32 v[184:185], v30
	v_cvt_pk_f32_fp8_sdwa v[186:187], v30 src0_sel:WORD_1
	v_pk_fma_f32 v[248:249], v[184:185], s[14:15], v[248:249] op_sel_hi:[1,0,1]
	v_pk_fma_f32 v[250:251], v[186:187], s[14:15], v[250:251] op_sel_hi:[1,0,1]
	v_cvt_pk_f32_fp8_e32 v[188:189], v31
	v_cvt_pk_f32_fp8_sdwa v[190:191], v31 src0_sel:WORD_1
	v_pk_fma_f32 v[216:217], v[188:189], s[14:15], v[216:217] op_sel_hi:[1,0,1]
	v_pk_fma_f32 v[218:219], v[190:191], s[14:15], v[218:219] op_sel_hi:[1,0,1]
	v_readlane_b32 s14, v1, 48
	v_cvt_pk_f32_fp8_e32 v[184:185], v24
	v_cvt_pk_f32_fp8_sdwa v[186:187], v24 src0_sel:WORD_1
	v_pk_fma_f32 v[240:241], v[184:185], s[14:15], v[240:241] op_sel_hi:[1,0,1]
	v_pk_fma_f32 v[242:243], v[186:187], s[14:15], v[242:243] op_sel_hi:[1,0,1]
	v_cvt_pk_f32_fp8_e32 v[188:189], v25
	v_cvt_pk_f32_fp8_sdwa v[190:191], v25 src0_sel:WORD_1
	v_pk_fma_f32 v[244:245], v[188:189], s[14:15], v[244:245] op_sel_hi:[1,0,1]
	v_pk_fma_f32 v[246:247], v[190:191], s[14:15], v[246:247] op_sel_hi:[1,0,1]
	v_cvt_pk_f32_fp8_e32 v[184:185], v26
	v_cvt_pk_f32_fp8_sdwa v[186:187], v26 src0_sel:WORD_1
	v_pk_fma_f32 v[248:249], v[184:185], s[14:15], v[248:249] op_sel_hi:[1,0,1]
	v_pk_fma_f32 v[250:251], v[186:187], s[14:15], v[250:251] op_sel_hi:[1,0,1]
	v_cvt_pk_f32_fp8_e32 v[188:189], v27
	v_cvt_pk_f32_fp8_sdwa v[190:191], v27 src0_sel:WORD_1
	v_pk_fma_f32 v[216:217], v[188:189], s[14:15], v[216:217] op_sel_hi:[1,0,1]
	v_pk_fma_f32 v[218:219], v[190:191], s[14:15], v[218:219] op_sel_hi:[1,0,1]
	v_readlane_b32 s14, v1, 56
	v_cvt_pk_f32_fp8_e32 v[184:185], v20
	v_cvt_pk_f32_fp8_sdwa v[186:187], v20 src0_sel:WORD_1
	v_pk_fma_f32 v[240:241], v[184:185], s[14:15], v[240:241] op_sel_hi:[1,0,1]
	v_pk_fma_f32 v[242:243], v[186:187], s[14:15], v[242:243] op_sel_hi:[1,0,1]
	v_cvt_pk_f32_fp8_e32 v[188:189], v21
	v_cvt_pk_f32_fp8_sdwa v[190:191], v21 src0_sel:WORD_1
	v_pk_fma_f32 v[244:245], v[188:189], s[14:15], v[244:245] op_sel_hi:[1,0,1]
	v_pk_fma_f32 v[246:247], v[190:191], s[14:15], v[246:247] op_sel_hi:[1,0,1]
	v_cvt_pk_f32_fp8_e32 v[184:185], v22
	v_cvt_pk_f32_fp8_sdwa v[186:187], v22 src0_sel:WORD_1
	v_pk_fma_f32 v[248:249], v[184:185], s[14:15], v[248:249] op_sel_hi:[1,0,1]
	v_pk_fma_f32 v[250:251], v[186:187], s[14:15], v[250:251] op_sel_hi:[1,0,1]
	v_cvt_pk_f32_fp8_e32 v[188:189], v23
	v_cvt_pk_f32_fp8_sdwa v[190:191], v23 src0_sel:WORD_1
	v_pk_fma_f32 v[216:217], v[188:189], s[14:15], v[216:217] op_sel_hi:[1,0,1]
	v_pk_fma_f32 v[218:219], v[190:191], s[14:15], v[218:219] op_sel_hi:[1,0,1]
	s_branch .Lp6c1_axdone
